# on top of v12: setprio raised before the pre-MMA barrier and lowered after the post-MMA barrier (one fewer issue slot on each side of the MFMA section)
# baseline (speedup 1.0000x reference)
; #define PG8_STAGE(bufoff, gbase, voff) do { _Pragma("unroll") for (int _i = 0; _i < 2; ++_i) { unsigned keep_; \
;         asm volatile("s_mov_b32 %0, m0\n\ts_mov_b32 m0, %3\n\ts_nop 0\n\tglobal_load_lds_dwordx4 %1, %2\n\ts_mov_b32 m0, %0" : "=&s"(keep_) : "v"((voff)[_i]), "s"((const char*)(gbase)), "s"(ldsbase + (unsigned)((bufoff) + _i * 8192)) : "memory"); } } while (0)
; #define PG8_WAIT_V(n) asm volatile("s_waitcnt vmcnt(" #n ")" ::: "memory")
; #define PG8_WAIT_L(n) asm volatile("s_waitcnt lgkmcnt(" #n ")" ::: "memory")
; #define PG8_BAR __builtin_amdgcn_s_barrier()
; #define PG8_SCHED __builtin_amdgcn_sched_barrier(0)
;     DI int nt(const Unit& u) const { return (u.aux & 8) ? PLED / 64 : ((u.aux & 4) ? (D_ / 2) / 64 : D_ / 64); }
; template <class Epi, class Sched, bool ALIGN_EPI, bool FP8 = false>
; DI void gemm_phase(LAS unsigned char* lds, const Gemm g, const Sched& S, const Epi& E) {
;     ...
;         for (int t = 0; t < nt; t += 2) {
;             if constexpr (Epi::MID) { if (t == (nt >> 1)) E.mid(acc, cur, wr, wc, fr, fq); }
;             const bool last = (t == nt - 2);
;             const char* a1 = cA + (size_t)(t + 1) * kstep;
;             const char* a2 = last ? nA : cA + (size_t)(t + 2) * kstep; const char* b2 = last ? nB : cB + (size_t)(t + 2) * kstep;
;             const char* a3 = a2 + kstep; const char* b3 = b2 + kstep;
;             PG8_LDB(B0, 0, 0); PG8_LDB(B1, 0, 1); PG8_SCHED; PG8_LDA(At, 0, 0); PG8_STAGE(PG8_SA(1, 1), a1 + hstepA, voffA);
;             PG8_WAIT_V(8); PG8_WAIT_L(0); PG8_BAR; PG8_MMA(0, 0, At, B0); PG8_MMA(0, 1, At, B1); PG8_BAR; PG8_SCHED;
;             PG8_LDA(At, 0, 1); PG8_STAGE(PG8_SB(0, 0), b2, voffB); PG8_STAGE(PG8_SB(0, 1), b2 + hstepB, voffB); PG8_STAGE(PG8_SA(0, 0), a2, voffA);
;             PG8_WAIT_V(8); PG8_WAIT_L(0); PG8_BAR; PG8_MMA(1, 0, At, B0); PG8_MMA(1, 1, At, B1); PG8_BAR; PG8_SCHED;
.LBB0_255:
	s_add_i32 s53, s51, 2
	s_add_u32 s42, s18, s56
	s_addc_u32 s43, s19, s57
	s_add_u32 s58, s42, 0x100
	v_add_u32_e32 v130, 0x10000, v157
	s_addc_u32 s59, s43, 0
	ds_read_b128 v[146:149], v130
	ds_read_b128 v[150:153], v130 offset:1024
	ds_read_b128 v[160:163], v130 offset:2048
	ds_read_b128 v[164:167], v130 offset:3072
	v_add_u32_e32 v130, 0x14000, v157
	s_add_u32 s60, s22, s56
	ds_read_b128 v[168:171], v130
	ds_read_b128 v[172:175], v130 offset:1024
	ds_read_b128 v[176:179], v130 offset:2048
	ds_read_b128 v[180:183], v130 offset:3072
	s_addc_u32 s61, s23, s57
	s_add_u32 s60, s60, 0x100
	s_addc_u32 s61, s61, 0
	s_cmp_eq_u32 s20, s51
	s_cselect_b32 s62, s8, s58
	s_cselect_b32 s63, s9, s59
	s_cselect_b32 s60, s54, s60
	s_cselect_b32 s61, s55, s61
	s_add_u32 s58, s62, 0x80
	s_addc_u32 s59, s63, 0
	ds_read_b128 v[184:187], v158
	ds_read_b128 v[188:191], v158 offset:1024
	ds_read_b128 v[192:195], v158 offset:2048
	ds_read_b128 v[196:199], v158 offset:3072
	ds_read_b128 v[200:203], v158 offset:4096
	ds_read_b128 v[204:207], v158 offset:5120
	ds_read_b128 v[208:211], v158 offset:6144
	ds_read_b128 v[212:215], v158 offset:7168
	s_add_u32 s42, s42, 0x80080
	s_addc_u32 s43, s43, 0
	s_mov_b32 s51, m0
	s_mov_b32 m0, s89
	s_nop 0
	global_load_lds_dwordx4 v129, s[42:43]
	s_mov_b32 m0, s51
	s_nop 0
	s_mov_b32 s51, m0
	s_mov_b32 m0, s90
	s_nop 0
	global_load_lds_dwordx4 v154, s[42:43]
	s_mov_b32 m0, s51
	s_waitcnt vmcnt(8)
	s_waitcnt lgkmcnt(0)
	s_setprio 1
	s_barrier
	v_mfma_f32_16x16x32_bf16 v[124:127], v[146:149], v[184:187], v[124:127]
	v_mfma_f32_16x16x32_bf16 v[120:123], v[160:163], v[184:187], v[120:123]
	v_mfma_f32_16x16x32_bf16 v[116:119], v[146:149], v[192:195], v[116:119]
	v_mfma_f32_16x16x32_bf16 v[112:115], v[160:163], v[192:195], v[112:115]
	v_mfma_f32_16x16x32_bf16 v[108:111], v[146:149], v[200:203], v[108:111]
	v_mfma_f32_16x16x32_bf16 v[104:107], v[160:163], v[200:203], v[104:107]
	v_mfma_f32_16x16x32_bf16 v[100:103], v[146:149], v[208:211], v[100:103]
	v_mfma_f32_16x16x32_bf16 v[96:99], v[160:163], v[208:211], v[96:99]
	v_mfma_f32_16x16x32_bf16 v[124:127], v[150:153], v[188:191], v[124:127]
	v_mfma_f32_16x16x32_bf16 v[120:123], v[164:167], v[188:191], v[120:123]
	v_mfma_f32_16x16x32_bf16 v[116:119], v[150:153], v[196:199], v[116:119]
	v_mfma_f32_16x16x32_bf16 v[112:115], v[164:167], v[196:199], v[112:115]
	v_mfma_f32_16x16x32_bf16 v[108:111], v[150:153], v[204:207], v[108:111]
	v_mfma_f32_16x16x32_bf16 v[104:107], v[164:167], v[204:207], v[104:107]
	v_mfma_f32_16x16x32_bf16 v[100:103], v[150:153], v[212:215], v[100:103]
	v_mfma_f32_16x16x32_bf16 v[96:99], v[164:167], v[212:215], v[96:99]
	v_mfma_f32_16x16x32_bf16 v[92:95], v[168:171], v[184:187], v[92:95]
	v_mfma_f32_16x16x32_bf16 v[88:91], v[176:179], v[184:187], v[88:91]
	v_mfma_f32_16x16x32_bf16 v[84:87], v[168:171], v[192:195], v[84:87]
	v_mfma_f32_16x16x32_bf16 v[80:83], v[176:179], v[192:195], v[80:83]
	v_mfma_f32_16x16x32_bf16 v[76:79], v[168:171], v[200:203], v[76:79]
	v_mfma_f32_16x16x32_bf16 v[72:75], v[176:179], v[200:203], v[72:75]
	v_mfma_f32_16x16x32_bf16 v[68:71], v[168:171], v[208:211], v[68:71]
	v_mfma_f32_16x16x32_bf16 v[64:67], v[176:179], v[208:211], v[64:67]
	v_mfma_f32_16x16x32_bf16 v[92:95], v[172:175], v[188:191], v[92:95]
	v_mfma_f32_16x16x32_bf16 v[88:91], v[180:183], v[188:191], v[88:91]
	v_mfma_f32_16x16x32_bf16 v[84:87], v[172:175], v[196:199], v[84:87]
	v_mfma_f32_16x16x32_bf16 v[80:83], v[180:183], v[196:199], v[80:83]
	v_mfma_f32_16x16x32_bf16 v[76:79], v[172:175], v[204:207], v[76:79]
	v_mfma_f32_16x16x32_bf16 v[72:75], v[180:183], v[204:207], v[72:75]
	v_mfma_f32_16x16x32_bf16 v[68:71], v[172:175], v[212:215], v[68:71]
	v_mfma_f32_16x16x32_bf16 v[64:67], v[180:183], v[212:215], v[64:67]
	s_barrier
	s_setprio 0
	ds_read_b128 v[184:187], v158 offset:16384
	ds_read_b128 v[188:191], v158 offset:17408
	ds_read_b128 v[192:195], v158 offset:18432
	ds_read_b128 v[196:199], v158 offset:19456
	ds_read_b128 v[200:203], v158 offset:20480
	ds_read_b128 v[204:207], v158 offset:21504
	ds_read_b128 v[208:211], v158 offset:22528
	ds_read_b128 v[212:215], v158 offset:23552
	s_mov_b32 s42, m0
	s_mov_b32 m0, s17
	s_nop 0
	global_load_lds_dwordx4 v145, s[60:61]
	s_mov_b32 m0, s42
	s_nop 0
	s_mov_b32 s42, m0
	s_mov_b32 m0, s68
	s_nop 0
	global_load_lds_dwordx4 v155, s[60:61]
	s_mov_b32 m0, s42
	s_add_u32 s42, s60, 0x80000
	s_addc_u32 s43, s61, 0
	s_mov_b32 s51, m0
	s_mov_b32 m0, s69
	s_nop 0
	global_load_lds_dwordx4 v145, s[42:43]
	s_mov_b32 m0, s51
	s_nop 0
	s_mov_b32 s51, m0
	s_mov_b32 m0, s70
	s_nop 0
	global_load_lds_dwordx4 v155, s[42:43]
	s_mov_b32 m0, s51
	s_mov_b32 s42, m0
	s_mov_b32 m0, s15
	s_nop 0
	global_load_lds_dwordx4 v129, s[62:63]
	s_mov_b32 m0, s42
	s_nop 0
	s_mov_b32 s42, m0
	s_mov_b32 m0, s71
	s_nop 0
	global_load_lds_dwordx4 v154, s[62:63]
	s_mov_b32 m0, s42
	s_waitcnt vmcnt(8)
	s_waitcnt lgkmcnt(0)
	s_setprio 1
	s_barrier
; #define PG8_STAGE(bufoff, gbase, voff) do { _Pragma("unroll") for (int _i = 0; _i < 2; ++_i) { unsigned keep_; \
;         asm volatile("s_mov_b32 %0, m0\n\ts_mov_b32 m0, %3\n\ts_nop 0\n\tglobal_load_lds_dwordx4 %1, %2\n\ts_mov_b32 m0, %0" : "=&s"(keep_) : "v"((voff)[_i]), "s"((const char*)(gbase)), "s"(ldsbase + (unsigned)((bufoff) + _i * 8192)) : "memory"); } } while (0)
; #define PG8_WAIT_V(n) asm volatile("s_waitcnt vmcnt(" #n ")" ::: "memory")
; #define PG8_WAIT_L(n) asm volatile("s_waitcnt lgkmcnt(" #n ")" ::: "memory")
; #define PG8_BAR __builtin_amdgcn_s_barrier()
; #define PG8_SCHED __builtin_amdgcn_sched_barrier(0)
; template <class Epi, class Sched, bool ALIGN_EPI, bool FP8 = false>
; DI void gemm_phase(LAS unsigned char* lds, const Gemm g, const Sched& S, const Epi& E) {
;     ...
;             PG8_WAIT_V(8); PG8_WAIT_L(0); PG8_BAR; PG8_MMA(1, 0, At, B0); PG8_MMA(1, 1, At, B1); PG8_BAR; PG8_SCHED;
;             PG8_LDB(B0, 1, 0); PG8_LDB(B1, 1, 1); PG8_SCHED; PG8_LDA(At, 1, 0); PG8_STAGE(PG8_SA(0, 1), a2 + hstepA, voffA);
;             PG8_WAIT_V(8); PG8_WAIT_L(0); PG8_BAR; PG8_MMA(0, 0, At, B0); PG8_MMA(0, 1, At, B1); PG8_BAR; PG8_SCHED;
;             PG8_LDA(At, 1, 1); PG8_STAGE(PG8_SB(1, 0), b3, voffB); PG8_STAGE(PG8_SB(1, 1), b3 + hstepB, voffB); PG8_STAGE(PG8_SA(1, 0), a3, voffA);
;             PG8_WAIT_V(8); PG8_WAIT_L(0); PG8_BAR; PG8_MMA(1, 0, At, B0); PG8_MMA(1, 1, At, B1); PG8_BAR; PG8_SCHED;
	v_mfma_f32_16x16x32_bf16 v[60:63], v[146:149], v[184:187], v[60:63]
	v_mfma_f32_16x16x32_bf16 v[56:59], v[160:163], v[184:187], v[56:59]
	v_mfma_f32_16x16x32_bf16 v[52:55], v[146:149], v[192:195], v[52:55]
	v_mfma_f32_16x16x32_bf16 v[48:51], v[160:163], v[192:195], v[48:51]
	v_mfma_f32_16x16x32_bf16 v[44:47], v[146:149], v[200:203], v[44:47]
	v_mfma_f32_16x16x32_bf16 v[40:43], v[160:163], v[200:203], v[40:43]
	v_mfma_f32_16x16x32_bf16 v[36:39], v[146:149], v[208:211], v[36:39]
	v_mfma_f32_16x16x32_bf16 v[32:35], v[160:163], v[208:211], v[32:35]
	v_mfma_f32_16x16x32_bf16 v[60:63], v[150:153], v[188:191], v[60:63]
	v_mfma_f32_16x16x32_bf16 v[56:59], v[164:167], v[188:191], v[56:59]
	v_mfma_f32_16x16x32_bf16 v[52:55], v[150:153], v[196:199], v[52:55]
	v_mfma_f32_16x16x32_bf16 v[48:51], v[164:167], v[196:199], v[48:51]
	v_mfma_f32_16x16x32_bf16 v[44:47], v[150:153], v[204:207], v[44:47]
	v_mfma_f32_16x16x32_bf16 v[40:43], v[164:167], v[204:207], v[40:43]
	v_mfma_f32_16x16x32_bf16 v[36:39], v[150:153], v[212:215], v[36:39]
	v_mfma_f32_16x16x32_bf16 v[32:35], v[164:167], v[212:215], v[32:35]
	v_mfma_f32_16x16x32_bf16 v[28:31], v[168:171], v[184:187], v[28:31]
	v_mfma_f32_16x16x32_bf16 v[24:27], v[176:179], v[184:187], v[24:27]
	v_mfma_f32_16x16x32_bf16 v[20:23], v[168:171], v[192:195], v[20:23]
	v_mfma_f32_16x16x32_bf16 v[16:19], v[176:179], v[192:195], v[16:19]
	v_mfma_f32_16x16x32_bf16 v[12:15], v[168:171], v[200:203], v[12:15]
	v_mfma_f32_16x16x32_bf16 v[8:11], v[176:179], v[200:203], v[8:11]
	v_mfma_f32_16x16x32_bf16 v[4:7], v[168:171], v[208:211], v[4:7]
	v_mfma_f32_16x16x32_bf16 v[0:3], v[176:179], v[208:211], v[0:3]
	v_mfma_f32_16x16x32_bf16 v[28:31], v[172:175], v[188:191], v[28:31]
	v_mfma_f32_16x16x32_bf16 v[24:27], v[180:183], v[188:191], v[24:27]
	v_mfma_f32_16x16x32_bf16 v[20:23], v[172:175], v[196:199], v[20:23]
	v_mfma_f32_16x16x32_bf16 v[16:19], v[180:183], v[196:199], v[16:19]
	v_mfma_f32_16x16x32_bf16 v[12:15], v[172:175], v[204:207], v[12:15]
	v_mfma_f32_16x16x32_bf16 v[8:11], v[180:183], v[204:207], v[8:11]
	v_mfma_f32_16x16x32_bf16 v[4:7], v[172:175], v[212:215], v[4:7]
	v_mfma_f32_16x16x32_bf16 v[0:3], v[180:183], v[212:215], v[0:3]
	s_barrier
	s_setprio 0
	v_add_u32_e32 v130, 0x18000, v157
	ds_read_b128 v[146:149], v130
	ds_read_b128 v[150:153], v130 offset:1024
	ds_read_b128 v[160:163], v130 offset:2048
	ds_read_b128 v[164:167], v130 offset:3072
	v_add_u32_e32 v130, 0x1c000, v157
	ds_read_b128 v[168:171], v130
	ds_read_b128 v[172:175], v130 offset:1024
	ds_read_b128 v[176:179], v130 offset:2048
	ds_read_b128 v[180:183], v130 offset:3072
	ds_read_b128 v[184:187], v158 offset:32768
	ds_read_b128 v[188:191], v158 offset:33792
	ds_read_b128 v[192:195], v158 offset:34816
	ds_read_b128 v[196:199], v158 offset:35840
	ds_read_b128 v[200:203], v158 offset:36864
	ds_read_b128 v[204:207], v158 offset:37888
	ds_read_b128 v[208:211], v158 offset:38912
	ds_read_b128 v[212:215], v158 offset:39936
	s_add_u32 s42, s62, 0x80000
	s_addc_u32 s43, s63, 0
	s_mov_b32 s51, m0
	s_mov_b32 m0, s72
	s_nop 0
	global_load_lds_dwordx4 v129, s[42:43]
	s_mov_b32 m0, s51
	s_nop 0
	s_mov_b32 s51, m0
	s_mov_b32 m0, s73
	s_nop 0
	global_load_lds_dwordx4 v154, s[42:43]
	s_mov_b32 m0, s51
	s_waitcnt vmcnt(8)
	s_waitcnt lgkmcnt(0)
	s_setprio 1
	s_barrier
	v_mfma_f32_16x16x32_bf16 v[124:127], v[146:149], v[184:187], v[124:127]
	v_mfma_f32_16x16x32_bf16 v[120:123], v[160:163], v[184:187], v[120:123]
	v_mfma_f32_16x16x32_bf16 v[116:119], v[146:149], v[192:195], v[116:119]
	v_mfma_f32_16x16x32_bf16 v[112:115], v[160:163], v[192:195], v[112:115]
	v_mfma_f32_16x16x32_bf16 v[108:111], v[146:149], v[200:203], v[108:111]
	v_mfma_f32_16x16x32_bf16 v[104:107], v[160:163], v[200:203], v[104:107]
	v_mfma_f32_16x16x32_bf16 v[100:103], v[146:149], v[208:211], v[100:103]
	v_mfma_f32_16x16x32_bf16 v[96:99], v[160:163], v[208:211], v[96:99]
	v_mfma_f32_16x16x32_bf16 v[124:127], v[150:153], v[188:191], v[124:127]
	v_mfma_f32_16x16x32_bf16 v[120:123], v[164:167], v[188:191], v[120:123]
	v_mfma_f32_16x16x32_bf16 v[116:119], v[150:153], v[196:199], v[116:119]
	v_mfma_f32_16x16x32_bf16 v[112:115], v[164:167], v[196:199], v[112:115]
	v_mfma_f32_16x16x32_bf16 v[108:111], v[150:153], v[204:207], v[108:111]
	v_mfma_f32_16x16x32_bf16 v[104:107], v[164:167], v[204:207], v[104:107]
	v_mfma_f32_16x16x32_bf16 v[100:103], v[150:153], v[212:215], v[100:103]
	v_mfma_f32_16x16x32_bf16 v[96:99], v[164:167], v[212:215], v[96:99]
	v_mfma_f32_16x16x32_bf16 v[92:95], v[168:171], v[184:187], v[92:95]
	v_mfma_f32_16x16x32_bf16 v[88:91], v[176:179], v[184:187], v[88:91]
	v_mfma_f32_16x16x32_bf16 v[84:87], v[168:171], v[192:195], v[84:87]
	v_mfma_f32_16x16x32_bf16 v[80:83], v[176:179], v[192:195], v[80:83]
	v_mfma_f32_16x16x32_bf16 v[76:79], v[168:171], v[200:203], v[76:79]
	v_mfma_f32_16x16x32_bf16 v[72:75], v[176:179], v[200:203], v[72:75]
	v_mfma_f32_16x16x32_bf16 v[68:71], v[168:171], v[208:211], v[68:71]
	v_mfma_f32_16x16x32_bf16 v[64:67], v[176:179], v[208:211], v[64:67]
	v_mfma_f32_16x16x32_bf16 v[92:95], v[172:175], v[188:191], v[92:95]
	v_mfma_f32_16x16x32_bf16 v[88:91], v[180:183], v[188:191], v[88:91]
	v_mfma_f32_16x16x32_bf16 v[84:87], v[172:175], v[196:199], v[84:87]
	v_mfma_f32_16x16x32_bf16 v[80:83], v[180:183], v[196:199], v[80:83]
	v_mfma_f32_16x16x32_bf16 v[76:79], v[172:175], v[204:207], v[76:79]
	v_mfma_f32_16x16x32_bf16 v[72:75], v[180:183], v[204:207], v[72:75]
	v_mfma_f32_16x16x32_bf16 v[68:71], v[172:175], v[212:215], v[68:71]
	v_mfma_f32_16x16x32_bf16 v[64:67], v[180:183], v[212:215], v[64:67]
	s_barrier
; #define PG8_STAGE(bufoff, gbase, voff) do { _Pragma("unroll") for (int _i = 0; _i < 2; ++_i) { unsigned keep_; \
;         asm volatile("s_mov_b32 %0, m0\n\ts_mov_b32 m0, %3\n\ts_nop 0\n\tglobal_load_lds_dwordx4 %1, %2\n\ts_mov_b32 m0, %0" : "=&s"(keep_) : "v"((voff)[_i]), "s"((const char*)(gbase)), "s"(ldsbase + (unsigned)((bufoff) + _i * 8192)) : "memory"); } } while (0)
; #define PG8_WAIT_V(n) asm volatile("s_waitcnt vmcnt(" #n ")" ::: "memory")
; #define PG8_WAIT_L(n) asm volatile("s_waitcnt lgkmcnt(" #n ")" ::: "memory")
; #define PG8_BAR __builtin_amdgcn_s_barrier()
; #define PG8_SCHED __builtin_amdgcn_sched_barrier(0)
; template <class Epi, class Sched, bool ALIGN_EPI, bool FP8 = false>
; DI void gemm_phase(LAS unsigned char* lds, const Gemm g, const Sched& S, const Epi& E) {
;     ...
;             PG8_LDA(At, 1, 1); PG8_STAGE(PG8_SB(1, 0), b3, voffB); PG8_STAGE(PG8_SB(1, 1), b3 + hstepB, voffB); PG8_STAGE(PG8_SA(1, 0), a3, voffA);
;             PG8_WAIT_V(8); PG8_WAIT_L(0); PG8_BAR; PG8_MMA(1, 0, At, B0); PG8_MMA(1, 1, At, B1); PG8_BAR; PG8_SCHED;
;         }
	s_setprio 0
	ds_read_b128 v[184:187], v158 offset:49152
	ds_read_b128 v[188:191], v158 offset:50176
	ds_read_b128 v[192:195], v158 offset:51200
	ds_read_b128 v[196:199], v158 offset:52224
	ds_read_b128 v[200:203], v158 offset:53248
	ds_read_b128 v[204:207], v158 offset:54272
	ds_read_b128 v[208:211], v158 offset:55296
	ds_read_b128 v[212:215], v158 offset:56320
	s_add_u32 s42, s60, 0x80
	s_addc_u32 s43, s61, 0
	s_mov_b32 s51, m0
	s_mov_b32 m0, s83
	s_nop 0
	global_load_lds_dwordx4 v145, s[42:43]
	s_mov_b32 m0, s51
	s_nop 0
	s_mov_b32 s51, m0
	s_mov_b32 m0, s84
	s_nop 0
	global_load_lds_dwordx4 v155, s[42:43]
	s_mov_b32 m0, s51
	s_add_u32 s42, s60, 0x80080
	s_addc_u32 s43, s61, 0
	s_mov_b32 s51, m0
	s_mov_b32 m0, s87
	s_nop 0
	global_load_lds_dwordx4 v145, s[42:43]
	s_mov_b32 m0, s51
	s_nop 0
	s_mov_b32 s51, m0
	s_mov_b32 m0, s88
	s_nop 0
	global_load_lds_dwordx4 v155, s[42:43]
	s_mov_b32 m0, s51
	s_mov_b32 s42, m0
	s_mov_b32 m0, s85
	s_nop 0
	global_load_lds_dwordx4 v129, s[58:59]
	s_mov_b32 m0, s42
	s_nop 0
	s_mov_b32 s42, m0
	s_mov_b32 m0, s86
	s_nop 0
	global_load_lds_dwordx4 v154, s[58:59]
	s_mov_b32 m0, s42
	s_waitcnt vmcnt(8)
	s_waitcnt lgkmcnt(0)
	s_setprio 1
	s_barrier
	v_mfma_f32_16x16x32_bf16 v[60:63], v[146:149], v[184:187], v[60:63]
	v_mfma_f32_16x16x32_bf16 v[56:59], v[160:163], v[184:187], v[56:59]
	v_mfma_f32_16x16x32_bf16 v[52:55], v[146:149], v[192:195], v[52:55]
	v_mfma_f32_16x16x32_bf16 v[48:51], v[160:163], v[192:195], v[48:51]
	v_mfma_f32_16x16x32_bf16 v[44:47], v[146:149], v[200:203], v[44:47]
	v_mfma_f32_16x16x32_bf16 v[40:43], v[160:163], v[200:203], v[40:43]
	v_mfma_f32_16x16x32_bf16 v[36:39], v[146:149], v[208:211], v[36:39]
	v_mfma_f32_16x16x32_bf16 v[32:35], v[160:163], v[208:211], v[32:35]
	v_mfma_f32_16x16x32_bf16 v[60:63], v[150:153], v[188:191], v[60:63]
	v_mfma_f32_16x16x32_bf16 v[56:59], v[164:167], v[188:191], v[56:59]
	v_mfma_f32_16x16x32_bf16 v[52:55], v[150:153], v[196:199], v[52:55]
	v_mfma_f32_16x16x32_bf16 v[48:51], v[164:167], v[196:199], v[48:51]
	v_mfma_f32_16x16x32_bf16 v[44:47], v[150:153], v[204:207], v[44:47]
	v_mfma_f32_16x16x32_bf16 v[40:43], v[164:167], v[204:207], v[40:43]
	v_mfma_f32_16x16x32_bf16 v[36:39], v[150:153], v[212:215], v[36:39]
	v_mfma_f32_16x16x32_bf16 v[32:35], v[164:167], v[212:215], v[32:35]
	v_mfma_f32_16x16x32_bf16 v[28:31], v[168:171], v[184:187], v[28:31]
	v_mfma_f32_16x16x32_bf16 v[24:27], v[176:179], v[184:187], v[24:27]
	v_mfma_f32_16x16x32_bf16 v[20:23], v[168:171], v[192:195], v[20:23]
	v_mfma_f32_16x16x32_bf16 v[16:19], v[176:179], v[192:195], v[16:19]
	v_mfma_f32_16x16x32_bf16 v[12:15], v[168:171], v[200:203], v[12:15]
	v_mfma_f32_16x16x32_bf16 v[8:11], v[176:179], v[200:203], v[8:11]
	v_mfma_f32_16x16x32_bf16 v[4:7], v[168:171], v[208:211], v[4:7]
	v_mfma_f32_16x16x32_bf16 v[0:3], v[176:179], v[208:211], v[0:3]
	v_mfma_f32_16x16x32_bf16 v[28:31], v[172:175], v[188:191], v[28:31]
	v_mfma_f32_16x16x32_bf16 v[24:27], v[180:183], v[188:191], v[24:27]
	v_mfma_f32_16x16x32_bf16 v[20:23], v[172:175], v[196:199], v[20:23]
	v_mfma_f32_16x16x32_bf16 v[16:19], v[180:183], v[196:199], v[16:19]
	v_mfma_f32_16x16x32_bf16 v[12:15], v[172:175], v[204:207], v[12:15]
	v_mfma_f32_16x16x32_bf16 v[8:11], v[180:183], v[204:207], v[8:11]
	v_mfma_f32_16x16x32_bf16 v[4:7], v[172:175], v[212:215], v[4:7]
	v_mfma_f32_16x16x32_bf16 v[0:3], v[180:183], v[212:215], v[0:3]
	s_barrier
	s_setprio 0
	s_add_u32 s56, s56, 0x100
	s_addc_u32 s57, s57, 0
	s_cmp_ge_u32 s53, s81
	s_mov_b32 s51, s53
	s_cbranch_scc0 .LBB0_255
	s_and_b64 vcc, exec, s[26:27]
	s_cbranch_vccnz .LBB0_265
	s_bitcmp0_b32 s77, 1
	s_mov_b64 s[56:57], -1
	v_lshl_add_u32 v142, s14, 8, v156
	s_cbranch_scc0 .LBB0_266

; #define PG8_STAGE(bufoff, gbase, voff) do { _Pragma("unroll") for (int _i = 0; _i < 2; ++_i) { unsigned keep_; \
;         asm volatile("s_mov_b32 %0, m0\n\ts_mov_b32 m0, %3\n\ts_nop 0\n\tglobal_load_lds_dwordx4 %1, %2\n\ts_mov_b32 m0, %0" : "=&s"(keep_) : "v"((voff)[_i]), "s"((const char*)(gbase)), "s"(ldsbase + (unsigned)((bufoff) + _i * 8192)) : "memory"); } } while (0)
; #define PG8_WAIT_V(n) asm volatile("s_waitcnt vmcnt(" #n ")" ::: "memory")
; #define PG8_WAIT_L(n) asm volatile("s_waitcnt lgkmcnt(" #n ")" ::: "memory")
; #define PG8_BAR __builtin_amdgcn_s_barrier()
; #define PG8_SCHED __builtin_amdgcn_sched_barrier(0)
;     DI int nt(const Unit& u) const { return (u.aux & 8) ? PLED / 64 : ((u.aux & 4) ? (D_ / 2) / 64 : D_ / 64); }
; template <class Epi, class Sched, bool ALIGN_EPI, bool FP8 = false>
; DI void gemm_phase(LAS unsigned char* lds, const Gemm g, const Sched& S, const Epi& E) {
;     ...
;         for (int t = 0; t < nt; t += 2) {
;             if constexpr (Epi::MID) { if (t == (nt >> 1)) E.mid(acc, cur, wr, wc, fr, fq); }
;             const bool last = (t == nt - 2);
;             const char* a1 = cA + (size_t)(t + 1) * kstep;
;             const char* a2 = last ? nA : cA + (size_t)(t + 2) * kstep; const char* b2 = last ? nB : cB + (size_t)(t + 2) * kstep;
;             const char* a3 = a2 + kstep; const char* b3 = b2 + kstep;
;             PG8_LDB(B0, 0, 0); PG8_LDB(B1, 0, 1); PG8_SCHED; PG8_LDA(At, 0, 0); PG8_STAGE(PG8_SA(1, 1), a1 + hstepA, voffA);
;             PG8_WAIT_V(8); PG8_WAIT_L(0); PG8_BAR; PG8_MMA(0, 0, At, B0); PG8_MMA(0, 1, At, B1); PG8_BAR; PG8_SCHED;
;             PG8_LDA(At, 0, 1); PG8_STAGE(PG8_SB(0, 0), b2, voffB); PG8_STAGE(PG8_SB(0, 1), b2 + hstepB, voffB); PG8_STAGE(PG8_SA(0, 0), a2, voffA);
;             PG8_WAIT_V(8); PG8_WAIT_L(0); PG8_BAR; PG8_MMA(1, 0, At, B0); PG8_MMA(1, 1, At, B1); PG8_BAR; PG8_SCHED;
.LBB0_298:
	ds_read_b128 v[104:107], v151
	s_waitcnt vmcnt(8)
	ds_read_b128 v[108:111], v151 offset:16
	ds_read_b128 v[112:115], v151 offset:2048
	ds_read_b128 v[116:119], v151 offset:2064
	ds_read_b128 v[160:163], v151 offset:16384
	ds_read_b128 v[164:167], v151 offset:16400
	ds_read_b128 v[168:171], v151 offset:18432
	ds_read_b128 v[172:175], v151 offset:18448
	s_add_u32 s52, s50, 0x100
	s_addc_u32 s53, s51, 0
	s_cmp_eq_u32 s91, 12
	s_cselect_b32 s58, s87, s52
	s_cselect_b32 s59, s43, s53
	s_cselect_b32 s56, s88, s89
	s_cselect_b32 s57, s41, s90
	s_add_u32 s54, s58, 0x80
	s_addc_u32 s55, s59, 0
	ds_read_b128 v[176:179], v150
	ds_read_b128 v[180:183], v150 offset:16
	ds_read_b128 v[184:187], v150 offset:2048
	ds_read_b128 v[188:191], v150 offset:2064
	ds_read_b128 v[192:195], v150 offset:4096
	ds_read_b128 v[196:199], v150 offset:4112
	ds_read_b128 v[200:203], v150 offset:6144
	ds_read_b128 v[204:207], v150 offset:6160
	s_add_u32 s50, s50, 0x40080
	s_addc_u32 s51, s51, 0
	s_mov_b32 s92, m0
	s_mov_b32 m0, s75
	s_nop 0
	global_load_lds_dwordx4 v152, s[50:51]
	s_mov_b32 m0, s92
	s_nop 0
	s_mov_b32 s92, m0
	s_mov_b32 m0, s77
	s_nop 0
	global_load_lds_dwordx4 v154, s[50:51]
	s_mov_b32 m0, s92
	s_waitcnt vmcnt(8)
	s_waitcnt lgkmcnt(0)
	s_setprio 1
	s_barrier
	v_mfma_scale_f32_16x16x128_f8f6f4 v[140:143], v[104:111], v[176:183], v[140:143], v158, v158 op_sel_hi:[0,0,0]
	v_mfma_scale_f32_16x16x128_f8f6f4 v[136:139], v[112:119], v[176:183], v[136:139], v158, v158 op_sel_hi:[0,0,0]
	v_mfma_scale_f32_16x16x128_f8f6f4 v[124:127], v[104:111], v[184:191], v[124:127], v158, v158 op_sel_hi:[0,0,0]
	v_mfma_scale_f32_16x16x128_f8f6f4 v[120:123], v[112:119], v[184:191], v[120:123], v158, v158 op_sel_hi:[0,0,0]
	v_mfma_scale_f32_16x16x128_f8f6f4 v[208:211], v[104:111], v[192:199], v[92:95], v158, v158 op_sel_hi:[0,0,0]
	v_mfma_scale_f32_16x16x128_f8f6f4 v[212:215], v[112:119], v[192:199], v[88:91], v158, v158 op_sel_hi:[0,0,0]
	v_mfma_scale_f32_16x16x128_f8f6f4 v[216:219], v[104:111], v[200:207], v[76:79], v158, v158 op_sel_hi:[0,0,0]
	v_mfma_scale_f32_16x16x128_f8f6f4 v[220:223], v[112:119], v[200:207], v[72:75], v158, v158 op_sel_hi:[0,0,0]
	v_mfma_scale_f32_16x16x128_f8f6f4 v[132:135], v[160:167], v[176:183], v[132:135], v158, v158 op_sel_hi:[0,0,0]
	v_mfma_scale_f32_16x16x128_f8f6f4 v[128:131], v[168:175], v[176:183], v[128:131], v158, v158 op_sel_hi:[0,0,0]
	v_mfma_scale_f32_16x16x128_f8f6f4 v[100:103], v[160:167], v[184:191], v[100:103], v158, v158 op_sel_hi:[0,0,0]
	v_mfma_scale_f32_16x16x128_f8f6f4 v[96:99], v[168:175], v[184:191], v[96:99], v158, v158 op_sel_hi:[0,0,0]
	v_mfma_scale_f32_16x16x128_f8f6f4 v[176:179], v[160:167], v[192:199], v[84:87], v158, v158 op_sel_hi:[0,0,0]
	v_mfma_scale_f32_16x16x128_f8f6f4 v[180:183], v[168:175], v[192:199], v[80:83], v158, v158 op_sel_hi:[0,0,0]
	v_mfma_scale_f32_16x16x128_f8f6f4 v[184:187], v[160:167], v[200:207], v[68:71], v158, v158 op_sel_hi:[0,0,0]
	v_mfma_scale_f32_16x16x128_f8f6f4 v[188:191], v[168:175], v[200:207], v[64:67], v158, v158 op_sel_hi:[0,0,0]
	s_barrier
	s_setprio 0
	s_nop 4
	ds_read_b128 v[64:67], v150 offset:16384
	ds_read_b128 v[68:71], v150 offset:16400
	ds_read_b128 v[72:75], v150 offset:18432
	ds_read_b128 v[76:79], v150 offset:18448
	ds_read_b128 v[80:83], v150 offset:20480
	ds_read_b128 v[84:87], v150 offset:20496
	ds_read_b128 v[88:91], v150 offset:22528
	ds_read_b128 v[92:95], v150 offset:22544
	s_mov_b32 s50, m0
	s_mov_b32 m0, s49
	s_nop 0
	global_load_lds_dwordx4 v153, s[56:57]
	s_mov_b32 m0, s50
	s_nop 0
	s_mov_b32 s50, m0
	s_mov_b32 m0, s63
	s_nop 0
	global_load_lds_dwordx4 v155, s[56:57]
	s_mov_b32 m0, s50
	s_add_u32 s50, s56, 0x40000
	s_addc_u32 s51, s57, 0
	s_mov_b32 s92, m0
	s_mov_b32 m0, s64
	s_nop 0
	global_load_lds_dwordx4 v153, s[50:51]
	s_mov_b32 m0, s92
	s_nop 0
	s_mov_b32 s92, m0
	s_mov_b32 m0, s65
	s_nop 0
	global_load_lds_dwordx4 v155, s[50:51]
	s_mov_b32 m0, s92
	s_mov_b32 s50, m0
	s_mov_b32 m0, s62
	s_nop 0
	global_load_lds_dwordx4 v152, s[58:59]
	s_mov_b32 m0, s50
	s_nop 0
	s_mov_b32 s50, m0
	s_mov_b32 m0, s66
	s_nop 0
	global_load_lds_dwordx4 v154, s[58:59]
	s_mov_b32 m0, s50
	s_waitcnt vmcnt(8)
	s_waitcnt lgkmcnt(0)
	s_setprio 1
	s_barrier
	v_mfma_scale_f32_16x16x128_f8f6f4 v[60:63], v[104:111], v[64:71], v[60:63], v158, v158 op_sel_hi:[0,0,0]
	v_mfma_scale_f32_16x16x128_f8f6f4 v[56:59], v[112:119], v[64:71], v[56:59], v158, v158 op_sel_hi:[0,0,0]
	v_mfma_scale_f32_16x16x128_f8f6f4 v[192:195], v[104:111], v[72:79], v[44:47], v158, v158 op_sel_hi:[0,0,0]
	v_mfma_scale_f32_16x16x128_f8f6f4 v[196:199], v[112:119], v[72:79], v[40:43], v158, v158 op_sel_hi:[0,0,0]
	v_mfma_scale_f32_16x16x128_f8f6f4 v[200:203], v[104:111], v[80:87], v[28:31], v158, v158 op_sel_hi:[0,0,0]
	v_mfma_scale_f32_16x16x128_f8f6f4 v[204:207], v[112:119], v[80:87], v[24:27], v158, v158 op_sel_hi:[0,0,0]
	v_mfma_scale_f32_16x16x128_f8f6f4 v[224:227], v[104:111], v[88:95], v[12:15], v158, v158 op_sel_hi:[0,0,0]
	v_mfma_scale_f32_16x16x128_f8f6f4 v[228:231], v[112:119], v[88:95], v[8:11], v158, v158 op_sel_hi:[0,0,0]
	v_mfma_scale_f32_16x16x128_f8f6f4 v[52:55], v[160:167], v[64:71], v[52:55], v158, v158 op_sel_hi:[0,0,0]
	v_mfma_scale_f32_16x16x128_f8f6f4 v[48:51], v[168:175], v[64:71], v[48:51], v158, v158 op_sel_hi:[0,0,0]
	v_mfma_scale_f32_16x16x128_f8f6f4 v[232:235], v[160:167], v[72:79], v[36:39], v158, v158 op_sel_hi:[0,0,0]
	v_mfma_scale_f32_16x16x128_f8f6f4 v[236:239], v[168:175], v[72:79], v[32:35], v158, v158 op_sel_hi:[0,0,0]
	v_mfma_scale_f32_16x16x128_f8f6f4 v[240:243], v[160:167], v[80:87], v[20:23], v158, v158 op_sel_hi:[0,0,0]
	v_mfma_scale_f32_16x16x128_f8f6f4 v[244:247], v[168:175], v[80:87], v[16:19], v158, v158 op_sel_hi:[0,0,0]
	v_mfma_scale_f32_16x16x128_f8f6f4 v[248:251], v[160:167], v[88:95], v[4:7], v158, v158 op_sel_hi:[0,0,0]
	v_mfma_scale_f32_16x16x128_f8f6f4 v[144:147], v[168:175], v[88:95], v[0:3], v158, v158 op_sel_hi:[0,0,0]
	s_barrier
; #define PG8_STAGE(bufoff, gbase, voff) do { _Pragma("unroll") for (int _i = 0; _i < 2; ++_i) { unsigned keep_; \
;         asm volatile("s_mov_b32 %0, m0\n\ts_mov_b32 m0, %3\n\ts_nop 0\n\tglobal_load_lds_dwordx4 %1, %2\n\ts_mov_b32 m0, %0" : "=&s"(keep_) : "v"((voff)[_i]), "s"((const char*)(gbase)), "s"(ldsbase + (unsigned)((bufoff) + _i * 8192)) : "memory"); } } while (0)
; #define PG8_WAIT_V(n) asm volatile("s_waitcnt vmcnt(" #n ")" ::: "memory")
; #define PG8_WAIT_L(n) asm volatile("s_waitcnt lgkmcnt(" #n ")" ::: "memory")
; #define PG8_BAR __builtin_amdgcn_s_barrier()
; #define PG8_SCHED __builtin_amdgcn_sched_barrier(0)
; template <class Epi, class Sched, bool ALIGN_EPI, bool FP8 = false>
; DI void gemm_phase(LAS unsigned char* lds, const Gemm g, const Sched& S, const Epi& E) {
;     ...
;             PG8_LDB(B0, 1, 0); PG8_LDB(B1, 1, 1); PG8_SCHED; PG8_LDA(At, 1, 0); PG8_STAGE(PG8_SA(0, 1), a2 + hstepA, voffA);
;             PG8_WAIT_V(8); PG8_WAIT_L(0); PG8_BAR; PG8_MMA(0, 0, At, B0); PG8_MMA(0, 1, At, B1); PG8_BAR; PG8_SCHED;
;             PG8_LDA(At, 1, 1); PG8_STAGE(PG8_SB(1, 0), b3, voffB); PG8_STAGE(PG8_SB(1, 1), b3 + hstepB, voffB); PG8_STAGE(PG8_SA(1, 0), a3, voffA);
;             PG8_WAIT_V(8); PG8_WAIT_L(0); PG8_BAR; PG8_MMA(1, 0, At, B0); PG8_MMA(1, 1, At, B1); PG8_BAR; PG8_SCHED;
;         }
	s_setprio 0
	s_nop 4
	ds_read_b128 v[0:3], v151 offset:32768
	ds_read_b128 v[4:7], v151 offset:32784
	ds_read_b128 v[16:19], v151 offset:34816
	ds_read_b128 v[20:23], v151 offset:34832
	ds_read_b128 v[104:107], v151 offset:49152
	ds_read_b128 v[108:111], v151 offset:49168
	ds_read_b128 v[112:115], v151 offset:51200
	ds_read_b128 v[116:119], v151 offset:51216
	ds_read_b128 v[8:11], v150 offset:32768
	ds_read_b128 v[12:15], v150 offset:32784
	ds_read_b128 v[24:27], v150 offset:34816
	ds_read_b128 v[28:31], v150 offset:34832
	ds_read_b128 v[32:35], v150 offset:36864
	ds_read_b128 v[36:39], v150 offset:36880
	ds_read_b128 v[40:43], v150 offset:38912
	ds_read_b128 v[44:47], v150 offset:38928
	s_add_u32 s50, s58, 0x40000
	s_addc_u32 s51, s59, 0
	s_mov_b32 s58, m0
	s_mov_b32 m0, s67
	s_nop 0
	global_load_lds_dwordx4 v152, s[50:51]
	s_mov_b32 m0, s58
	s_nop 0
	s_mov_b32 s58, m0
	s_mov_b32 m0, s68
	s_nop 0
	global_load_lds_dwordx4 v154, s[50:51]
	s_mov_b32 m0, s58
	s_waitcnt vmcnt(8)
	s_waitcnt lgkmcnt(0)
	s_setprio 1
	s_barrier
	v_mfma_scale_f32_16x16x128_f8f6f4 v[140:143], v[0:7], v[8:15], v[140:143], v158, v158 op_sel_hi:[0,0,0]
	v_mfma_scale_f32_16x16x128_f8f6f4 v[136:139], v[16:23], v[8:15], v[136:139], v158, v158 op_sel_hi:[0,0,0]
	v_mfma_scale_f32_16x16x128_f8f6f4 v[124:127], v[0:7], v[24:31], v[124:127], v158, v158 op_sel_hi:[0,0,0]
	v_mfma_scale_f32_16x16x128_f8f6f4 v[120:123], v[16:23], v[24:31], v[120:123], v158, v158 op_sel_hi:[0,0,0]
	v_mfma_scale_f32_16x16x128_f8f6f4 v[92:95], v[0:7], v[32:39], v[208:211], v158, v158 op_sel_hi:[0,0,0]
	v_mfma_scale_f32_16x16x128_f8f6f4 v[88:91], v[16:23], v[32:39], v[212:215], v158, v158 op_sel_hi:[0,0,0]
	v_mfma_scale_f32_16x16x128_f8f6f4 v[76:79], v[0:7], v[40:47], v[216:219], v158, v158 op_sel_hi:[0,0,0]
	v_mfma_scale_f32_16x16x128_f8f6f4 v[72:75], v[16:23], v[40:47], v[220:223], v158, v158 op_sel_hi:[0,0,0]
	v_mfma_scale_f32_16x16x128_f8f6f4 v[132:135], v[104:111], v[8:15], v[132:135], v158, v158 op_sel_hi:[0,0,0]
	v_mfma_scale_f32_16x16x128_f8f6f4 v[128:131], v[112:119], v[8:15], v[128:131], v158, v158 op_sel_hi:[0,0,0]
	v_mfma_scale_f32_16x16x128_f8f6f4 v[100:103], v[104:111], v[24:31], v[100:103], v158, v158 op_sel_hi:[0,0,0]
	v_mfma_scale_f32_16x16x128_f8f6f4 v[96:99], v[112:119], v[24:31], v[96:99], v158, v158 op_sel_hi:[0,0,0]
	v_mfma_scale_f32_16x16x128_f8f6f4 v[84:87], v[104:111], v[32:39], v[176:179], v158, v158 op_sel_hi:[0,0,0]
	v_mfma_scale_f32_16x16x128_f8f6f4 v[80:83], v[112:119], v[32:39], v[180:183], v158, v158 op_sel_hi:[0,0,0]
	v_mfma_scale_f32_16x16x128_f8f6f4 v[68:71], v[104:111], v[40:47], v[184:187], v158, v158 op_sel_hi:[0,0,0]
	v_mfma_scale_f32_16x16x128_f8f6f4 v[64:67], v[112:119], v[40:47], v[188:191], v158, v158 op_sel_hi:[0,0,0]
	s_barrier
	s_setprio 0
	ds_read_b128 v[32:35], v150 offset:49152
	ds_read_b128 v[36:39], v150 offset:49168
	ds_read_b128 v[160:163], v150 offset:51200
	ds_read_b128 v[164:167], v150 offset:51216
	ds_read_b128 v[168:171], v150 offset:53248
	ds_read_b128 v[172:175], v150 offset:53264
	ds_read_b128 v[176:179], v150 offset:55296
	ds_read_b128 v[180:183], v150 offset:55312
	s_add_u32 s50, s56, 0x80
	s_addc_u32 s51, s57, 0
	s_mov_b32 s58, m0
	s_mov_b32 m0, s69
	s_nop 0
	global_load_lds_dwordx4 v153, s[50:51]
	s_mov_b32 m0, s58
	s_nop 0
	s_mov_b32 s58, m0
	s_mov_b32 m0, s70
	s_nop 0
	global_load_lds_dwordx4 v155, s[50:51]
	s_mov_b32 m0, s58
	s_add_u32 s50, s56, 0x40080
	s_addc_u32 s51, s57, 0
	s_mov_b32 s56, m0
	s_mov_b32 m0, s73
	s_nop 0
	global_load_lds_dwordx4 v153, s[50:51]
	s_mov_b32 m0, s56
	s_nop 0
	s_mov_b32 s56, m0
	s_mov_b32 m0, s74
	s_nop 0
	global_load_lds_dwordx4 v155, s[50:51]
	s_mov_b32 m0, s56
	s_mov_b32 s50, m0
	s_mov_b32 m0, s71
	s_nop 0
	global_load_lds_dwordx4 v152, s[54:55]
	s_mov_b32 m0, s50
	s_nop 0
	s_mov_b32 s50, m0
	s_mov_b32 m0, s72
	s_nop 0
	global_load_lds_dwordx4 v154, s[54:55]
	s_mov_b32 m0, s50
	s_waitcnt vmcnt(8)
	s_waitcnt lgkmcnt(0)
	s_setprio 1
	s_barrier
	v_mfma_scale_f32_16x16x128_f8f6f4 v[60:63], v[0:7], v[32:39], v[60:63], v158, v158 op_sel_hi:[0,0,0]
	v_mfma_scale_f32_16x16x128_f8f6f4 v[56:59], v[16:23], v[32:39], v[56:59], v158, v158 op_sel_hi:[0,0,0]
	v_mfma_scale_f32_16x16x128_f8f6f4 v[44:47], v[0:7], v[160:167], v[192:195], v158, v158 op_sel_hi:[0,0,0]
	v_mfma_scale_f32_16x16x128_f8f6f4 v[40:43], v[16:23], v[160:167], v[196:199], v158, v158 op_sel_hi:[0,0,0]
	v_mfma_scale_f32_16x16x128_f8f6f4 v[28:31], v[0:7], v[168:175], v[200:203], v158, v158 op_sel_hi:[0,0,0]
	v_mfma_scale_f32_16x16x128_f8f6f4 v[24:27], v[16:23], v[168:175], v[204:207], v158, v158 op_sel_hi:[0,0,0]
	v_mfma_scale_f32_16x16x128_f8f6f4 v[12:15], v[0:7], v[176:183], v[224:227], v158, v158 op_sel_hi:[0,0,0]
	v_mfma_scale_f32_16x16x128_f8f6f4 v[8:11], v[16:23], v[176:183], v[228:231], v158, v158 op_sel_hi:[0,0,0]
	v_mfma_scale_f32_16x16x128_f8f6f4 v[52:55], v[104:111], v[32:39], v[52:55], v158, v158 op_sel_hi:[0,0,0]
	v_mfma_scale_f32_16x16x128_f8f6f4 v[48:51], v[112:119], v[32:39], v[48:51], v158, v158 op_sel_hi:[0,0,0]
	v_mfma_scale_f32_16x16x128_f8f6f4 v[36:39], v[104:111], v[160:167], v[232:235], v158, v158 op_sel_hi:[0,0,0]
	v_mfma_scale_f32_16x16x128_f8f6f4 v[32:35], v[112:119], v[160:167], v[236:239], v158, v158 op_sel_hi:[0,0,0]
	v_mfma_scale_f32_16x16x128_f8f6f4 v[20:23], v[104:111], v[168:175], v[240:243], v158, v158 op_sel_hi:[0,0,0]
	v_mfma_scale_f32_16x16x128_f8f6f4 v[16:19], v[112:119], v[168:175], v[244:247], v158, v158 op_sel_hi:[0,0,0]
	v_mfma_scale_f32_16x16x128_f8f6f4 v[4:7], v[104:111], v[176:183], v[248:251], v158, v158 op_sel_hi:[0,0,0]
	v_mfma_scale_f32_16x16x128_f8f6f4 v[0:3], v[112:119], v[176:183], v[144:147], v158, v158 op_sel_hi:[0,0,0]
	s_barrier
	s_setprio 0
	s_add_i32 s91, s91, 2
	s_add_u32 s89, s89, 0x100
	s_addc_u32 s90, s90, 0
	s_cmp_gt_u32 s91, 13
	s_mov_b64 s[50:51], s[52:53]
	s_cbranch_scc0 .LBB0_298
	s_and_b64 vcc, exec, s[16:17]
	s_cbranch_vccz .LBB0_301
	s_barrier

; #define PG8_STAGE(bufoff, gbase, voff) do { _Pragma("unroll") for (int _i = 0; _i < 2; ++_i) { unsigned keep_; \
;         asm volatile("s_mov_b32 %0, m0\n\ts_mov_b32 m0, %3\n\ts_nop 0\n\tglobal_load_lds_dwordx4 %1, %2\n\ts_mov_b32 m0, %0" : "=&s"(keep_) : "v"((voff)[_i]), "s"((const char*)(gbase)), "s"(ldsbase + (unsigned)((bufoff) + _i * 8192)) : "memory"); } } while (0)
; #define PG8_WAIT_V(n) asm volatile("s_waitcnt vmcnt(" #n ")" ::: "memory")
; #define PG8_WAIT_L(n) asm volatile("s_waitcnt lgkmcnt(" #n ")" ::: "memory")
; #define PG8_BAR __builtin_amdgcn_s_barrier()
; #define PG8_SCHED __builtin_amdgcn_sched_barrier(0)
;     DI int nt(const Unit& u) const { return (u.aux & 8) ? PLED / 64 : ((u.aux & 4) ? (D_ / 2) / 64 : D_ / 64); }
; template <class Epi, class Sched, bool ALIGN_EPI, bool FP8 = false>
; DI void gemm_phase(LAS unsigned char* lds, const Gemm g, const Sched& S, const Epi& E) {
;     ...
;         for (int t = 0; t < nt; t += 2) {
;             if constexpr (Epi::MID) { if (t == (nt >> 1)) E.mid(acc, cur, wr, wc, fr, fq); }
;             const bool last = (t == nt - 2);
;             const char* a1 = cA + (size_t)(t + 1) * kstep;
;             const char* a2 = last ? nA : cA + (size_t)(t + 2) * kstep; const char* b2 = last ? nB : cB + (size_t)(t + 2) * kstep;
;             const char* a3 = a2 + kstep; const char* b3 = b2 + kstep;
;             PG8_LDB(B0, 0, 0); PG8_LDB(B1, 0, 1); PG8_SCHED; PG8_LDA(At, 0, 0); PG8_STAGE(PG8_SA(1, 1), a1 + hstepA, voffA);
;             PG8_WAIT_V(8); PG8_WAIT_L(0); PG8_BAR; PG8_MMA(0, 0, At, B0); PG8_MMA(0, 1, At, B1); PG8_BAR; PG8_SCHED;
;             PG8_LDA(At, 0, 1); PG8_STAGE(PG8_SB(0, 0), b2, voffB); PG8_STAGE(PG8_SB(0, 1), b2 + hstepB, voffB); PG8_STAGE(PG8_SA(0, 0), a2, voffA);
.LBB0_489:
	v_add_u32_e32 v1, 0x10000, v160
	ds_read_b128 v[132:135], v1
	ds_read_b128 v[136:139], v1 offset:1024
	ds_read_b128 v[140:143], v1 offset:2048
	ds_read_b128 v[162:165], v1 offset:3072
	v_add_u32_e32 v1, 0x14000, v160
	ds_read_b128 v[166:169], v1
	ds_read_b128 v[170:173], v1 offset:1024
	ds_read_b128 v[174:177], v1 offset:2048
	ds_read_b128 v[178:181], v1 offset:3072
	s_add_u32 s28, s26, 0x100
	s_addc_u32 s29, s27, 0
	s_cmp_eq_u32 s69, 28
	s_cselect_b32 s44, s65, s28
	s_cselect_b32 s45, s21, s29
	s_cselect_b32 s42, s66, s67
	s_cselect_b32 s43, s19, s68
	s_add_u32 s40, s44, 0x80
	s_addc_u32 s41, s45, 0
	ds_read_b128 v[182:185], v161
	ds_read_b128 v[186:189], v161 offset:1024
	ds_read_b128 v[190:193], v161 offset:2048
	ds_read_b128 v[194:197], v161 offset:3072
	ds_read_b128 v[198:201], v161 offset:4096
	ds_read_b128 v[202:205], v161 offset:5120
	ds_read_b128 v[206:209], v161 offset:6144
	ds_read_b128 v[210:213], v161 offset:7168
	s_add_u32 s26, s26, 0x80080
	s_addc_u32 s27, s27, 0
	s_mov_b32 s70, m0
	s_mov_b32 m0, s61
	s_nop 0
	global_load_lds_dwordx4 v154, s[26:27]
	s_mov_b32 m0, s70
	s_nop 0
	s_mov_b32 s70, m0
	s_mov_b32 m0, s62
	s_nop 0
	global_load_lds_dwordx4 v156, s[26:27]
	s_mov_b32 m0, s70
	s_waitcnt vmcnt(8)
	s_waitcnt lgkmcnt(0)
	s_setprio 1
	s_barrier
	v_mfma_f32_16x16x32_bf16 v[128:131], v[132:135], v[182:185], v[128:131]
	v_mfma_f32_16x16x32_bf16 v[124:127], v[140:143], v[182:185], v[124:127]
	v_mfma_f32_16x16x32_bf16 v[112:115], v[132:135], v[190:193], v[112:115]
	v_mfma_f32_16x16x32_bf16 v[108:111], v[140:143], v[190:193], v[108:111]
	v_mfma_f32_16x16x32_bf16 v[96:99], v[132:135], v[198:201], v[96:99]
	v_mfma_f32_16x16x32_bf16 v[92:95], v[140:143], v[198:201], v[92:95]
	v_mfma_f32_16x16x32_bf16 v[80:83], v[132:135], v[206:209], v[80:83]
	v_mfma_f32_16x16x32_bf16 v[76:79], v[140:143], v[206:209], v[76:79]
	v_mfma_f32_16x16x32_bf16 v[128:131], v[136:139], v[186:189], v[128:131]
	v_mfma_f32_16x16x32_bf16 v[124:127], v[162:165], v[186:189], v[124:127]
	v_mfma_f32_16x16x32_bf16 v[112:115], v[136:139], v[194:197], v[112:115]
	v_mfma_f32_16x16x32_bf16 v[108:111], v[162:165], v[194:197], v[108:111]
	v_mfma_f32_16x16x32_bf16 v[96:99], v[136:139], v[202:205], v[96:99]
	v_mfma_f32_16x16x32_bf16 v[92:95], v[162:165], v[202:205], v[92:95]
	v_mfma_f32_16x16x32_bf16 v[80:83], v[136:139], v[210:213], v[80:83]
	v_mfma_f32_16x16x32_bf16 v[76:79], v[162:165], v[210:213], v[76:79]
	v_mfma_f32_16x16x32_bf16 v[120:123], v[166:169], v[182:185], v[120:123]
	v_mfma_f32_16x16x32_bf16 v[116:119], v[174:177], v[182:185], v[116:119]
	v_mfma_f32_16x16x32_bf16 v[104:107], v[166:169], v[190:193], v[104:107]
	v_mfma_f32_16x16x32_bf16 v[100:103], v[174:177], v[190:193], v[100:103]
	v_mfma_f32_16x16x32_bf16 v[88:91], v[166:169], v[198:201], v[88:91]
	v_mfma_f32_16x16x32_bf16 v[84:87], v[174:177], v[198:201], v[84:87]
	v_mfma_f32_16x16x32_bf16 v[72:75], v[166:169], v[206:209], v[72:75]
	v_mfma_f32_16x16x32_bf16 v[68:71], v[174:177], v[206:209], v[68:71]
	v_mfma_f32_16x16x32_bf16 v[120:123], v[170:173], v[186:189], v[120:123]
	v_mfma_f32_16x16x32_bf16 v[116:119], v[178:181], v[186:189], v[116:119]
	v_mfma_f32_16x16x32_bf16 v[104:107], v[170:173], v[194:197], v[104:107]
	v_mfma_f32_16x16x32_bf16 v[100:103], v[178:181], v[194:197], v[100:103]
	v_mfma_f32_16x16x32_bf16 v[88:91], v[170:173], v[202:205], v[88:91]
	v_mfma_f32_16x16x32_bf16 v[84:87], v[178:181], v[202:205], v[84:87]
	v_mfma_f32_16x16x32_bf16 v[72:75], v[170:173], v[210:213], v[72:75]
	v_mfma_f32_16x16x32_bf16 v[68:71], v[178:181], v[210:213], v[68:71]
	s_barrier
	s_setprio 0
	ds_read_b128 v[182:185], v161 offset:16384
	ds_read_b128 v[186:189], v161 offset:17408
	ds_read_b128 v[190:193], v161 offset:18432
	ds_read_b128 v[194:197], v161 offset:19456
	ds_read_b128 v[198:201], v161 offset:20480
	ds_read_b128 v[202:205], v161 offset:21504
	ds_read_b128 v[206:209], v161 offset:22528
	ds_read_b128 v[210:213], v161 offset:23552
	s_mov_b32 s26, m0
	s_mov_b32 m0, s48
	s_nop 0
	global_load_lds_dwordx4 v155, s[42:43]
	s_mov_b32 m0, s26
	s_nop 0
	s_mov_b32 s26, m0
	s_mov_b32 m0, s49
	s_nop 0
	global_load_lds_dwordx4 v157, s[42:43]
	s_mov_b32 m0, s26
	s_add_u32 s26, s42, 0x80000
	s_addc_u32 s27, s43, 0
	s_mov_b32 s70, m0
	s_mov_b32 m0, s50
	s_nop 0
	global_load_lds_dwordx4 v155, s[26:27]
	s_mov_b32 m0, s70
	s_nop 0
	s_mov_b32 s70, m0
	s_mov_b32 m0, s51
	s_nop 0
	global_load_lds_dwordx4 v157, s[26:27]
	s_mov_b32 m0, s70
	s_mov_b32 s26, m0
	s_mov_b32 m0, s47
	s_nop 0
	global_load_lds_dwordx4 v154, s[44:45]
	s_mov_b32 m0, s26
	s_nop 0
	s_mov_b32 s26, m0
	s_mov_b32 m0, s52
	s_nop 0
	global_load_lds_dwordx4 v156, s[44:45]
	s_mov_b32 m0, s26
	s_waitcnt vmcnt(8)
	s_waitcnt lgkmcnt(0)
	s_setprio 1
	s_barrier
; #define PG8_STAGE(bufoff, gbase, voff) do { _Pragma("unroll") for (int _i = 0; _i < 2; ++_i) { unsigned keep_; \
;         asm volatile("s_mov_b32 %0, m0\n\ts_mov_b32 m0, %3\n\ts_nop 0\n\tglobal_load_lds_dwordx4 %1, %2\n\ts_mov_b32 m0, %0" : "=&s"(keep_) : "v"((voff)[_i]), "s"((const char*)(gbase)), "s"(ldsbase + (unsigned)((bufoff) + _i * 8192)) : "memory"); } } while (0)
; #define PG8_WAIT_V(n) asm volatile("s_waitcnt vmcnt(" #n ")" ::: "memory")
; #define PG8_WAIT_L(n) asm volatile("s_waitcnt lgkmcnt(" #n ")" ::: "memory")
; #define PG8_BAR __builtin_amdgcn_s_barrier()
; #define PG8_SCHED __builtin_amdgcn_sched_barrier(0)
; template <class Epi, class Sched, bool ALIGN_EPI, bool FP8 = false>
; DI void gemm_phase(LAS unsigned char* lds, const Gemm g, const Sched& S, const Epi& E) {
;     ...
;             PG8_WAIT_V(8); PG8_WAIT_L(0); PG8_BAR; PG8_MMA(1, 0, At, B0); PG8_MMA(1, 1, At, B1); PG8_BAR; PG8_SCHED;
;             PG8_LDB(B0, 1, 0); PG8_LDB(B1, 1, 1); PG8_SCHED; PG8_LDA(At, 1, 0); PG8_STAGE(PG8_SA(0, 1), a2 + hstepA, voffA);
;             PG8_WAIT_V(8); PG8_WAIT_L(0); PG8_BAR; PG8_MMA(0, 0, At, B0); PG8_MMA(0, 1, At, B1); PG8_BAR; PG8_SCHED;
;             PG8_LDA(At, 1, 1); PG8_STAGE(PG8_SB(1, 0), b3, voffB); PG8_STAGE(PG8_SB(1, 1), b3 + hstepB, voffB); PG8_STAGE(PG8_SA(1, 0), a3, voffA);
	v_mfma_f32_16x16x32_bf16 v[64:67], v[132:135], v[182:185], v[64:67]
	v_mfma_f32_16x16x32_bf16 v[60:63], v[140:143], v[182:185], v[60:63]
	v_mfma_f32_16x16x32_bf16 v[48:51], v[132:135], v[190:193], v[48:51]
	v_mfma_f32_16x16x32_bf16 v[44:47], v[140:143], v[190:193], v[44:47]
	v_mfma_f32_16x16x32_bf16 v[32:35], v[132:135], v[198:201], v[32:35]
	v_mfma_f32_16x16x32_bf16 v[28:31], v[140:143], v[198:201], v[28:31]
	v_mfma_f32_16x16x32_bf16 v[16:19], v[132:135], v[206:209], v[16:19]
	v_mfma_f32_16x16x32_bf16 v[12:15], v[140:143], v[206:209], v[12:15]
	v_mfma_f32_16x16x32_bf16 v[64:67], v[136:139], v[186:189], v[64:67]
	v_mfma_f32_16x16x32_bf16 v[60:63], v[162:165], v[186:189], v[60:63]
	v_mfma_f32_16x16x32_bf16 v[48:51], v[136:139], v[194:197], v[48:51]
	v_mfma_f32_16x16x32_bf16 v[44:47], v[162:165], v[194:197], v[44:47]
	v_mfma_f32_16x16x32_bf16 v[32:35], v[136:139], v[202:205], v[32:35]
	v_mfma_f32_16x16x32_bf16 v[28:31], v[162:165], v[202:205], v[28:31]
	v_mfma_f32_16x16x32_bf16 v[16:19], v[136:139], v[210:213], v[16:19]
	v_mfma_f32_16x16x32_bf16 v[12:15], v[162:165], v[210:213], v[12:15]
	v_mfma_f32_16x16x32_bf16 v[56:59], v[166:169], v[182:185], v[56:59]
	v_mfma_f32_16x16x32_bf16 v[52:55], v[174:177], v[182:185], v[52:55]
	v_mfma_f32_16x16x32_bf16 v[40:43], v[166:169], v[190:193], v[40:43]
	v_mfma_f32_16x16x32_bf16 v[36:39], v[174:177], v[190:193], v[36:39]
	v_mfma_f32_16x16x32_bf16 v[24:27], v[166:169], v[198:201], v[24:27]
	v_mfma_f32_16x16x32_bf16 v[20:23], v[174:177], v[198:201], v[20:23]
	v_mfma_f32_16x16x32_bf16 v[8:11], v[166:169], v[206:209], v[8:11]
	v_mfma_f32_16x16x32_bf16 v[2:5], v[174:177], v[206:209], v[4:7]
	v_mfma_f32_16x16x32_bf16 v[56:59], v[170:173], v[186:189], v[56:59]
	v_mfma_f32_16x16x32_bf16 v[52:55], v[178:181], v[186:189], v[52:55]
	v_mfma_f32_16x16x32_bf16 v[40:43], v[170:173], v[194:197], v[40:43]
	v_mfma_f32_16x16x32_bf16 v[36:39], v[178:181], v[194:197], v[36:39]
	v_mfma_f32_16x16x32_bf16 v[24:27], v[170:173], v[202:205], v[24:27]
	v_mfma_f32_16x16x32_bf16 v[20:23], v[178:181], v[202:205], v[20:23]
	v_mfma_f32_16x16x32_bf16 v[8:11], v[170:173], v[210:213], v[8:11]
	v_mfma_f32_16x16x32_bf16 v[2:5], v[178:181], v[210:213], v[2:5]
	s_barrier
	s_setprio 0
	v_add_u32_e32 v1, 0x18000, v160
	ds_read_b128 v[132:135], v1
	ds_read_b128 v[136:139], v1 offset:1024
	ds_read_b128 v[140:143], v1 offset:2048
	ds_read_b128 v[162:165], v1 offset:3072
	v_add_u32_e32 v1, 0x1c000, v160
	ds_read_b128 v[166:169], v1
	ds_read_b128 v[170:173], v1 offset:1024
	ds_read_b128 v[174:177], v1 offset:2048
	ds_read_b128 v[178:181], v1 offset:3072
	ds_read_b128 v[182:185], v161 offset:32768
	ds_read_b128 v[186:189], v161 offset:33792
	ds_read_b128 v[190:193], v161 offset:34816
	ds_read_b128 v[194:197], v161 offset:35840
	ds_read_b128 v[198:201], v161 offset:36864
	ds_read_b128 v[202:205], v161 offset:37888
	ds_read_b128 v[206:209], v161 offset:38912
	ds_read_b128 v[210:213], v161 offset:39936
	s_add_u32 s26, s44, 0x80000
	s_addc_u32 s27, s45, 0
	s_mov_b32 s44, m0
	s_mov_b32 m0, s53
	s_nop 0
	global_load_lds_dwordx4 v154, s[26:27]
	s_mov_b32 m0, s44
	s_nop 0
	s_mov_b32 s44, m0
	s_mov_b32 m0, s54
	s_nop 0
	global_load_lds_dwordx4 v156, s[26:27]
	s_mov_b32 m0, s44
	s_waitcnt vmcnt(8)
	s_waitcnt lgkmcnt(0)
	s_setprio 1
	s_barrier
	v_mfma_f32_16x16x32_bf16 v[128:131], v[132:135], v[182:185], v[128:131]
	v_mfma_f32_16x16x32_bf16 v[124:127], v[140:143], v[182:185], v[124:127]
	v_mfma_f32_16x16x32_bf16 v[112:115], v[132:135], v[190:193], v[112:115]
	v_mfma_f32_16x16x32_bf16 v[108:111], v[140:143], v[190:193], v[108:111]
	v_mfma_f32_16x16x32_bf16 v[96:99], v[132:135], v[198:201], v[96:99]
	v_mfma_f32_16x16x32_bf16 v[92:95], v[140:143], v[198:201], v[92:95]
	v_mfma_f32_16x16x32_bf16 v[80:83], v[132:135], v[206:209], v[80:83]
	v_mfma_f32_16x16x32_bf16 v[76:79], v[140:143], v[206:209], v[76:79]
	v_mfma_f32_16x16x32_bf16 v[128:131], v[136:139], v[186:189], v[128:131]
	v_mfma_f32_16x16x32_bf16 v[124:127], v[162:165], v[186:189], v[124:127]
	v_mfma_f32_16x16x32_bf16 v[112:115], v[136:139], v[194:197], v[112:115]
	v_mfma_f32_16x16x32_bf16 v[108:111], v[162:165], v[194:197], v[108:111]
	v_mfma_f32_16x16x32_bf16 v[96:99], v[136:139], v[202:205], v[96:99]
	v_mfma_f32_16x16x32_bf16 v[92:95], v[162:165], v[202:205], v[92:95]
	v_mfma_f32_16x16x32_bf16 v[80:83], v[136:139], v[210:213], v[80:83]
	v_mfma_f32_16x16x32_bf16 v[76:79], v[162:165], v[210:213], v[76:79]
	v_mfma_f32_16x16x32_bf16 v[120:123], v[166:169], v[182:185], v[120:123]
	v_mfma_f32_16x16x32_bf16 v[116:119], v[174:177], v[182:185], v[116:119]
	v_mfma_f32_16x16x32_bf16 v[104:107], v[166:169], v[190:193], v[104:107]
	v_mfma_f32_16x16x32_bf16 v[100:103], v[174:177], v[190:193], v[100:103]
	v_mfma_f32_16x16x32_bf16 v[88:91], v[166:169], v[198:201], v[88:91]
	v_mfma_f32_16x16x32_bf16 v[84:87], v[174:177], v[198:201], v[84:87]
	v_mfma_f32_16x16x32_bf16 v[72:75], v[166:169], v[206:209], v[72:75]
	v_mfma_f32_16x16x32_bf16 v[68:71], v[174:177], v[206:209], v[68:71]
	v_mfma_f32_16x16x32_bf16 v[120:123], v[170:173], v[186:189], v[120:123]
	v_mfma_f32_16x16x32_bf16 v[116:119], v[178:181], v[186:189], v[116:119]
	v_mfma_f32_16x16x32_bf16 v[104:107], v[170:173], v[194:197], v[104:107]
	v_mfma_f32_16x16x32_bf16 v[100:103], v[178:181], v[194:197], v[100:103]
	v_mfma_f32_16x16x32_bf16 v[88:91], v[170:173], v[202:205], v[88:91]
	v_mfma_f32_16x16x32_bf16 v[84:87], v[178:181], v[202:205], v[84:87]
	v_mfma_f32_16x16x32_bf16 v[72:75], v[170:173], v[210:213], v[72:75]
	v_mfma_f32_16x16x32_bf16 v[68:71], v[178:181], v[210:213], v[68:71]
	s_barrier
; #define PG8_STAGE(bufoff, gbase, voff) do { _Pragma("unroll") for (int _i = 0; _i < 2; ++_i) { unsigned keep_; \
;         asm volatile("s_mov_b32 %0, m0\n\ts_mov_b32 m0, %3\n\ts_nop 0\n\tglobal_load_lds_dwordx4 %1, %2\n\ts_mov_b32 m0, %0" : "=&s"(keep_) : "v"((voff)[_i]), "s"((const char*)(gbase)), "s"(ldsbase + (unsigned)((bufoff) + _i * 8192)) : "memory"); } } while (0)
; #define PG8_WAIT_V(n) asm volatile("s_waitcnt vmcnt(" #n ")" ::: "memory")
; #define PG8_WAIT_L(n) asm volatile("s_waitcnt lgkmcnt(" #n ")" ::: "memory")
; #define PG8_BAR __builtin_amdgcn_s_barrier()
; #define PG8_SCHED __builtin_amdgcn_sched_barrier(0)
; template <class Epi, class Sched, bool ALIGN_EPI, bool FP8 = false>
; DI void gemm_phase(LAS unsigned char* lds, const Gemm g, const Sched& S, const Epi& E) {
;     ...
;             PG8_LDA(At, 1, 1); PG8_STAGE(PG8_SB(1, 0), b3, voffB); PG8_STAGE(PG8_SB(1, 1), b3 + hstepB, voffB); PG8_STAGE(PG8_SA(1, 0), a3, voffA);
;             PG8_WAIT_V(8); PG8_WAIT_L(0); PG8_BAR; PG8_MMA(1, 0, At, B0); PG8_MMA(1, 1, At, B1); PG8_BAR; PG8_SCHED;
;         }
	s_setprio 0
	ds_read_b128 v[182:185], v161 offset:49152
	ds_read_b128 v[186:189], v161 offset:50176
	ds_read_b128 v[190:193], v161 offset:51200
	ds_read_b128 v[194:197], v161 offset:52224
	ds_read_b128 v[198:201], v161 offset:53248
	ds_read_b128 v[202:205], v161 offset:54272
	ds_read_b128 v[206:209], v161 offset:55296
	ds_read_b128 v[210:213], v161 offset:56320
	s_add_u32 s26, s42, 0x80
	s_addc_u32 s27, s43, 0
	s_mov_b32 s44, m0
	s_mov_b32 m0, s55
	s_nop 0
	global_load_lds_dwordx4 v155, s[26:27]
	s_mov_b32 m0, s44
	s_nop 0
	s_mov_b32 s44, m0
	s_mov_b32 m0, s56
	s_nop 0
	global_load_lds_dwordx4 v157, s[26:27]
	s_mov_b32 m0, s44
	s_add_u32 s26, s42, 0x80080
	s_addc_u32 s27, s43, 0
	s_mov_b32 s42, m0
	s_mov_b32 m0, s59
	s_nop 0
	global_load_lds_dwordx4 v155, s[26:27]
	s_mov_b32 m0, s42
	s_nop 0
	s_mov_b32 s42, m0
	s_mov_b32 m0, s60
	s_nop 0
	global_load_lds_dwordx4 v157, s[26:27]
	s_mov_b32 m0, s42
	s_mov_b32 s26, m0
	s_mov_b32 m0, s57
	s_nop 0
	global_load_lds_dwordx4 v154, s[40:41]
	s_mov_b32 m0, s26
	s_nop 0
	s_mov_b32 s26, m0
	s_mov_b32 m0, s58
	s_nop 0
	global_load_lds_dwordx4 v156, s[40:41]
	s_mov_b32 m0, s26
	s_waitcnt vmcnt(8)
	s_waitcnt lgkmcnt(0)
	s_setprio 1
	s_barrier
	v_mfma_f32_16x16x32_bf16 v[64:67], v[132:135], v[182:185], v[64:67]
	v_mfma_f32_16x16x32_bf16 v[60:63], v[140:143], v[182:185], v[60:63]
	v_mfma_f32_16x16x32_bf16 v[48:51], v[132:135], v[190:193], v[48:51]
	v_mfma_f32_16x16x32_bf16 v[44:47], v[140:143], v[190:193], v[44:47]
	v_mfma_f32_16x16x32_bf16 v[32:35], v[132:135], v[198:201], v[32:35]
	v_mfma_f32_16x16x32_bf16 v[28:31], v[140:143], v[198:201], v[28:31]
	v_mfma_f32_16x16x32_bf16 v[16:19], v[132:135], v[206:209], v[16:19]
	v_mfma_f32_16x16x32_bf16 v[12:15], v[140:143], v[206:209], v[12:15]
	v_mfma_f32_16x16x32_bf16 v[64:67], v[136:139], v[186:189], v[64:67]
	v_mfma_f32_16x16x32_bf16 v[60:63], v[162:165], v[186:189], v[60:63]
	v_mfma_f32_16x16x32_bf16 v[48:51], v[136:139], v[194:197], v[48:51]
	v_mfma_f32_16x16x32_bf16 v[44:47], v[162:165], v[194:197], v[44:47]
	v_mfma_f32_16x16x32_bf16 v[32:35], v[136:139], v[202:205], v[32:35]
	v_mfma_f32_16x16x32_bf16 v[28:31], v[162:165], v[202:205], v[28:31]
	v_mfma_f32_16x16x32_bf16 v[16:19], v[136:139], v[210:213], v[16:19]
	v_mfma_f32_16x16x32_bf16 v[12:15], v[162:165], v[210:213], v[12:15]
	v_mfma_f32_16x16x32_bf16 v[56:59], v[166:169], v[182:185], v[56:59]
	v_mfma_f32_16x16x32_bf16 v[52:55], v[174:177], v[182:185], v[52:55]
	v_mfma_f32_16x16x32_bf16 v[40:43], v[166:169], v[190:193], v[40:43]
	v_mfma_f32_16x16x32_bf16 v[36:39], v[174:177], v[190:193], v[36:39]
	v_mfma_f32_16x16x32_bf16 v[24:27], v[166:169], v[198:201], v[24:27]
	v_mfma_f32_16x16x32_bf16 v[20:23], v[174:177], v[198:201], v[20:23]
	v_mfma_f32_16x16x32_bf16 v[6:9], v[166:169], v[206:209], v[8:11]
	v_mfma_f32_16x16x32_bf16 v[2:5], v[174:177], v[206:209], v[2:5]
	v_mfma_f32_16x16x32_bf16 v[56:59], v[170:173], v[186:189], v[56:59]
	v_mfma_f32_16x16x32_bf16 v[52:55], v[178:181], v[186:189], v[52:55]
	v_mfma_f32_16x16x32_bf16 v[40:43], v[170:173], v[194:197], v[40:43]
	v_mfma_f32_16x16x32_bf16 v[36:39], v[178:181], v[194:197], v[36:39]
	v_mfma_f32_16x16x32_bf16 v[24:27], v[170:173], v[202:205], v[24:27]
	v_mfma_f32_16x16x32_bf16 v[20:23], v[178:181], v[202:205], v[20:23]
	v_mfma_f32_16x16x32_bf16 v[8:11], v[170:173], v[210:213], v[6:9]
	v_mfma_f32_16x16x32_bf16 v[4:7], v[178:181], v[210:213], v[2:5]
	s_barrier
	s_setprio 0
	s_add_i32 s69, s69, 2
	s_add_u32 s67, s67, 0x100
	s_addc_u32 s68, s68, 0
	s_cmp_gt_u32 s69, 29
	s_cbranch_scc1 .LBB0_491
	s_mov_b64 s[26:27], s[28:29]
	s_cmp_lg_u32 s69, 14
	s_cbranch_scc0 .LBB0_488
	s_branch .LBB0_489

; #define PG8_STAGE(bufoff, gbase, voff) do { _Pragma("unroll") for (int _i = 0; _i < 2; ++_i) { unsigned keep_; \
;         asm volatile("s_mov_b32 %0, m0\n\ts_mov_b32 m0, %3\n\ts_nop 0\n\tglobal_load_lds_dwordx4 %1, %2\n\ts_mov_b32 m0, %0" : "=&s"(keep_) : "v"((voff)[_i]), "s"((const char*)(gbase)), "s"(ldsbase + (unsigned)((bufoff) + _i * 8192)) : "memory"); } } while (0)
; #define PG8_WAIT_V(n) asm volatile("s_waitcnt vmcnt(" #n ")" ::: "memory")
; #define PG8_WAIT_L(n) asm volatile("s_waitcnt lgkmcnt(" #n ")" ::: "memory")
; #define PG8_BAR __builtin_amdgcn_s_barrier()
; #define PG8_SCHED __builtin_amdgcn_sched_barrier(0)
;     DI int nt(const Unit& u) const { return (u.aux & 8) ? PLED / 64 : ((u.aux & 4) ? (D_ / 2) / 64 : D_ / 64); }
; template <class Epi, class Sched, bool ALIGN_EPI, bool FP8 = false>
; DI void gemm_phase(LAS unsigned char* lds, const Gemm g, const Sched& S, const Epi& E) {
;     ...
;         for (int t = 0; t < nt; t += 2) {
;             if constexpr (Epi::MID) { if (t == (nt >> 1)) E.mid(acc, cur, wr, wc, fr, fq); }
;             const bool last = (t == nt - 2);
;             const char* a1 = cA + (size_t)(t + 1) * kstep;
;             const char* a2 = last ? nA : cA + (size_t)(t + 2) * kstep; const char* b2 = last ? nB : cB + (size_t)(t + 2) * kstep;
;             const char* a3 = a2 + kstep; const char* b3 = b2 + kstep;
;             PG8_LDB(B0, 0, 0); PG8_LDB(B1, 0, 1); PG8_SCHED; PG8_LDA(At, 0, 0); PG8_STAGE(PG8_SA(1, 1), a1 + hstepA, voffA);
;             PG8_WAIT_V(8); PG8_WAIT_L(0); PG8_BAR; PG8_MMA(0, 0, At, B0); PG8_MMA(0, 1, At, B1); PG8_BAR; PG8_SCHED;
;             PG8_LDA(At, 0, 1); PG8_STAGE(PG8_SB(0, 0), b2, voffB); PG8_STAGE(PG8_SB(0, 1), b2 + hstepB, voffB); PG8_STAGE(PG8_SA(0, 0), a2, voffA);
.LBB0_569:
	ds_read_b128 v[146:149], v140
	ds_read_b128 v[150:153], v140 offset:1024
	ds_read_b128 v[154:157], v140 offset:2048
	ds_read_b128 v[158:161], v140 offset:3072
	ds_read_b128 v[162:165], v141
	ds_read_b128 v[166:169], v141 offset:1024
	ds_read_b128 v[170:173], v141 offset:2048
	ds_read_b128 v[174:177], v141 offset:3072
	s_add_u32 s66, s64, 0x100
	s_addc_u32 s67, s65, 0
	s_cmp_eq_u32 s97, 28
	s_cselect_b32 s72, s93, s66
	s_cselect_b32 s73, s57, s67
	s_cselect_b32 s70, s94, s95
	s_cselect_b32 s71, s55, s96
	s_add_u32 s68, s72, 0x80
	s_addc_u32 s69, s73, 0
	ds_read_b128 v[178:181], v142
	ds_read_b128 v[182:185], v142 offset:1024
	ds_read_b128 v[186:189], v142 offset:2048
	ds_read_b128 v[190:193], v142 offset:3072
	ds_read_b128 v[194:197], v142 offset:4096
	ds_read_b128 v[198:201], v142 offset:5120
	ds_read_b128 v[202:205], v142 offset:6144
	ds_read_b128 v[206:209], v142 offset:7168
	s_add_u32 s64, s64, 0x80080
	s_addc_u32 s65, s65, 0
	s_mov_b32 vcc_lo, m0
	s_mov_b32 m0, s89
	s_nop 0
	global_load_lds_dwordx4 v134, s[64:65]
	s_mov_b32 m0, vcc_lo
	s_nop 0
	s_mov_b32 vcc_lo, m0
	s_mov_b32 m0, s90
	s_nop 0
	global_load_lds_dwordx4 v136, s[64:65]
	s_mov_b32 m0, vcc_lo
	s_waitcnt vmcnt(8)
	s_waitcnt lgkmcnt(0)
	s_setprio 1
	s_barrier
	v_mfma_f32_16x16x32_bf16 v[124:127], v[146:149], v[178:181], v[124:127]
	v_mfma_f32_16x16x32_bf16 v[120:123], v[154:157], v[178:181], v[120:123]
	v_mfma_f32_16x16x32_bf16 v[108:111], v[146:149], v[186:189], v[108:111]
	v_mfma_f32_16x16x32_bf16 v[104:107], v[154:157], v[186:189], v[104:107]
	v_mfma_f32_16x16x32_bf16 v[92:95], v[146:149], v[194:197], v[92:95]
	v_mfma_f32_16x16x32_bf16 v[88:91], v[154:157], v[194:197], v[88:91]
	v_mfma_f32_16x16x32_bf16 v[76:79], v[146:149], v[202:205], v[76:79]
	v_mfma_f32_16x16x32_bf16 v[72:75], v[154:157], v[202:205], v[72:75]
	v_mfma_f32_16x16x32_bf16 v[124:127], v[150:153], v[182:185], v[124:127]
	v_mfma_f32_16x16x32_bf16 v[120:123], v[158:161], v[182:185], v[120:123]
	v_mfma_f32_16x16x32_bf16 v[108:111], v[150:153], v[190:193], v[108:111]
	v_mfma_f32_16x16x32_bf16 v[104:107], v[158:161], v[190:193], v[104:107]
	v_mfma_f32_16x16x32_bf16 v[92:95], v[150:153], v[198:201], v[92:95]
	v_mfma_f32_16x16x32_bf16 v[88:91], v[158:161], v[198:201], v[88:91]
	v_mfma_f32_16x16x32_bf16 v[76:79], v[150:153], v[206:209], v[76:79]
	v_mfma_f32_16x16x32_bf16 v[72:75], v[158:161], v[206:209], v[72:75]
	v_mfma_f32_16x16x32_bf16 v[116:119], v[162:165], v[178:181], v[116:119]
	v_mfma_f32_16x16x32_bf16 v[112:115], v[170:173], v[178:181], v[112:115]
	v_mfma_f32_16x16x32_bf16 v[100:103], v[162:165], v[186:189], v[100:103]
	v_mfma_f32_16x16x32_bf16 v[96:99], v[170:173], v[186:189], v[96:99]
	v_mfma_f32_16x16x32_bf16 v[84:87], v[162:165], v[194:197], v[84:87]
	v_mfma_f32_16x16x32_bf16 v[80:83], v[170:173], v[194:197], v[80:83]
	v_mfma_f32_16x16x32_bf16 v[68:71], v[162:165], v[202:205], v[68:71]
	v_mfma_f32_16x16x32_bf16 v[64:67], v[170:173], v[202:205], v[64:67]
	v_mfma_f32_16x16x32_bf16 v[116:119], v[166:169], v[182:185], v[116:119]
	v_mfma_f32_16x16x32_bf16 v[112:115], v[174:177], v[182:185], v[112:115]
	v_mfma_f32_16x16x32_bf16 v[100:103], v[166:169], v[190:193], v[100:103]
	v_mfma_f32_16x16x32_bf16 v[96:99], v[174:177], v[190:193], v[96:99]
	v_mfma_f32_16x16x32_bf16 v[84:87], v[166:169], v[198:201], v[84:87]
	v_mfma_f32_16x16x32_bf16 v[80:83], v[174:177], v[198:201], v[80:83]
	v_mfma_f32_16x16x32_bf16 v[68:71], v[166:169], v[206:209], v[68:71]
	v_mfma_f32_16x16x32_bf16 v[64:67], v[174:177], v[206:209], v[64:67]
	s_barrier
	s_setprio 0
	ds_read_b128 v[178:181], v142 offset:16384
	ds_read_b128 v[182:185], v142 offset:17408
	ds_read_b128 v[186:189], v142 offset:18432
	ds_read_b128 v[190:193], v142 offset:19456
	ds_read_b128 v[194:197], v142 offset:20480
	ds_read_b128 v[198:201], v142 offset:21504
	ds_read_b128 v[202:205], v142 offset:22528
	ds_read_b128 v[206:209], v142 offset:23552
	s_mov_b32 s64, m0
	s_mov_b32 m0, s63
	s_nop 0
	global_load_lds_dwordx4 v135, s[70:71]
	s_mov_b32 m0, s64
	s_nop 0
	s_mov_b32 s64, m0
	s_mov_b32 m0, s75
	s_nop 0
	global_load_lds_dwordx4 v137, s[70:71]
	s_mov_b32 m0, s64
	s_add_u32 s64, s70, 0x80000
	s_addc_u32 s65, s71, 0
	s_mov_b32 vcc_lo, m0
	s_mov_b32 m0, s77
	s_nop 0
	global_load_lds_dwordx4 v135, s[64:65]
	s_mov_b32 m0, vcc_lo
	s_nop 0
	s_mov_b32 vcc_lo, m0
	s_mov_b32 m0, s79
	s_nop 0
	global_load_lds_dwordx4 v137, s[64:65]
	s_mov_b32 m0, vcc_lo
	s_mov_b32 s64, m0
	s_mov_b32 m0, s74
	s_nop 0
	global_load_lds_dwordx4 v134, s[72:73]
	s_mov_b32 m0, s64
	s_nop 0
	s_mov_b32 s64, m0
	s_mov_b32 m0, s80
	s_nop 0
	global_load_lds_dwordx4 v136, s[72:73]
	s_mov_b32 m0, s64
	s_waitcnt vmcnt(8)
	s_waitcnt lgkmcnt(0)
	s_setprio 1
	s_barrier
; #define PG8_STAGE(bufoff, gbase, voff) do { _Pragma("unroll") for (int _i = 0; _i < 2; ++_i) { unsigned keep_; \
;         asm volatile("s_mov_b32 %0, m0\n\ts_mov_b32 m0, %3\n\ts_nop 0\n\tglobal_load_lds_dwordx4 %1, %2\n\ts_mov_b32 m0, %0" : "=&s"(keep_) : "v"((voff)[_i]), "s"((const char*)(gbase)), "s"(ldsbase + (unsigned)((bufoff) + _i * 8192)) : "memory"); } } while (0)
; #define PG8_WAIT_V(n) asm volatile("s_waitcnt vmcnt(" #n ")" ::: "memory")
; #define PG8_WAIT_L(n) asm volatile("s_waitcnt lgkmcnt(" #n ")" ::: "memory")
; #define PG8_BAR __builtin_amdgcn_s_barrier()
; #define PG8_SCHED __builtin_amdgcn_sched_barrier(0)
; template <class Epi, class Sched, bool ALIGN_EPI, bool FP8 = false>
; DI void gemm_phase(LAS unsigned char* lds, const Gemm g, const Sched& S, const Epi& E) {
;     ...
;             PG8_WAIT_V(8); PG8_WAIT_L(0); PG8_BAR; PG8_MMA(1, 0, At, B0); PG8_MMA(1, 1, At, B1); PG8_BAR; PG8_SCHED;
;             PG8_LDB(B0, 1, 0); PG8_LDB(B1, 1, 1); PG8_SCHED; PG8_LDA(At, 1, 0); PG8_STAGE(PG8_SA(0, 1), a2 + hstepA, voffA);
;             PG8_WAIT_V(8); PG8_WAIT_L(0); PG8_BAR; PG8_MMA(0, 0, At, B0); PG8_MMA(0, 1, At, B1); PG8_BAR; PG8_SCHED;
;             PG8_LDA(At, 1, 1); PG8_STAGE(PG8_SB(1, 0), b3, voffB); PG8_STAGE(PG8_SB(1, 1), b3 + hstepB, voffB); PG8_STAGE(PG8_SA(1, 0), a3, voffA);
	v_mfma_f32_16x16x32_bf16 v[60:63], v[146:149], v[178:181], v[60:63]
	v_mfma_f32_16x16x32_bf16 v[56:59], v[154:157], v[178:181], v[56:59]
	v_mfma_f32_16x16x32_bf16 v[44:47], v[146:149], v[186:189], v[44:47]
	v_mfma_f32_16x16x32_bf16 v[40:43], v[154:157], v[186:189], v[40:43]
	v_mfma_f32_16x16x32_bf16 v[28:31], v[146:149], v[194:197], v[28:31]
	v_mfma_f32_16x16x32_bf16 v[24:27], v[154:157], v[194:197], v[24:27]
	v_mfma_f32_16x16x32_bf16 v[12:15], v[146:149], v[202:205], v[12:15]
	v_mfma_f32_16x16x32_bf16 v[8:11], v[154:157], v[202:205], v[8:11]
	v_mfma_f32_16x16x32_bf16 v[60:63], v[150:153], v[182:185], v[60:63]
	v_mfma_f32_16x16x32_bf16 v[56:59], v[158:161], v[182:185], v[56:59]
	v_mfma_f32_16x16x32_bf16 v[44:47], v[150:153], v[190:193], v[44:47]
	v_mfma_f32_16x16x32_bf16 v[40:43], v[158:161], v[190:193], v[40:43]
	v_mfma_f32_16x16x32_bf16 v[28:31], v[150:153], v[198:201], v[28:31]
	v_mfma_f32_16x16x32_bf16 v[24:27], v[158:161], v[198:201], v[24:27]
	v_mfma_f32_16x16x32_bf16 v[12:15], v[150:153], v[206:209], v[12:15]
	v_mfma_f32_16x16x32_bf16 v[8:11], v[158:161], v[206:209], v[8:11]
	v_mfma_f32_16x16x32_bf16 v[52:55], v[162:165], v[178:181], v[52:55]
	v_mfma_f32_16x16x32_bf16 v[48:51], v[170:173], v[178:181], v[48:51]
	v_mfma_f32_16x16x32_bf16 v[36:39], v[162:165], v[186:189], v[36:39]
	v_mfma_f32_16x16x32_bf16 v[32:35], v[170:173], v[186:189], v[32:35]
	v_mfma_f32_16x16x32_bf16 v[20:23], v[162:165], v[194:197], v[20:23]
	v_mfma_f32_16x16x32_bf16 v[16:19], v[170:173], v[194:197], v[16:19]
	v_mfma_f32_16x16x32_bf16 v[4:7], v[162:165], v[202:205], v[4:7]
	v_mfma_f32_16x16x32_bf16 v[0:3], v[170:173], v[202:205], v[0:3]
	v_mfma_f32_16x16x32_bf16 v[52:55], v[166:169], v[182:185], v[52:55]
	v_mfma_f32_16x16x32_bf16 v[48:51], v[174:177], v[182:185], v[48:51]
	v_mfma_f32_16x16x32_bf16 v[36:39], v[166:169], v[190:193], v[36:39]
	v_mfma_f32_16x16x32_bf16 v[32:35], v[174:177], v[190:193], v[32:35]
	v_mfma_f32_16x16x32_bf16 v[20:23], v[166:169], v[198:201], v[20:23]
	v_mfma_f32_16x16x32_bf16 v[16:19], v[174:177], v[198:201], v[16:19]
	v_mfma_f32_16x16x32_bf16 v[4:7], v[166:169], v[206:209], v[4:7]
	v_mfma_f32_16x16x32_bf16 v[0:3], v[174:177], v[206:209], v[0:3]
	s_barrier
	s_setprio 0
	ds_read_b128 v[146:149], v143
	ds_read_b128 v[150:153], v143 offset:1024
	ds_read_b128 v[154:157], v143 offset:2048
	ds_read_b128 v[158:161], v143 offset:3072
	ds_read_b128 v[162:165], v144
	ds_read_b128 v[166:169], v144 offset:1024
	ds_read_b128 v[170:173], v144 offset:2048
	ds_read_b128 v[174:177], v144 offset:3072
	ds_read_b128 v[178:181], v142 offset:32768
	ds_read_b128 v[182:185], v142 offset:33792
	ds_read_b128 v[186:189], v142 offset:34816
	ds_read_b128 v[190:193], v142 offset:35840
	ds_read_b128 v[194:197], v142 offset:36864
	ds_read_b128 v[198:201], v142 offset:37888
	ds_read_b128 v[202:205], v142 offset:38912
	ds_read_b128 v[206:209], v142 offset:39936
	s_add_u32 s64, s72, 0x80000
	s_addc_u32 s65, s73, 0
	s_mov_b32 s72, m0
	s_mov_b32 m0, s81
	s_nop 0
	global_load_lds_dwordx4 v134, s[64:65]
	s_mov_b32 m0, s72
	s_nop 0
	s_mov_b32 s72, m0
	s_mov_b32 m0, s82
	s_nop 0
	global_load_lds_dwordx4 v136, s[64:65]
	s_mov_b32 m0, s72
	s_waitcnt vmcnt(8)
	s_waitcnt lgkmcnt(0)
	s_setprio 1
	s_barrier
	v_mfma_f32_16x16x32_bf16 v[124:127], v[146:149], v[178:181], v[124:127]
	v_mfma_f32_16x16x32_bf16 v[120:123], v[154:157], v[178:181], v[120:123]
	v_mfma_f32_16x16x32_bf16 v[108:111], v[146:149], v[186:189], v[108:111]
	v_mfma_f32_16x16x32_bf16 v[104:107], v[154:157], v[186:189], v[104:107]
	v_mfma_f32_16x16x32_bf16 v[92:95], v[146:149], v[194:197], v[92:95]
	v_mfma_f32_16x16x32_bf16 v[88:91], v[154:157], v[194:197], v[88:91]
	v_mfma_f32_16x16x32_bf16 v[76:79], v[146:149], v[202:205], v[76:79]
	v_mfma_f32_16x16x32_bf16 v[72:75], v[154:157], v[202:205], v[72:75]
	v_mfma_f32_16x16x32_bf16 v[124:127], v[150:153], v[182:185], v[124:127]
	v_mfma_f32_16x16x32_bf16 v[120:123], v[158:161], v[182:185], v[120:123]
	v_mfma_f32_16x16x32_bf16 v[108:111], v[150:153], v[190:193], v[108:111]
	v_mfma_f32_16x16x32_bf16 v[104:107], v[158:161], v[190:193], v[104:107]
	v_mfma_f32_16x16x32_bf16 v[92:95], v[150:153], v[198:201], v[92:95]
	v_mfma_f32_16x16x32_bf16 v[88:91], v[158:161], v[198:201], v[88:91]
	v_mfma_f32_16x16x32_bf16 v[76:79], v[150:153], v[206:209], v[76:79]
	v_mfma_f32_16x16x32_bf16 v[72:75], v[158:161], v[206:209], v[72:75]
	v_mfma_f32_16x16x32_bf16 v[116:119], v[162:165], v[178:181], v[116:119]
	v_mfma_f32_16x16x32_bf16 v[112:115], v[170:173], v[178:181], v[112:115]
	v_mfma_f32_16x16x32_bf16 v[100:103], v[162:165], v[186:189], v[100:103]
	v_mfma_f32_16x16x32_bf16 v[96:99], v[170:173], v[186:189], v[96:99]
	v_mfma_f32_16x16x32_bf16 v[84:87], v[162:165], v[194:197], v[84:87]
	v_mfma_f32_16x16x32_bf16 v[80:83], v[170:173], v[194:197], v[80:83]
	v_mfma_f32_16x16x32_bf16 v[68:71], v[162:165], v[202:205], v[68:71]
	v_mfma_f32_16x16x32_bf16 v[64:67], v[170:173], v[202:205], v[64:67]
	v_mfma_f32_16x16x32_bf16 v[116:119], v[166:169], v[182:185], v[116:119]
	v_mfma_f32_16x16x32_bf16 v[112:115], v[174:177], v[182:185], v[112:115]
	v_mfma_f32_16x16x32_bf16 v[100:103], v[166:169], v[190:193], v[100:103]
	v_mfma_f32_16x16x32_bf16 v[96:99], v[174:177], v[190:193], v[96:99]
	v_mfma_f32_16x16x32_bf16 v[84:87], v[166:169], v[198:201], v[84:87]
	v_mfma_f32_16x16x32_bf16 v[80:83], v[174:177], v[198:201], v[80:83]
	v_mfma_f32_16x16x32_bf16 v[68:71], v[166:169], v[206:209], v[68:71]
	v_mfma_f32_16x16x32_bf16 v[64:67], v[174:177], v[206:209], v[64:67]
	s_barrier
; #define PG8_STAGE(bufoff, gbase, voff) do { _Pragma("unroll") for (int _i = 0; _i < 2; ++_i) { unsigned keep_; \
;         asm volatile("s_mov_b32 %0, m0\n\ts_mov_b32 m0, %3\n\ts_nop 0\n\tglobal_load_lds_dwordx4 %1, %2\n\ts_mov_b32 m0, %0" : "=&s"(keep_) : "v"((voff)[_i]), "s"((const char*)(gbase)), "s"(ldsbase + (unsigned)((bufoff) + _i * 8192)) : "memory"); } } while (0)
; #define PG8_WAIT_V(n) asm volatile("s_waitcnt vmcnt(" #n ")" ::: "memory")
; #define PG8_WAIT_L(n) asm volatile("s_waitcnt lgkmcnt(" #n ")" ::: "memory")
; #define PG8_BAR __builtin_amdgcn_s_barrier()
; #define PG8_SCHED __builtin_amdgcn_sched_barrier(0)
; template <class Epi, class Sched, bool ALIGN_EPI, bool FP8 = false>
; DI void gemm_phase(LAS unsigned char* lds, const Gemm g, const Sched& S, const Epi& E) {
;     ...
;             PG8_LDA(At, 1, 1); PG8_STAGE(PG8_SB(1, 0), b3, voffB); PG8_STAGE(PG8_SB(1, 1), b3 + hstepB, voffB); PG8_STAGE(PG8_SA(1, 0), a3, voffA);
;             PG8_WAIT_V(8); PG8_WAIT_L(0); PG8_BAR; PG8_MMA(1, 0, At, B0); PG8_MMA(1, 1, At, B1); PG8_BAR; PG8_SCHED;
;         }
	s_setprio 0
	ds_read_b128 v[178:181], v142 offset:49152
	ds_read_b128 v[182:185], v142 offset:50176
	ds_read_b128 v[186:189], v142 offset:51200
	ds_read_b128 v[190:193], v142 offset:52224
	ds_read_b128 v[194:197], v142 offset:53248
	ds_read_b128 v[198:201], v142 offset:54272
	ds_read_b128 v[202:205], v142 offset:55296
	ds_read_b128 v[206:209], v142 offset:56320
	s_add_u32 s64, s70, 0x80
	s_addc_u32 s65, s71, 0
	s_mov_b32 s72, m0
	s_mov_b32 m0, s83
	s_nop 0
	global_load_lds_dwordx4 v135, s[64:65]
	s_mov_b32 m0, s72
	s_nop 0
	s_mov_b32 s72, m0
	s_mov_b32 m0, s84
	s_nop 0
	global_load_lds_dwordx4 v137, s[64:65]
	s_mov_b32 m0, s72
	s_add_u32 s64, s70, 0x80080
	s_addc_u32 s65, s71, 0
	s_mov_b32 s70, m0
	s_mov_b32 m0, s87
	s_nop 0
	global_load_lds_dwordx4 v135, s[64:65]
	s_mov_b32 m0, s70
	s_nop 0
	s_mov_b32 s70, m0
	s_mov_b32 m0, s88
	s_nop 0
	global_load_lds_dwordx4 v137, s[64:65]
	s_mov_b32 m0, s70
	s_mov_b32 s64, m0
	s_mov_b32 m0, s85
	s_nop 0
	global_load_lds_dwordx4 v134, s[68:69]
	s_mov_b32 m0, s64
	s_nop 0
	s_mov_b32 s64, m0
	s_mov_b32 m0, s86
	s_nop 0
	global_load_lds_dwordx4 v136, s[68:69]
	s_mov_b32 m0, s64
	s_waitcnt vmcnt(8)
	s_waitcnt lgkmcnt(0)
	s_setprio 1
	s_barrier
	v_mfma_f32_16x16x32_bf16 v[60:63], v[146:149], v[178:181], v[60:63]
	v_mfma_f32_16x16x32_bf16 v[56:59], v[154:157], v[178:181], v[56:59]
	v_mfma_f32_16x16x32_bf16 v[44:47], v[146:149], v[186:189], v[44:47]
	v_mfma_f32_16x16x32_bf16 v[40:43], v[154:157], v[186:189], v[40:43]
	v_mfma_f32_16x16x32_bf16 v[28:31], v[146:149], v[194:197], v[28:31]
	v_mfma_f32_16x16x32_bf16 v[24:27], v[154:157], v[194:197], v[24:27]
	v_mfma_f32_16x16x32_bf16 v[12:15], v[146:149], v[202:205], v[12:15]
	v_mfma_f32_16x16x32_bf16 v[8:11], v[154:157], v[202:205], v[8:11]
	v_mfma_f32_16x16x32_bf16 v[60:63], v[150:153], v[182:185], v[60:63]
	v_mfma_f32_16x16x32_bf16 v[56:59], v[158:161], v[182:185], v[56:59]
	v_mfma_f32_16x16x32_bf16 v[44:47], v[150:153], v[190:193], v[44:47]
	v_mfma_f32_16x16x32_bf16 v[40:43], v[158:161], v[190:193], v[40:43]
	v_mfma_f32_16x16x32_bf16 v[28:31], v[150:153], v[198:201], v[28:31]
	v_mfma_f32_16x16x32_bf16 v[24:27], v[158:161], v[198:201], v[24:27]
	v_mfma_f32_16x16x32_bf16 v[12:15], v[150:153], v[206:209], v[12:15]
	v_mfma_f32_16x16x32_bf16 v[8:11], v[158:161], v[206:209], v[8:11]
	v_mfma_f32_16x16x32_bf16 v[52:55], v[162:165], v[178:181], v[52:55]
	v_mfma_f32_16x16x32_bf16 v[48:51], v[170:173], v[178:181], v[48:51]
	v_mfma_f32_16x16x32_bf16 v[36:39], v[162:165], v[186:189], v[36:39]
	v_mfma_f32_16x16x32_bf16 v[32:35], v[170:173], v[186:189], v[32:35]
	v_mfma_f32_16x16x32_bf16 v[20:23], v[162:165], v[194:197], v[20:23]
	v_mfma_f32_16x16x32_bf16 v[16:19], v[170:173], v[194:197], v[16:19]
	v_mfma_f32_16x16x32_bf16 v[4:7], v[162:165], v[202:205], v[4:7]
	v_mfma_f32_16x16x32_bf16 v[0:3], v[170:173], v[202:205], v[0:3]
	v_mfma_f32_16x16x32_bf16 v[52:55], v[166:169], v[182:185], v[52:55]
	v_mfma_f32_16x16x32_bf16 v[48:51], v[174:177], v[182:185], v[48:51]
	v_mfma_f32_16x16x32_bf16 v[36:39], v[166:169], v[190:193], v[36:39]
	v_mfma_f32_16x16x32_bf16 v[32:35], v[174:177], v[190:193], v[32:35]
	v_mfma_f32_16x16x32_bf16 v[20:23], v[166:169], v[198:201], v[20:23]
	v_mfma_f32_16x16x32_bf16 v[16:19], v[174:177], v[198:201], v[16:19]
	v_mfma_f32_16x16x32_bf16 v[4:7], v[166:169], v[206:209], v[4:7]
	v_mfma_f32_16x16x32_bf16 v[0:3], v[174:177], v[206:209], v[0:3]
	s_barrier
	s_setprio 0
	s_add_i32 s97, s97, 2
	s_add_u32 s95, s95, 0x100
	s_addc_u32 s96, s96, 0
	s_cmp_gt_u32 s97, 29
	s_mov_b64 s[64:65], s[66:67]
	s_cbranch_scc0 .LBB0_569
	s_and_b64 vcc, exec, s[14:15]
	s_cbranch_vccz .LBB0_572
	s_barrier

; #define PG8_STAGE(bufoff, gbase, voff) do { _Pragma("unroll") for (int _i = 0; _i < 2; ++_i) { unsigned keep_; \
;         asm volatile("s_mov_b32 %0, m0\n\ts_mov_b32 m0, %3\n\ts_nop 0\n\tglobal_load_lds_dwordx4 %1, %2\n\ts_mov_b32 m0, %0" : "=&s"(keep_) : "v"((voff)[_i]), "s"((const char*)(gbase)), "s"(ldsbase + (unsigned)((bufoff) + _i * 8192)) : "memory"); } } while (0)
; #define PG8_WAIT_V(n) asm volatile("s_waitcnt vmcnt(" #n ")" ::: "memory")
; #define PG8_WAIT_L(n) asm volatile("s_waitcnt lgkmcnt(" #n ")" ::: "memory")
; #define PG8_BAR __builtin_amdgcn_s_barrier()
; #define PG8_SCHED __builtin_amdgcn_sched_barrier(0)
;     DI int nt(const Unit& u) const { return (u.aux & 8) ? PLED / 64 : ((u.aux & 4) ? (D_ / 2) / 64 : D_ / 64); }
; template <class Epi, class Sched, bool ALIGN_EPI, bool FP8 = false>
; DI void gemm_phase(LAS unsigned char* lds, const Gemm g, const Sched& S, const Epi& E) {
;     ...
;         for (int t = 0; t < nt; t += 2) {
;             if constexpr (Epi::MID) { if (t == (nt >> 1)) E.mid(acc, cur, wr, wc, fr, fq); }
;             const bool last = (t == nt - 2);
;             const char* a1 = cA + (size_t)(t + 1) * kstep;
;             const char* a2 = last ? nA : cA + (size_t)(t + 2) * kstep; const char* b2 = last ? nB : cB + (size_t)(t + 2) * kstep;
;             const char* a3 = a2 + kstep; const char* b3 = b2 + kstep;
;             PG8_LDB(B0, 0, 0); PG8_LDB(B1, 0, 1); PG8_SCHED; PG8_LDA(At, 0, 0); PG8_STAGE(PG8_SA(1, 1), a1 + hstepA, voffA);
;             PG8_WAIT_V(8); PG8_WAIT_L(0); PG8_BAR; PG8_MMA(0, 0, At, B0); PG8_MMA(0, 1, At, B1); PG8_BAR; PG8_SCHED;
;             PG8_LDA(At, 0, 1); PG8_STAGE(PG8_SB(0, 0), b2, voffB); PG8_STAGE(PG8_SB(0, 1), b2 + hstepB, voffB); PG8_STAGE(PG8_SA(0, 0), a2, voffA);
.LBB0_700:
	ds_read_b128 v[148:151], v142
	ds_read_b128 v[152:155], v142 offset:1024
	ds_read_b128 v[156:159], v142 offset:2048
	ds_read_b128 v[160:163], v142 offset:3072
	ds_read_b128 v[164:167], v143
	ds_read_b128 v[168:171], v143 offset:1024
	ds_read_b128 v[172:175], v143 offset:2048
	ds_read_b128 v[176:179], v143 offset:3072
	s_add_u32 s26, s24, 0x100
	s_addc_u32 s27, s25, 0
	s_cmp_eq_u32 s71, 28
	s_cselect_b32 s42, s67, s26
	s_cselect_b32 s43, s17, s27
	s_cselect_b32 s40, s68, s69
	s_cselect_b32 s41, s13, s70
	s_add_u32 s28, s42, 0x80
	s_addc_u32 s29, s43, 0
	ds_read_b128 v[180:183], v144
	ds_read_b128 v[184:187], v144 offset:1024
	ds_read_b128 v[188:191], v144 offset:2048
	ds_read_b128 v[192:195], v144 offset:3072
	ds_read_b128 v[196:199], v144 offset:4096
	ds_read_b128 v[200:203], v144 offset:5120
	ds_read_b128 v[204:207], v144 offset:6144
	ds_read_b128 v[208:211], v144 offset:7168
	s_add_u32 s24, s24, 0x80080
	s_addc_u32 s25, s25, 0
	s_mov_b32 s72, m0
	s_mov_b32 m0, s61
	s_nop 0
	global_load_lds_dwordx4 v136, s[24:25]
	s_mov_b32 m0, s72
	s_nop 0
	s_mov_b32 s72, m0
	s_mov_b32 m0, s62
	s_nop 0
	global_load_lds_dwordx4 v138, s[24:25]
	s_mov_b32 m0, s72
	s_waitcnt vmcnt(8)
	s_waitcnt lgkmcnt(0)
	s_setprio 1
	s_barrier
	v_mfma_f32_16x16x32_bf16 v[124:127], v[148:151], v[180:183], v[124:127]
	v_mfma_f32_16x16x32_bf16 v[116:119], v[156:159], v[180:183], v[116:119]
	v_mfma_f32_16x16x32_bf16 v[108:111], v[148:151], v[188:191], v[108:111]
	v_mfma_f32_16x16x32_bf16 v[100:103], v[156:159], v[188:191], v[100:103]
	v_mfma_f32_16x16x32_bf16 v[92:95], v[148:151], v[196:199], v[92:95]
	v_mfma_f32_16x16x32_bf16 v[84:87], v[156:159], v[196:199], v[84:87]
	v_mfma_f32_16x16x32_bf16 v[76:79], v[148:151], v[204:207], v[76:79]
	v_mfma_f32_16x16x32_bf16 v[68:71], v[156:159], v[204:207], v[68:71]
	v_mfma_f32_16x16x32_bf16 v[124:127], v[152:155], v[184:187], v[124:127]
	v_mfma_f32_16x16x32_bf16 v[116:119], v[160:163], v[184:187], v[116:119]
	v_mfma_f32_16x16x32_bf16 v[108:111], v[152:155], v[192:195], v[108:111]
	v_mfma_f32_16x16x32_bf16 v[100:103], v[160:163], v[192:195], v[100:103]
	v_mfma_f32_16x16x32_bf16 v[92:95], v[152:155], v[200:203], v[92:95]
	v_mfma_f32_16x16x32_bf16 v[84:87], v[160:163], v[200:203], v[84:87]
	v_mfma_f32_16x16x32_bf16 v[76:79], v[152:155], v[208:211], v[76:79]
	v_mfma_f32_16x16x32_bf16 v[68:71], v[160:163], v[208:211], v[68:71]
	v_mfma_f32_16x16x32_bf16 v[120:123], v[164:167], v[180:183], v[120:123]
	v_mfma_f32_16x16x32_bf16 v[112:115], v[172:175], v[180:183], v[112:115]
	v_mfma_f32_16x16x32_bf16 v[104:107], v[164:167], v[188:191], v[104:107]
	v_mfma_f32_16x16x32_bf16 v[96:99], v[172:175], v[188:191], v[96:99]
	v_mfma_f32_16x16x32_bf16 v[88:91], v[164:167], v[196:199], v[88:91]
	v_mfma_f32_16x16x32_bf16 v[80:83], v[172:175], v[196:199], v[80:83]
	v_mfma_f32_16x16x32_bf16 v[72:75], v[164:167], v[204:207], v[72:75]
	v_mfma_f32_16x16x32_bf16 v[64:67], v[172:175], v[204:207], v[64:67]
	v_mfma_f32_16x16x32_bf16 v[120:123], v[168:171], v[184:187], v[120:123]
	v_mfma_f32_16x16x32_bf16 v[112:115], v[176:179], v[184:187], v[112:115]
	v_mfma_f32_16x16x32_bf16 v[104:107], v[168:171], v[192:195], v[104:107]
	v_mfma_f32_16x16x32_bf16 v[96:99], v[176:179], v[192:195], v[96:99]
	v_mfma_f32_16x16x32_bf16 v[88:91], v[168:171], v[200:203], v[88:91]
	v_mfma_f32_16x16x32_bf16 v[80:83], v[176:179], v[200:203], v[80:83]
	v_mfma_f32_16x16x32_bf16 v[72:75], v[168:171], v[208:211], v[72:75]
	v_mfma_f32_16x16x32_bf16 v[64:67], v[176:179], v[208:211], v[64:67]
	s_barrier
	s_setprio 0
	ds_read_b128 v[180:183], v144 offset:16384
	ds_read_b128 v[184:187], v144 offset:17408
	ds_read_b128 v[188:191], v144 offset:18432
	ds_read_b128 v[192:195], v144 offset:19456
	ds_read_b128 v[196:199], v144 offset:20480
	ds_read_b128 v[200:203], v144 offset:21504
	ds_read_b128 v[204:207], v144 offset:22528
	ds_read_b128 v[208:211], v144 offset:23552
	s_mov_b32 s24, m0
	s_mov_b32 m0, s23
	s_nop 0
	global_load_lds_dwordx4 v137, s[40:41]
	s_mov_b32 m0, s24
	s_nop 0
	s_mov_b32 s24, m0
	s_mov_b32 m0, s47
	s_nop 0
	global_load_lds_dwordx4 v139, s[40:41]
	s_mov_b32 m0, s24
	s_add_u32 s24, s40, 0x80000
	s_addc_u32 s25, s41, 0
	s_mov_b32 s72, m0
	s_mov_b32 m0, s48
	s_nop 0
	global_load_lds_dwordx4 v137, s[24:25]
	s_mov_b32 m0, s72
	s_nop 0
	s_mov_b32 s72, m0
	s_mov_b32 m0, s49
	s_nop 0
	global_load_lds_dwordx4 v139, s[24:25]
	s_mov_b32 m0, s72
	s_mov_b32 s24, m0
	s_mov_b32 m0, s44
	s_nop 0
	global_load_lds_dwordx4 v136, s[42:43]
	s_mov_b32 m0, s24
	s_nop 0
	s_mov_b32 s24, m0
	s_mov_b32 m0, s50
	s_nop 0
	global_load_lds_dwordx4 v138, s[42:43]
	s_mov_b32 m0, s24
	s_waitcnt vmcnt(8)
	s_waitcnt lgkmcnt(0)
	s_setprio 1
	s_barrier
; #define PG8_STAGE(bufoff, gbase, voff) do { _Pragma("unroll") for (int _i = 0; _i < 2; ++_i) { unsigned keep_; \
;         asm volatile("s_mov_b32 %0, m0\n\ts_mov_b32 m0, %3\n\ts_nop 0\n\tglobal_load_lds_dwordx4 %1, %2\n\ts_mov_b32 m0, %0" : "=&s"(keep_) : "v"((voff)[_i]), "s"((const char*)(gbase)), "s"(ldsbase + (unsigned)((bufoff) + _i * 8192)) : "memory"); } } while (0)
; #define PG8_WAIT_V(n) asm volatile("s_waitcnt vmcnt(" #n ")" ::: "memory")
; #define PG8_WAIT_L(n) asm volatile("s_waitcnt lgkmcnt(" #n ")" ::: "memory")
; #define PG8_BAR __builtin_amdgcn_s_barrier()
; #define PG8_SCHED __builtin_amdgcn_sched_barrier(0)
; template <class Epi, class Sched, bool ALIGN_EPI, bool FP8 = false>
; DI void gemm_phase(LAS unsigned char* lds, const Gemm g, const Sched& S, const Epi& E) {
;     ...
;             PG8_WAIT_V(8); PG8_WAIT_L(0); PG8_BAR; PG8_MMA(1, 0, At, B0); PG8_MMA(1, 1, At, B1); PG8_BAR; PG8_SCHED;
;             PG8_LDB(B0, 1, 0); PG8_LDB(B1, 1, 1); PG8_SCHED; PG8_LDA(At, 1, 0); PG8_STAGE(PG8_SA(0, 1), a2 + hstepA, voffA);
;             PG8_WAIT_V(8); PG8_WAIT_L(0); PG8_BAR; PG8_MMA(0, 0, At, B0); PG8_MMA(0, 1, At, B1); PG8_BAR; PG8_SCHED;
;             PG8_LDA(At, 1, 1); PG8_STAGE(PG8_SB(1, 0), b3, voffB); PG8_STAGE(PG8_SB(1, 1), b3 + hstepB, voffB); PG8_STAGE(PG8_SA(1, 0), a3, voffA);
	v_mfma_f32_16x16x32_bf16 v[60:63], v[148:151], v[180:183], v[60:63]
	v_mfma_f32_16x16x32_bf16 v[52:55], v[156:159], v[180:183], v[52:55]
	v_mfma_f32_16x16x32_bf16 v[44:47], v[148:151], v[188:191], v[44:47]
	v_mfma_f32_16x16x32_bf16 v[36:39], v[156:159], v[188:191], v[36:39]
	v_mfma_f32_16x16x32_bf16 v[28:31], v[148:151], v[196:199], v[28:31]
	v_mfma_f32_16x16x32_bf16 v[20:23], v[156:159], v[196:199], v[20:23]
	v_mfma_f32_16x16x32_bf16 v[12:15], v[148:151], v[204:207], v[12:15]
	v_mfma_f32_16x16x32_bf16 v[4:7], v[156:159], v[204:207], v[4:7]
	v_mfma_f32_16x16x32_bf16 v[60:63], v[152:155], v[184:187], v[60:63]
	v_mfma_f32_16x16x32_bf16 v[52:55], v[160:163], v[184:187], v[52:55]
	v_mfma_f32_16x16x32_bf16 v[44:47], v[152:155], v[192:195], v[44:47]
	v_mfma_f32_16x16x32_bf16 v[36:39], v[160:163], v[192:195], v[36:39]
	v_mfma_f32_16x16x32_bf16 v[28:31], v[152:155], v[200:203], v[28:31]
	v_mfma_f32_16x16x32_bf16 v[20:23], v[160:163], v[200:203], v[20:23]
	v_mfma_f32_16x16x32_bf16 v[12:15], v[152:155], v[208:211], v[12:15]
	v_mfma_f32_16x16x32_bf16 v[4:7], v[160:163], v[208:211], v[4:7]
	v_mfma_f32_16x16x32_bf16 v[56:59], v[164:167], v[180:183], v[56:59]
	v_mfma_f32_16x16x32_bf16 v[48:51], v[172:175], v[180:183], v[48:51]
	v_mfma_f32_16x16x32_bf16 v[40:43], v[164:167], v[188:191], v[40:43]
	v_mfma_f32_16x16x32_bf16 v[32:35], v[172:175], v[188:191], v[32:35]
	v_mfma_f32_16x16x32_bf16 v[24:27], v[164:167], v[196:199], v[24:27]
	v_mfma_f32_16x16x32_bf16 v[16:19], v[172:175], v[196:199], v[16:19]
	v_mfma_f32_16x16x32_bf16 v[8:11], v[164:167], v[204:207], v[8:11]
	v_mfma_f32_16x16x32_bf16 v[0:3], v[172:175], v[204:207], v[0:3]
	v_mfma_f32_16x16x32_bf16 v[56:59], v[168:171], v[184:187], v[56:59]
	v_mfma_f32_16x16x32_bf16 v[48:51], v[176:179], v[184:187], v[48:51]
	v_mfma_f32_16x16x32_bf16 v[40:43], v[168:171], v[192:195], v[40:43]
	v_mfma_f32_16x16x32_bf16 v[32:35], v[176:179], v[192:195], v[32:35]
	v_mfma_f32_16x16x32_bf16 v[24:27], v[168:171], v[200:203], v[24:27]
	v_mfma_f32_16x16x32_bf16 v[16:19], v[176:179], v[200:203], v[16:19]
	v_mfma_f32_16x16x32_bf16 v[8:11], v[168:171], v[208:211], v[8:11]
	v_mfma_f32_16x16x32_bf16 v[0:3], v[176:179], v[208:211], v[0:3]
	s_barrier
	s_setprio 0
	ds_read_b128 v[148:151], v145
	ds_read_b128 v[152:155], v145 offset:1024
	ds_read_b128 v[156:159], v145 offset:2048
	ds_read_b128 v[160:163], v145 offset:3072
	ds_read_b128 v[164:167], v146
	ds_read_b128 v[168:171], v146 offset:1024
	ds_read_b128 v[172:175], v146 offset:2048
	ds_read_b128 v[176:179], v146 offset:3072
	ds_read_b128 v[180:183], v144 offset:32768
	ds_read_b128 v[184:187], v144 offset:33792
	ds_read_b128 v[188:191], v144 offset:34816
	ds_read_b128 v[192:195], v144 offset:35840
	ds_read_b128 v[196:199], v144 offset:36864
	ds_read_b128 v[200:203], v144 offset:37888
	ds_read_b128 v[204:207], v144 offset:38912
	ds_read_b128 v[208:211], v144 offset:39936
	s_add_u32 s24, s42, 0x80000
	s_addc_u32 s25, s43, 0
	s_mov_b32 s42, m0
	s_mov_b32 m0, s51
	s_nop 0
	global_load_lds_dwordx4 v136, s[24:25]
	s_mov_b32 m0, s42
	s_nop 0
	s_mov_b32 s42, m0
	s_mov_b32 m0, s52
	s_nop 0
	global_load_lds_dwordx4 v138, s[24:25]
	s_mov_b32 m0, s42
	s_waitcnt vmcnt(8)
	s_waitcnt lgkmcnt(0)
	s_setprio 1
	s_barrier
	v_mfma_f32_16x16x32_bf16 v[124:127], v[148:151], v[180:183], v[124:127]
	v_mfma_f32_16x16x32_bf16 v[116:119], v[156:159], v[180:183], v[116:119]
	v_mfma_f32_16x16x32_bf16 v[108:111], v[148:151], v[188:191], v[108:111]
	v_mfma_f32_16x16x32_bf16 v[100:103], v[156:159], v[188:191], v[100:103]
	v_mfma_f32_16x16x32_bf16 v[92:95], v[148:151], v[196:199], v[92:95]
	v_mfma_f32_16x16x32_bf16 v[84:87], v[156:159], v[196:199], v[84:87]
	v_mfma_f32_16x16x32_bf16 v[76:79], v[148:151], v[204:207], v[76:79]
	v_mfma_f32_16x16x32_bf16 v[68:71], v[156:159], v[204:207], v[68:71]
	v_mfma_f32_16x16x32_bf16 v[124:127], v[152:155], v[184:187], v[124:127]
	v_mfma_f32_16x16x32_bf16 v[116:119], v[160:163], v[184:187], v[116:119]
	v_mfma_f32_16x16x32_bf16 v[108:111], v[152:155], v[192:195], v[108:111]
	v_mfma_f32_16x16x32_bf16 v[100:103], v[160:163], v[192:195], v[100:103]
	v_mfma_f32_16x16x32_bf16 v[92:95], v[152:155], v[200:203], v[92:95]
	v_mfma_f32_16x16x32_bf16 v[84:87], v[160:163], v[200:203], v[84:87]
	v_mfma_f32_16x16x32_bf16 v[76:79], v[152:155], v[208:211], v[76:79]
	v_mfma_f32_16x16x32_bf16 v[68:71], v[160:163], v[208:211], v[68:71]
	v_mfma_f32_16x16x32_bf16 v[120:123], v[164:167], v[180:183], v[120:123]
	v_mfma_f32_16x16x32_bf16 v[112:115], v[172:175], v[180:183], v[112:115]
	v_mfma_f32_16x16x32_bf16 v[104:107], v[164:167], v[188:191], v[104:107]
	v_mfma_f32_16x16x32_bf16 v[96:99], v[172:175], v[188:191], v[96:99]
	v_mfma_f32_16x16x32_bf16 v[88:91], v[164:167], v[196:199], v[88:91]
	v_mfma_f32_16x16x32_bf16 v[80:83], v[172:175], v[196:199], v[80:83]
	v_mfma_f32_16x16x32_bf16 v[72:75], v[164:167], v[204:207], v[72:75]
	v_mfma_f32_16x16x32_bf16 v[64:67], v[172:175], v[204:207], v[64:67]
	v_mfma_f32_16x16x32_bf16 v[120:123], v[168:171], v[184:187], v[120:123]
	v_mfma_f32_16x16x32_bf16 v[112:115], v[176:179], v[184:187], v[112:115]
	v_mfma_f32_16x16x32_bf16 v[104:107], v[168:171], v[192:195], v[104:107]
	v_mfma_f32_16x16x32_bf16 v[96:99], v[176:179], v[192:195], v[96:99]
	v_mfma_f32_16x16x32_bf16 v[88:91], v[168:171], v[200:203], v[88:91]
	v_mfma_f32_16x16x32_bf16 v[80:83], v[176:179], v[200:203], v[80:83]
	v_mfma_f32_16x16x32_bf16 v[72:75], v[168:171], v[208:211], v[72:75]
	v_mfma_f32_16x16x32_bf16 v[64:67], v[176:179], v[208:211], v[64:67]
	s_barrier
; #define PG8_STAGE(bufoff, gbase, voff) do { _Pragma("unroll") for (int _i = 0; _i < 2; ++_i) { unsigned keep_; \
;         asm volatile("s_mov_b32 %0, m0\n\ts_mov_b32 m0, %3\n\ts_nop 0\n\tglobal_load_lds_dwordx4 %1, %2\n\ts_mov_b32 m0, %0" : "=&s"(keep_) : "v"((voff)[_i]), "s"((const char*)(gbase)), "s"(ldsbase + (unsigned)((bufoff) + _i * 8192)) : "memory"); } } while (0)
; #define PG8_WAIT_V(n) asm volatile("s_waitcnt vmcnt(" #n ")" ::: "memory")
; #define PG8_WAIT_L(n) asm volatile("s_waitcnt lgkmcnt(" #n ")" ::: "memory")
; #define PG8_BAR __builtin_amdgcn_s_barrier()
; #define PG8_SCHED __builtin_amdgcn_sched_barrier(0)
; template <class Epi, class Sched, bool ALIGN_EPI, bool FP8 = false>
; DI void gemm_phase(LAS unsigned char* lds, const Gemm g, const Sched& S, const Epi& E) {
;     ...
;             PG8_LDA(At, 1, 1); PG8_STAGE(PG8_SB(1, 0), b3, voffB); PG8_STAGE(PG8_SB(1, 1), b3 + hstepB, voffB); PG8_STAGE(PG8_SA(1, 0), a3, voffA);
;             PG8_WAIT_V(8); PG8_WAIT_L(0); PG8_BAR; PG8_MMA(1, 0, At, B0); PG8_MMA(1, 1, At, B1); PG8_BAR; PG8_SCHED;
;         }
	s_setprio 0
	ds_read_b128 v[180:183], v144 offset:49152
	ds_read_b128 v[184:187], v144 offset:50176
	ds_read_b128 v[188:191], v144 offset:51200
	ds_read_b128 v[192:195], v144 offset:52224
	ds_read_b128 v[196:199], v144 offset:53248
	ds_read_b128 v[200:203], v144 offset:54272
	ds_read_b128 v[204:207], v144 offset:55296
	ds_read_b128 v[208:211], v144 offset:56320
	s_add_u32 s24, s40, 0x80
	s_addc_u32 s25, s41, 0
	s_mov_b32 s42, m0
	s_mov_b32 m0, s55
	s_nop 0
	global_load_lds_dwordx4 v137, s[24:25]
	s_mov_b32 m0, s42
	s_nop 0
	s_mov_b32 s42, m0
	s_mov_b32 m0, s56
	s_nop 0
	global_load_lds_dwordx4 v139, s[24:25]
	s_mov_b32 m0, s42
	s_add_u32 s24, s40, 0x80080
	s_addc_u32 s25, s41, 0
	s_mov_b32 s40, m0
	s_mov_b32 m0, s59
	s_nop 0
	global_load_lds_dwordx4 v137, s[24:25]
	s_mov_b32 m0, s40
	s_nop 0
	s_mov_b32 s40, m0
	s_mov_b32 m0, s60
	s_nop 0
	global_load_lds_dwordx4 v139, s[24:25]
	s_mov_b32 m0, s40
	s_mov_b32 s24, m0
	s_mov_b32 m0, s57
	s_nop 0
	global_load_lds_dwordx4 v136, s[28:29]
	s_mov_b32 m0, s24
	s_nop 0
	s_mov_b32 s24, m0
	s_mov_b32 m0, s58
	s_nop 0
	global_load_lds_dwordx4 v138, s[28:29]
	s_mov_b32 m0, s24
	s_waitcnt vmcnt(8)
	s_waitcnt lgkmcnt(0)
	s_setprio 1
	s_barrier
	v_mfma_f32_16x16x32_bf16 v[60:63], v[148:151], v[180:183], v[60:63]
	v_mfma_f32_16x16x32_bf16 v[52:55], v[156:159], v[180:183], v[52:55]
	v_mfma_f32_16x16x32_bf16 v[44:47], v[148:151], v[188:191], v[44:47]
	v_mfma_f32_16x16x32_bf16 v[36:39], v[156:159], v[188:191], v[36:39]
	v_mfma_f32_16x16x32_bf16 v[28:31], v[148:151], v[196:199], v[28:31]
	v_mfma_f32_16x16x32_bf16 v[20:23], v[156:159], v[196:199], v[20:23]
	v_mfma_f32_16x16x32_bf16 v[12:15], v[148:151], v[204:207], v[12:15]
	v_mfma_f32_16x16x32_bf16 v[4:7], v[156:159], v[204:207], v[4:7]
	v_mfma_f32_16x16x32_bf16 v[60:63], v[152:155], v[184:187], v[60:63]
	v_mfma_f32_16x16x32_bf16 v[52:55], v[160:163], v[184:187], v[52:55]
	v_mfma_f32_16x16x32_bf16 v[44:47], v[152:155], v[192:195], v[44:47]
	v_mfma_f32_16x16x32_bf16 v[36:39], v[160:163], v[192:195], v[36:39]
	v_mfma_f32_16x16x32_bf16 v[28:31], v[152:155], v[200:203], v[28:31]
	v_mfma_f32_16x16x32_bf16 v[20:23], v[160:163], v[200:203], v[20:23]
	v_mfma_f32_16x16x32_bf16 v[12:15], v[152:155], v[208:211], v[12:15]
	v_mfma_f32_16x16x32_bf16 v[4:7], v[160:163], v[208:211], v[4:7]
	v_mfma_f32_16x16x32_bf16 v[56:59], v[164:167], v[180:183], v[56:59]
	v_mfma_f32_16x16x32_bf16 v[48:51], v[172:175], v[180:183], v[48:51]
	v_mfma_f32_16x16x32_bf16 v[40:43], v[164:167], v[188:191], v[40:43]
	v_mfma_f32_16x16x32_bf16 v[32:35], v[172:175], v[188:191], v[32:35]
	v_mfma_f32_16x16x32_bf16 v[24:27], v[164:167], v[196:199], v[24:27]
	v_mfma_f32_16x16x32_bf16 v[16:19], v[172:175], v[196:199], v[16:19]
	v_mfma_f32_16x16x32_bf16 v[8:11], v[164:167], v[204:207], v[8:11]
	v_mfma_f32_16x16x32_bf16 v[0:3], v[172:175], v[204:207], v[0:3]
	v_mfma_f32_16x16x32_bf16 v[56:59], v[168:171], v[184:187], v[56:59]
	v_mfma_f32_16x16x32_bf16 v[48:51], v[176:179], v[184:187], v[48:51]
	v_mfma_f32_16x16x32_bf16 v[40:43], v[168:171], v[192:195], v[40:43]
	v_mfma_f32_16x16x32_bf16 v[32:35], v[176:179], v[192:195], v[32:35]
	v_mfma_f32_16x16x32_bf16 v[24:27], v[168:171], v[200:203], v[24:27]
	v_mfma_f32_16x16x32_bf16 v[16:19], v[176:179], v[200:203], v[16:19]
	v_mfma_f32_16x16x32_bf16 v[8:11], v[168:171], v[208:211], v[8:11]
	v_mfma_f32_16x16x32_bf16 v[0:3], v[176:179], v[208:211], v[0:3]
	s_barrier
	s_setprio 0
	s_add_i32 s71, s71, 2
	s_add_u32 s69, s69, 0x100
	s_addc_u32 s70, s70, 0
	s_cmp_gt_u32 s71, 29
	s_mov_b64 s[24:25], s[26:27]
	s_cbranch_scc0 .LBB0_700
	s_and_b64 vcc, exec, s[10:11]
	s_cbranch_vccz .LBB0_703
	s_barrier

; #define PG8_STAGE(bufoff, gbase, voff) do { _Pragma("unroll") for (int _i = 0; _i < 2; ++_i) { unsigned keep_; \
;         asm volatile("s_mov_b32 %0, m0\n\ts_mov_b32 m0, %3\n\ts_nop 0\n\tglobal_load_lds_dwordx4 %1, %2\n\ts_mov_b32 m0, %0" : "=&s"(keep_) : "v"((voff)[_i]), "s"((const char*)(gbase)), "s"(ldsbase + (unsigned)((bufoff) + _i * 8192)) : "memory"); } } while (0)
; #define PG8_WAIT_V(n) asm volatile("s_waitcnt vmcnt(" #n ")" ::: "memory")
; #define PG8_WAIT_L(n) asm volatile("s_waitcnt lgkmcnt(" #n ")" ::: "memory")
; #define PG8_BAR __builtin_amdgcn_s_barrier()
; #define PG8_SCHED __builtin_amdgcn_sched_barrier(0)
;     DI int nt(const Unit& u) const { return (u.aux & 8) ? PLED / 64 : ((u.aux & 4) ? (D_ / 2) / 64 : D_ / 64); }
; template <class Epi, class Sched, bool ALIGN_EPI, bool FP8 = false>
; DI void gemm_phase(LAS unsigned char* lds, const Gemm g, const Sched& S, const Epi& E) {
;     ...
;         for (int t = 0; t < nt; t += 2) {
;             if constexpr (Epi::MID) { if (t == (nt >> 1)) E.mid(acc, cur, wr, wc, fr, fq); }
;             const bool last = (t == nt - 2);
;             const char* a1 = cA + (size_t)(t + 1) * kstep;
;             const char* a2 = last ? nA : cA + (size_t)(t + 2) * kstep; const char* b2 = last ? nB : cB + (size_t)(t + 2) * kstep;
;             const char* a3 = a2 + kstep; const char* b3 = b2 + kstep;
;             PG8_LDB(B0, 0, 0); PG8_LDB(B1, 0, 1); PG8_SCHED; PG8_LDA(At, 0, 0); PG8_STAGE(PG8_SA(1, 1), a1 + hstepA, voffA);
;             PG8_WAIT_V(8); PG8_WAIT_L(0); PG8_BAR; PG8_MMA(0, 0, At, B0); PG8_MMA(0, 1, At, B1); PG8_BAR; PG8_SCHED;
;             PG8_LDA(At, 0, 1); PG8_STAGE(PG8_SB(0, 0), b2, voffB); PG8_STAGE(PG8_SB(0, 1), b2 + hstepB, voffB); PG8_STAGE(PG8_SA(0, 0), a2, voffA);
.LBB0_724:
	ds_read_b128 v[146:149], v140
	ds_read_b128 v[150:153], v140 offset:1024
	ds_read_b128 v[154:157], v140 offset:2048
	ds_read_b128 v[158:161], v140 offset:3072
	ds_read_b128 v[162:165], v141
	ds_read_b128 v[166:169], v141 offset:1024
	ds_read_b128 v[170:173], v141 offset:2048
	ds_read_b128 v[174:177], v141 offset:3072
	s_add_u32 s66, s64, 0x100
	s_addc_u32 s67, s65, 0
	s_cmp_eq_u32 vcc_lo, 28
	s_cselect_b32 s72, s94, s66
	s_cselect_b32 s73, s57, s67
	s_cselect_b32 s70, s95, s96
	s_cselect_b32 s71, s55, s97
	s_add_u32 s68, s72, 0x80
	s_addc_u32 s69, s73, 0
	ds_read_b128 v[178:181], v142
	ds_read_b128 v[182:185], v142 offset:1024
	ds_read_b128 v[186:189], v142 offset:2048
	ds_read_b128 v[190:193], v142 offset:3072
	ds_read_b128 v[194:197], v142 offset:4096
	ds_read_b128 v[198:201], v142 offset:5120
	ds_read_b128 v[202:205], v142 offset:6144
	ds_read_b128 v[206:209], v142 offset:7168
	s_add_u32 s64, s64, 0x80080
	s_addc_u32 s65, s65, 0
	s_mov_b32 vcc_hi, m0
	s_mov_b32 m0, s90
	s_nop 0
	global_load_lds_dwordx4 v134, s[64:65]
	s_mov_b32 m0, vcc_hi
	s_nop 0
	s_mov_b32 vcc_hi, m0
	s_mov_b32 m0, s91
	s_nop 0
	global_load_lds_dwordx4 v136, s[64:65]
	s_mov_b32 m0, vcc_hi
	s_waitcnt vmcnt(8)
	s_waitcnt lgkmcnt(0)
	s_setprio 1
	s_barrier
	v_mfma_f32_16x16x32_bf16 v[124:127], v[146:149], v[178:181], v[124:127]
	v_mfma_f32_16x16x32_bf16 v[120:123], v[154:157], v[178:181], v[120:123]
	v_mfma_f32_16x16x32_bf16 v[108:111], v[146:149], v[186:189], v[108:111]
	v_mfma_f32_16x16x32_bf16 v[104:107], v[154:157], v[186:189], v[104:107]
	v_mfma_f32_16x16x32_bf16 v[92:95], v[146:149], v[194:197], v[92:95]
	v_mfma_f32_16x16x32_bf16 v[88:91], v[154:157], v[194:197], v[88:91]
	v_mfma_f32_16x16x32_bf16 v[76:79], v[146:149], v[202:205], v[76:79]
	v_mfma_f32_16x16x32_bf16 v[72:75], v[154:157], v[202:205], v[72:75]
	v_mfma_f32_16x16x32_bf16 v[124:127], v[150:153], v[182:185], v[124:127]
	v_mfma_f32_16x16x32_bf16 v[120:123], v[158:161], v[182:185], v[120:123]
	v_mfma_f32_16x16x32_bf16 v[108:111], v[150:153], v[190:193], v[108:111]
	v_mfma_f32_16x16x32_bf16 v[104:107], v[158:161], v[190:193], v[104:107]
	v_mfma_f32_16x16x32_bf16 v[92:95], v[150:153], v[198:201], v[92:95]
	v_mfma_f32_16x16x32_bf16 v[88:91], v[158:161], v[198:201], v[88:91]
	v_mfma_f32_16x16x32_bf16 v[76:79], v[150:153], v[206:209], v[76:79]
	v_mfma_f32_16x16x32_bf16 v[72:75], v[158:161], v[206:209], v[72:75]
	v_mfma_f32_16x16x32_bf16 v[116:119], v[162:165], v[178:181], v[116:119]
	v_mfma_f32_16x16x32_bf16 v[112:115], v[170:173], v[178:181], v[112:115]
	v_mfma_f32_16x16x32_bf16 v[100:103], v[162:165], v[186:189], v[100:103]
	v_mfma_f32_16x16x32_bf16 v[96:99], v[170:173], v[186:189], v[96:99]
	v_mfma_f32_16x16x32_bf16 v[84:87], v[162:165], v[194:197], v[84:87]
	v_mfma_f32_16x16x32_bf16 v[80:83], v[170:173], v[194:197], v[80:83]
	v_mfma_f32_16x16x32_bf16 v[68:71], v[162:165], v[202:205], v[68:71]
	v_mfma_f32_16x16x32_bf16 v[64:67], v[170:173], v[202:205], v[64:67]
	v_mfma_f32_16x16x32_bf16 v[116:119], v[166:169], v[182:185], v[116:119]
	v_mfma_f32_16x16x32_bf16 v[112:115], v[174:177], v[182:185], v[112:115]
	v_mfma_f32_16x16x32_bf16 v[100:103], v[166:169], v[190:193], v[100:103]
	v_mfma_f32_16x16x32_bf16 v[96:99], v[174:177], v[190:193], v[96:99]
	v_mfma_f32_16x16x32_bf16 v[84:87], v[166:169], v[198:201], v[84:87]
	v_mfma_f32_16x16x32_bf16 v[80:83], v[174:177], v[198:201], v[80:83]
	v_mfma_f32_16x16x32_bf16 v[68:71], v[166:169], v[206:209], v[68:71]
	v_mfma_f32_16x16x32_bf16 v[64:67], v[174:177], v[206:209], v[64:67]
	s_barrier
	s_setprio 0
	ds_read_b128 v[178:181], v142 offset:16384
	ds_read_b128 v[182:185], v142 offset:17408
	ds_read_b128 v[186:189], v142 offset:18432
	ds_read_b128 v[190:193], v142 offset:19456
	ds_read_b128 v[194:197], v142 offset:20480
	ds_read_b128 v[198:201], v142 offset:21504
	ds_read_b128 v[202:205], v142 offset:22528
	ds_read_b128 v[206:209], v142 offset:23552
	s_mov_b32 s64, m0
	s_mov_b32 m0, s63
	s_nop 0
	global_load_lds_dwordx4 v135, s[70:71]
	s_mov_b32 m0, s64
	s_nop 0
	s_mov_b32 s64, m0
	s_mov_b32 m0, s77
	s_nop 0
	global_load_lds_dwordx4 v137, s[70:71]
	s_mov_b32 m0, s64
	s_add_u32 s64, s70, 0x80000
	s_addc_u32 s65, s71, 0
	s_mov_b32 vcc_hi, m0
	s_mov_b32 m0, s79
	s_nop 0
	global_load_lds_dwordx4 v135, s[64:65]
	s_mov_b32 m0, vcc_hi
	s_nop 0
	s_mov_b32 vcc_hi, m0
	s_mov_b32 m0, s80
	s_nop 0
	global_load_lds_dwordx4 v137, s[64:65]
	s_mov_b32 m0, vcc_hi
	s_mov_b32 s64, m0
	s_mov_b32 m0, s75
	s_nop 0
	global_load_lds_dwordx4 v134, s[72:73]
	s_mov_b32 m0, s64
	s_nop 0
	s_mov_b32 s64, m0
	s_mov_b32 m0, s81
	s_nop 0
	global_load_lds_dwordx4 v136, s[72:73]
	s_mov_b32 m0, s64
	s_waitcnt vmcnt(8)
	s_waitcnt lgkmcnt(0)
	s_setprio 1
	s_barrier
; #define PG8_STAGE(bufoff, gbase, voff) do { _Pragma("unroll") for (int _i = 0; _i < 2; ++_i) { unsigned keep_; \
;         asm volatile("s_mov_b32 %0, m0\n\ts_mov_b32 m0, %3\n\ts_nop 0\n\tglobal_load_lds_dwordx4 %1, %2\n\ts_mov_b32 m0, %0" : "=&s"(keep_) : "v"((voff)[_i]), "s"((const char*)(gbase)), "s"(ldsbase + (unsigned)((bufoff) + _i * 8192)) : "memory"); } } while (0)
; #define PG8_WAIT_V(n) asm volatile("s_waitcnt vmcnt(" #n ")" ::: "memory")
; #define PG8_WAIT_L(n) asm volatile("s_waitcnt lgkmcnt(" #n ")" ::: "memory")
; #define PG8_BAR __builtin_amdgcn_s_barrier()
; #define PG8_SCHED __builtin_amdgcn_sched_barrier(0)
; template <class Epi, class Sched, bool ALIGN_EPI, bool FP8 = false>
; DI void gemm_phase(LAS unsigned char* lds, const Gemm g, const Sched& S, const Epi& E) {
;     ...
;             PG8_WAIT_V(8); PG8_WAIT_L(0); PG8_BAR; PG8_MMA(1, 0, At, B0); PG8_MMA(1, 1, At, B1); PG8_BAR; PG8_SCHED;
;             PG8_LDB(B0, 1, 0); PG8_LDB(B1, 1, 1); PG8_SCHED; PG8_LDA(At, 1, 0); PG8_STAGE(PG8_SA(0, 1), a2 + hstepA, voffA);
;             PG8_WAIT_V(8); PG8_WAIT_L(0); PG8_BAR; PG8_MMA(0, 0, At, B0); PG8_MMA(0, 1, At, B1); PG8_BAR; PG8_SCHED;
;             PG8_LDA(At, 1, 1); PG8_STAGE(PG8_SB(1, 0), b3, voffB); PG8_STAGE(PG8_SB(1, 1), b3 + hstepB, voffB); PG8_STAGE(PG8_SA(1, 0), a3, voffA);
	v_mfma_f32_16x16x32_bf16 v[60:63], v[146:149], v[178:181], v[60:63]
	v_mfma_f32_16x16x32_bf16 v[56:59], v[154:157], v[178:181], v[56:59]
	v_mfma_f32_16x16x32_bf16 v[44:47], v[146:149], v[186:189], v[44:47]
	v_mfma_f32_16x16x32_bf16 v[40:43], v[154:157], v[186:189], v[40:43]
	v_mfma_f32_16x16x32_bf16 v[28:31], v[146:149], v[194:197], v[28:31]
	v_mfma_f32_16x16x32_bf16 v[24:27], v[154:157], v[194:197], v[24:27]
	v_mfma_f32_16x16x32_bf16 v[12:15], v[146:149], v[202:205], v[12:15]
	v_mfma_f32_16x16x32_bf16 v[8:11], v[154:157], v[202:205], v[8:11]
	v_mfma_f32_16x16x32_bf16 v[60:63], v[150:153], v[182:185], v[60:63]
	v_mfma_f32_16x16x32_bf16 v[56:59], v[158:161], v[182:185], v[56:59]
	v_mfma_f32_16x16x32_bf16 v[44:47], v[150:153], v[190:193], v[44:47]
	v_mfma_f32_16x16x32_bf16 v[40:43], v[158:161], v[190:193], v[40:43]
	v_mfma_f32_16x16x32_bf16 v[28:31], v[150:153], v[198:201], v[28:31]
	v_mfma_f32_16x16x32_bf16 v[24:27], v[158:161], v[198:201], v[24:27]
	v_mfma_f32_16x16x32_bf16 v[12:15], v[150:153], v[206:209], v[12:15]
	v_mfma_f32_16x16x32_bf16 v[8:11], v[158:161], v[206:209], v[8:11]
	v_mfma_f32_16x16x32_bf16 v[52:55], v[162:165], v[178:181], v[52:55]
	v_mfma_f32_16x16x32_bf16 v[48:51], v[170:173], v[178:181], v[48:51]
	v_mfma_f32_16x16x32_bf16 v[36:39], v[162:165], v[186:189], v[36:39]
	v_mfma_f32_16x16x32_bf16 v[32:35], v[170:173], v[186:189], v[32:35]
	v_mfma_f32_16x16x32_bf16 v[20:23], v[162:165], v[194:197], v[20:23]
	v_mfma_f32_16x16x32_bf16 v[16:19], v[170:173], v[194:197], v[16:19]
	v_mfma_f32_16x16x32_bf16 v[4:7], v[162:165], v[202:205], v[4:7]
	v_mfma_f32_16x16x32_bf16 v[0:3], v[170:173], v[202:205], v[0:3]
	v_mfma_f32_16x16x32_bf16 v[52:55], v[166:169], v[182:185], v[52:55]
	v_mfma_f32_16x16x32_bf16 v[48:51], v[174:177], v[182:185], v[48:51]
	v_mfma_f32_16x16x32_bf16 v[36:39], v[166:169], v[190:193], v[36:39]
	v_mfma_f32_16x16x32_bf16 v[32:35], v[174:177], v[190:193], v[32:35]
	v_mfma_f32_16x16x32_bf16 v[20:23], v[166:169], v[198:201], v[20:23]
	v_mfma_f32_16x16x32_bf16 v[16:19], v[174:177], v[198:201], v[16:19]
	v_mfma_f32_16x16x32_bf16 v[4:7], v[166:169], v[206:209], v[4:7]
	v_mfma_f32_16x16x32_bf16 v[0:3], v[174:177], v[206:209], v[0:3]
	s_barrier
	s_setprio 0
	ds_read_b128 v[146:149], v143
	ds_read_b128 v[150:153], v143 offset:1024
	ds_read_b128 v[154:157], v143 offset:2048
	ds_read_b128 v[158:161], v143 offset:3072
	ds_read_b128 v[162:165], v144
	ds_read_b128 v[166:169], v144 offset:1024
	ds_read_b128 v[170:173], v144 offset:2048
	ds_read_b128 v[174:177], v144 offset:3072
	ds_read_b128 v[178:181], v142 offset:32768
	ds_read_b128 v[182:185], v142 offset:33792
	ds_read_b128 v[186:189], v142 offset:34816
	ds_read_b128 v[190:193], v142 offset:35840
	ds_read_b128 v[194:197], v142 offset:36864
	ds_read_b128 v[198:201], v142 offset:37888
	ds_read_b128 v[202:205], v142 offset:38912
	ds_read_b128 v[206:209], v142 offset:39936
	s_add_u32 s64, s72, 0x80000
	s_addc_u32 s65, s73, 0
	s_mov_b32 s72, m0
	s_mov_b32 m0, s82
	s_nop 0
	global_load_lds_dwordx4 v134, s[64:65]
	s_mov_b32 m0, s72
	s_nop 0
	s_mov_b32 s72, m0
	s_mov_b32 m0, s83
	s_nop 0
	global_load_lds_dwordx4 v136, s[64:65]
	s_mov_b32 m0, s72
	s_waitcnt vmcnt(8)
	s_waitcnt lgkmcnt(0)
	s_setprio 1
	s_barrier
	v_mfma_f32_16x16x32_bf16 v[124:127], v[146:149], v[178:181], v[124:127]
	v_mfma_f32_16x16x32_bf16 v[120:123], v[154:157], v[178:181], v[120:123]
	v_mfma_f32_16x16x32_bf16 v[108:111], v[146:149], v[186:189], v[108:111]
	v_mfma_f32_16x16x32_bf16 v[104:107], v[154:157], v[186:189], v[104:107]
	v_mfma_f32_16x16x32_bf16 v[92:95], v[146:149], v[194:197], v[92:95]
	v_mfma_f32_16x16x32_bf16 v[88:91], v[154:157], v[194:197], v[88:91]
	v_mfma_f32_16x16x32_bf16 v[76:79], v[146:149], v[202:205], v[76:79]
	v_mfma_f32_16x16x32_bf16 v[72:75], v[154:157], v[202:205], v[72:75]
	v_mfma_f32_16x16x32_bf16 v[124:127], v[150:153], v[182:185], v[124:127]
	v_mfma_f32_16x16x32_bf16 v[120:123], v[158:161], v[182:185], v[120:123]
	v_mfma_f32_16x16x32_bf16 v[108:111], v[150:153], v[190:193], v[108:111]
	v_mfma_f32_16x16x32_bf16 v[104:107], v[158:161], v[190:193], v[104:107]
	v_mfma_f32_16x16x32_bf16 v[92:95], v[150:153], v[198:201], v[92:95]
	v_mfma_f32_16x16x32_bf16 v[88:91], v[158:161], v[198:201], v[88:91]
	v_mfma_f32_16x16x32_bf16 v[76:79], v[150:153], v[206:209], v[76:79]
	v_mfma_f32_16x16x32_bf16 v[72:75], v[158:161], v[206:209], v[72:75]
	v_mfma_f32_16x16x32_bf16 v[116:119], v[162:165], v[178:181], v[116:119]
	v_mfma_f32_16x16x32_bf16 v[112:115], v[170:173], v[178:181], v[112:115]
	v_mfma_f32_16x16x32_bf16 v[100:103], v[162:165], v[186:189], v[100:103]
	v_mfma_f32_16x16x32_bf16 v[96:99], v[170:173], v[186:189], v[96:99]
	v_mfma_f32_16x16x32_bf16 v[84:87], v[162:165], v[194:197], v[84:87]
	v_mfma_f32_16x16x32_bf16 v[80:83], v[170:173], v[194:197], v[80:83]
	v_mfma_f32_16x16x32_bf16 v[68:71], v[162:165], v[202:205], v[68:71]
	v_mfma_f32_16x16x32_bf16 v[64:67], v[170:173], v[202:205], v[64:67]
	v_mfma_f32_16x16x32_bf16 v[116:119], v[166:169], v[182:185], v[116:119]
	v_mfma_f32_16x16x32_bf16 v[112:115], v[174:177], v[182:185], v[112:115]
	v_mfma_f32_16x16x32_bf16 v[100:103], v[166:169], v[190:193], v[100:103]
	v_mfma_f32_16x16x32_bf16 v[96:99], v[174:177], v[190:193], v[96:99]
	v_mfma_f32_16x16x32_bf16 v[84:87], v[166:169], v[198:201], v[84:87]
	v_mfma_f32_16x16x32_bf16 v[80:83], v[174:177], v[198:201], v[80:83]
	v_mfma_f32_16x16x32_bf16 v[68:71], v[166:169], v[206:209], v[68:71]
	v_mfma_f32_16x16x32_bf16 v[64:67], v[174:177], v[206:209], v[64:67]
	s_barrier
; #define PG8_STAGE(bufoff, gbase, voff) do { _Pragma("unroll") for (int _i = 0; _i < 2; ++_i) { unsigned keep_; \
;         asm volatile("s_mov_b32 %0, m0\n\ts_mov_b32 m0, %3\n\ts_nop 0\n\tglobal_load_lds_dwordx4 %1, %2\n\ts_mov_b32 m0, %0" : "=&s"(keep_) : "v"((voff)[_i]), "s"((const char*)(gbase)), "s"(ldsbase + (unsigned)((bufoff) + _i * 8192)) : "memory"); } } while (0)
; #define PG8_WAIT_V(n) asm volatile("s_waitcnt vmcnt(" #n ")" ::: "memory")
; #define PG8_WAIT_L(n) asm volatile("s_waitcnt lgkmcnt(" #n ")" ::: "memory")
; #define PG8_BAR __builtin_amdgcn_s_barrier()
; #define PG8_SCHED __builtin_amdgcn_sched_barrier(0)
; template <class Epi, class Sched, bool ALIGN_EPI, bool FP8 = false>
; DI void gemm_phase(LAS unsigned char* lds, const Gemm g, const Sched& S, const Epi& E) {
;     ...
;             PG8_LDA(At, 1, 1); PG8_STAGE(PG8_SB(1, 0), b3, voffB); PG8_STAGE(PG8_SB(1, 1), b3 + hstepB, voffB); PG8_STAGE(PG8_SA(1, 0), a3, voffA);
;             PG8_WAIT_V(8); PG8_WAIT_L(0); PG8_BAR; PG8_MMA(1, 0, At, B0); PG8_MMA(1, 1, At, B1); PG8_BAR; PG8_SCHED;
;         }
	s_setprio 0
	ds_read_b128 v[178:181], v142 offset:49152
	ds_read_b128 v[182:185], v142 offset:50176
	ds_read_b128 v[186:189], v142 offset:51200
	ds_read_b128 v[190:193], v142 offset:52224
	ds_read_b128 v[194:197], v142 offset:53248
	ds_read_b128 v[198:201], v142 offset:54272
	ds_read_b128 v[202:205], v142 offset:55296
	ds_read_b128 v[206:209], v142 offset:56320
	s_add_u32 s64, s70, 0x80
	s_addc_u32 s65, s71, 0
	s_mov_b32 s72, m0
	s_mov_b32 m0, s84
	s_nop 0
	global_load_lds_dwordx4 v135, s[64:65]
	s_mov_b32 m0, s72
	s_nop 0
	s_mov_b32 s72, m0
	s_mov_b32 m0, s85
	s_nop 0
	global_load_lds_dwordx4 v137, s[64:65]
	s_mov_b32 m0, s72
	s_add_u32 s64, s70, 0x80080
	s_addc_u32 s65, s71, 0
	s_mov_b32 s70, m0
	s_mov_b32 m0, s88
	s_nop 0
	global_load_lds_dwordx4 v135, s[64:65]
	s_mov_b32 m0, s70
	s_nop 0
	s_mov_b32 s70, m0
	s_mov_b32 m0, s89
	s_nop 0
	global_load_lds_dwordx4 v137, s[64:65]
	s_mov_b32 m0, s70
	s_mov_b32 s64, m0
	s_mov_b32 m0, s86
	s_nop 0
	global_load_lds_dwordx4 v134, s[68:69]
	s_mov_b32 m0, s64
	s_nop 0
	s_mov_b32 s64, m0
	s_mov_b32 m0, s87
	s_nop 0
	global_load_lds_dwordx4 v136, s[68:69]
	s_mov_b32 m0, s64
	s_waitcnt vmcnt(8)
	s_waitcnt lgkmcnt(0)
	s_setprio 1
	s_barrier
	v_mfma_f32_16x16x32_bf16 v[60:63], v[146:149], v[178:181], v[60:63]
	v_mfma_f32_16x16x32_bf16 v[56:59], v[154:157], v[178:181], v[56:59]
	v_mfma_f32_16x16x32_bf16 v[44:47], v[146:149], v[186:189], v[44:47]
	v_mfma_f32_16x16x32_bf16 v[40:43], v[154:157], v[186:189], v[40:43]
	v_mfma_f32_16x16x32_bf16 v[28:31], v[146:149], v[194:197], v[28:31]
	v_mfma_f32_16x16x32_bf16 v[24:27], v[154:157], v[194:197], v[24:27]
	v_mfma_f32_16x16x32_bf16 v[12:15], v[146:149], v[202:205], v[12:15]
	v_mfma_f32_16x16x32_bf16 v[8:11], v[154:157], v[202:205], v[8:11]
	v_mfma_f32_16x16x32_bf16 v[60:63], v[150:153], v[182:185], v[60:63]
	v_mfma_f32_16x16x32_bf16 v[56:59], v[158:161], v[182:185], v[56:59]
	v_mfma_f32_16x16x32_bf16 v[44:47], v[150:153], v[190:193], v[44:47]
	v_mfma_f32_16x16x32_bf16 v[40:43], v[158:161], v[190:193], v[40:43]
	v_mfma_f32_16x16x32_bf16 v[28:31], v[150:153], v[198:201], v[28:31]
	v_mfma_f32_16x16x32_bf16 v[24:27], v[158:161], v[198:201], v[24:27]
	v_mfma_f32_16x16x32_bf16 v[12:15], v[150:153], v[206:209], v[12:15]
	v_mfma_f32_16x16x32_bf16 v[8:11], v[158:161], v[206:209], v[8:11]
	v_mfma_f32_16x16x32_bf16 v[52:55], v[162:165], v[178:181], v[52:55]
	v_mfma_f32_16x16x32_bf16 v[48:51], v[170:173], v[178:181], v[48:51]
	v_mfma_f32_16x16x32_bf16 v[36:39], v[162:165], v[186:189], v[36:39]
	v_mfma_f32_16x16x32_bf16 v[32:35], v[170:173], v[186:189], v[32:35]
	v_mfma_f32_16x16x32_bf16 v[20:23], v[162:165], v[194:197], v[20:23]
	v_mfma_f32_16x16x32_bf16 v[16:19], v[170:173], v[194:197], v[16:19]
	v_mfma_f32_16x16x32_bf16 v[4:7], v[162:165], v[202:205], v[4:7]
	v_mfma_f32_16x16x32_bf16 v[0:3], v[170:173], v[202:205], v[0:3]
	v_mfma_f32_16x16x32_bf16 v[52:55], v[166:169], v[182:185], v[52:55]
	v_mfma_f32_16x16x32_bf16 v[48:51], v[174:177], v[182:185], v[48:51]
	v_mfma_f32_16x16x32_bf16 v[36:39], v[166:169], v[190:193], v[36:39]
	v_mfma_f32_16x16x32_bf16 v[32:35], v[174:177], v[190:193], v[32:35]
	v_mfma_f32_16x16x32_bf16 v[20:23], v[166:169], v[198:201], v[20:23]
	v_mfma_f32_16x16x32_bf16 v[16:19], v[174:177], v[198:201], v[16:19]
	v_mfma_f32_16x16x32_bf16 v[4:7], v[166:169], v[206:209], v[4:7]
	v_mfma_f32_16x16x32_bf16 v[0:3], v[174:177], v[206:209], v[0:3]
	s_barrier
	s_setprio 0
	s_add_i32 vcc_lo, vcc_lo, 2
	s_add_u32 s96, s96, 0x100
	s_addc_u32 s97, s97, 0
	s_cmp_gt_u32 vcc_lo, 29
	s_mov_b64 s[64:65], s[66:67]
	s_cbranch_scc0 .LBB0_724
	s_and_b64 vcc, exec, s[16:17]
	s_cbranch_vccz .LBB0_727
	s_barrier

; #define PG8_STAGE(bufoff, gbase, voff) do { _Pragma("unroll") for (int _i = 0; _i < 2; ++_i) { unsigned keep_; \
;         asm volatile("s_mov_b32 %0, m0\n\ts_mov_b32 m0, %3\n\ts_nop 0\n\tglobal_load_lds_dwordx4 %1, %2\n\ts_mov_b32 m0, %0" : "=&s"(keep_) : "v"((voff)[_i]), "s"((const char*)(gbase)), "s"(ldsbase + (unsigned)((bufoff) + _i * 8192)) : "memory"); } } while (0)
; #define PG8_WAIT_V(n) asm volatile("s_waitcnt vmcnt(" #n ")" ::: "memory")
; #define PG8_WAIT_L(n) asm volatile("s_waitcnt lgkmcnt(" #n ")" ::: "memory")
; #define PG8_BAR __builtin_amdgcn_s_barrier()
; #define PG8_SCHED __builtin_amdgcn_sched_barrier(0)
;     DI int nt(const Unit& u) const { return (u.aux & 8) ? PLED / 64 : ((u.aux & 4) ? (D_ / 2) / 64 : D_ / 64); }
; template <class Epi, class Sched, bool ALIGN_EPI, bool FP8 = false>
; DI void gemm_phase(LAS unsigned char* lds, const Gemm g, const Sched& S, const Epi& E) {
;     ...
;         for (int t = 0; t < nt; t += 2) {
;             if constexpr (Epi::MID) { if (t == (nt >> 1)) E.mid(acc, cur, wr, wc, fr, fq); }
;             const bool last = (t == nt - 2);
;             const char* a1 = cA + (size_t)(t + 1) * kstep;
;             const char* a2 = last ? nA : cA + (size_t)(t + 2) * kstep; const char* b2 = last ? nB : cB + (size_t)(t + 2) * kstep;
;             const char* a3 = a2 + kstep; const char* b3 = b2 + kstep;
;             PG8_LDB(B0, 0, 0); PG8_LDB(B1, 0, 1); PG8_SCHED; PG8_LDA(At, 0, 0); PG8_STAGE(PG8_SA(1, 1), a1 + hstepA, voffA);
;             PG8_WAIT_V(8); PG8_WAIT_L(0); PG8_BAR; PG8_MMA(0, 0, At, B0); PG8_MMA(0, 1, At, B1); PG8_BAR; PG8_SCHED;
;             PG8_LDA(At, 0, 1); PG8_STAGE(PG8_SB(0, 0), b2, voffB); PG8_STAGE(PG8_SB(0, 1), b2 + hstepB, voffB); PG8_STAGE(PG8_SA(0, 0), a2, voffA);
;             PG8_WAIT_V(8); PG8_WAIT_L(0); PG8_BAR; PG8_MMA(1, 0, At, B0); PG8_MMA(1, 1, At, B1); PG8_BAR; PG8_SCHED;
.LBB0_809:
	ds_read_b128 v[144:147], v135
	ds_read_b128 v[148:151], v135 offset:16
	ds_read_b128 v[152:155], v135 offset:2048
	ds_read_b128 v[156:159], v135 offset:2064
	ds_read_b128 v[160:163], v135 offset:16384
	ds_read_b128 v[164:167], v135 offset:16400
	ds_read_b128 v[168:171], v135 offset:18432
	ds_read_b128 v[172:175], v135 offset:18448
	s_add_u32 s50, s48, 0x100
	s_addc_u32 s51, s49, 0
	s_cmp_eq_u32 s83, 40
	s_cselect_b32 s56, s6, s50
	s_cselect_b32 s57, s7, s51
	s_cselect_b32 s54, s46, s81
	s_cselect_b32 s55, s47, s82
	s_add_u32 s52, s56, 0x80
	s_addc_u32 s53, s57, 0
	ds_read_b128 v[176:179], v134
	ds_read_b128 v[180:183], v134 offset:16
	ds_read_b128 v[184:187], v134 offset:2048
	ds_read_b128 v[188:191], v134 offset:2064
	ds_read_b128 v[192:195], v134 offset:4096
	ds_read_b128 v[196:199], v134 offset:4112
	ds_read_b128 v[200:203], v134 offset:6144
	ds_read_b128 v[204:207], v134 offset:6160
	s_add_u32 s48, s48, 0xb0080
	s_addc_u32 s49, s49, 0
	s_mov_b32 s84, m0
	s_mov_b32 m0, s72
	s_nop 0
	global_load_lds_dwordx4 v136, s[48:49]
	s_mov_b32 m0, s84
	s_nop 0
	s_mov_b32 s84, m0
	s_mov_b32 m0, s73
	s_nop 0
	global_load_lds_dwordx4 v138, s[48:49]
	s_mov_b32 m0, s84
	s_waitcnt vmcnt(8)
	s_waitcnt lgkmcnt(0)
	s_setprio 1
	s_barrier
	v_mfma_scale_f32_16x16x128_f8f6f4 v[124:127], v[144:151], v[176:183], v[124:127], v142, v142 op_sel_hi:[0,0,0]
	v_mfma_scale_f32_16x16x128_f8f6f4 v[120:123], v[152:159], v[176:183], v[120:123], v142, v142 op_sel_hi:[0,0,0]
	v_mfma_scale_f32_16x16x128_f8f6f4 v[108:111], v[144:151], v[184:191], v[108:111], v142, v142 op_sel_hi:[0,0,0]
	v_mfma_scale_f32_16x16x128_f8f6f4 v[104:107], v[152:159], v[184:191], v[104:107], v142, v142 op_sel_hi:[0,0,0]
	v_mfma_scale_f32_16x16x128_f8f6f4 v[208:211], v[144:151], v[192:199], v[92:95], v142, v142 op_sel_hi:[0,0,0]
	v_mfma_scale_f32_16x16x128_f8f6f4 v[212:215], v[152:159], v[192:199], v[88:91], v142, v142 op_sel_hi:[0,0,0]
	v_mfma_scale_f32_16x16x128_f8f6f4 v[216:219], v[144:151], v[200:207], v[76:79], v142, v142 op_sel_hi:[0,0,0]
	v_mfma_scale_f32_16x16x128_f8f6f4 v[220:223], v[152:159], v[200:207], v[72:75], v142, v142 op_sel_hi:[0,0,0]
	v_mfma_scale_f32_16x16x128_f8f6f4 v[116:119], v[160:167], v[176:183], v[116:119], v142, v142 op_sel_hi:[0,0,0]
	v_mfma_scale_f32_16x16x128_f8f6f4 v[112:115], v[168:175], v[176:183], v[112:115], v142, v142 op_sel_hi:[0,0,0]
	v_mfma_scale_f32_16x16x128_f8f6f4 v[100:103], v[160:167], v[184:191], v[100:103], v142, v142 op_sel_hi:[0,0,0]
	v_mfma_scale_f32_16x16x128_f8f6f4 v[96:99], v[168:175], v[184:191], v[96:99], v142, v142 op_sel_hi:[0,0,0]
	v_mfma_scale_f32_16x16x128_f8f6f4 v[176:179], v[160:167], v[192:199], v[84:87], v142, v142 op_sel_hi:[0,0,0]
	v_mfma_scale_f32_16x16x128_f8f6f4 v[180:183], v[168:175], v[192:199], v[80:83], v142, v142 op_sel_hi:[0,0,0]
	v_mfma_scale_f32_16x16x128_f8f6f4 v[184:187], v[160:167], v[200:207], v[68:71], v142, v142 op_sel_hi:[0,0,0]
	v_mfma_scale_f32_16x16x128_f8f6f4 v[188:191], v[168:175], v[200:207], v[64:67], v142, v142 op_sel_hi:[0,0,0]
	s_barrier
	s_setprio 0
	s_nop 4
	ds_read_b128 v[64:67], v134 offset:16384
	ds_read_b128 v[68:71], v134 offset:16400
	ds_read_b128 v[72:75], v134 offset:18432
	ds_read_b128 v[76:79], v134 offset:18448
	ds_read_b128 v[80:83], v134 offset:20480
	ds_read_b128 v[84:87], v134 offset:20496
	ds_read_b128 v[88:91], v134 offset:22528
	ds_read_b128 v[92:95], v134 offset:22544
	s_mov_b32 s48, m0
	s_mov_b32 m0, s59
	s_nop 0
	global_load_lds_dwordx4 v137, s[54:55]
	s_mov_b32 m0, s48
	s_nop 0
	s_mov_b32 s48, m0
	s_mov_b32 m0, s60
	s_nop 0
	global_load_lds_dwordx4 v139, s[54:55]
	s_mov_b32 m0, s48
	s_add_u32 s48, s54, 0xb0000
	s_addc_u32 s49, s55, 0
	s_mov_b32 s84, m0
	s_mov_b32 m0, s61
	s_nop 0
	global_load_lds_dwordx4 v137, s[48:49]
	s_mov_b32 m0, s84
	s_nop 0
	s_mov_b32 s84, m0
	s_mov_b32 m0, s62
	s_nop 0
	global_load_lds_dwordx4 v139, s[48:49]
	s_mov_b32 m0, s84
	s_mov_b32 s48, m0
	s_mov_b32 m0, s58
	s_nop 0
	global_load_lds_dwordx4 v136, s[56:57]
	s_mov_b32 m0, s48
	s_nop 0
	s_mov_b32 s48, m0
	s_mov_b32 m0, s63
	s_nop 0
	global_load_lds_dwordx4 v138, s[56:57]
	s_mov_b32 m0, s48
	s_waitcnt vmcnt(8)
	s_waitcnt lgkmcnt(0)
	s_setprio 1
	s_barrier
	v_mfma_scale_f32_16x16x128_f8f6f4 v[60:63], v[144:151], v[64:71], v[60:63], v142, v142 op_sel_hi:[0,0,0]
	v_mfma_scale_f32_16x16x128_f8f6f4 v[56:59], v[152:159], v[64:71], v[56:59], v142, v142 op_sel_hi:[0,0,0]
	v_mfma_scale_f32_16x16x128_f8f6f4 v[192:195], v[144:151], v[72:79], v[44:47], v142, v142 op_sel_hi:[0,0,0]
	v_mfma_scale_f32_16x16x128_f8f6f4 v[196:199], v[152:159], v[72:79], v[40:43], v142, v142 op_sel_hi:[0,0,0]
	v_mfma_scale_f32_16x16x128_f8f6f4 v[200:203], v[144:151], v[80:87], v[28:31], v142, v142 op_sel_hi:[0,0,0]
	v_mfma_scale_f32_16x16x128_f8f6f4 v[204:207], v[152:159], v[80:87], v[24:27], v142, v142 op_sel_hi:[0,0,0]
	v_mfma_scale_f32_16x16x128_f8f6f4 v[224:227], v[144:151], v[88:95], v[12:15], v142, v142 op_sel_hi:[0,0,0]
	v_mfma_scale_f32_16x16x128_f8f6f4 v[228:231], v[152:159], v[88:95], v[8:11], v142, v142 op_sel_hi:[0,0,0]
	v_mfma_scale_f32_16x16x128_f8f6f4 v[52:55], v[160:167], v[64:71], v[52:55], v142, v142 op_sel_hi:[0,0,0]
	v_mfma_scale_f32_16x16x128_f8f6f4 v[48:51], v[168:175], v[64:71], v[48:51], v142, v142 op_sel_hi:[0,0,0]
	v_mfma_scale_f32_16x16x128_f8f6f4 v[232:235], v[160:167], v[72:79], v[36:39], v142, v142 op_sel_hi:[0,0,0]
	v_mfma_scale_f32_16x16x128_f8f6f4 v[236:239], v[168:175], v[72:79], v[32:35], v142, v142 op_sel_hi:[0,0,0]
	v_mfma_scale_f32_16x16x128_f8f6f4 v[240:243], v[160:167], v[80:87], v[20:23], v142, v142 op_sel_hi:[0,0,0]
	v_mfma_scale_f32_16x16x128_f8f6f4 v[244:247], v[168:175], v[80:87], v[16:19], v142, v142 op_sel_hi:[0,0,0]
	v_mfma_scale_f32_16x16x128_f8f6f4 v[248:251], v[160:167], v[88:95], v[4:7], v142, v142 op_sel_hi:[0,0,0]
	v_mfma_scale_f32_16x16x128_f8f6f4 v[128:131], v[168:175], v[88:95], v[0:3], v142, v142 op_sel_hi:[0,0,0]
	s_barrier
; #define PG8_STAGE(bufoff, gbase, voff) do { _Pragma("unroll") for (int _i = 0; _i < 2; ++_i) { unsigned keep_; \
;         asm volatile("s_mov_b32 %0, m0\n\ts_mov_b32 m0, %3\n\ts_nop 0\n\tglobal_load_lds_dwordx4 %1, %2\n\ts_mov_b32 m0, %0" : "=&s"(keep_) : "v"((voff)[_i]), "s"((const char*)(gbase)), "s"(ldsbase + (unsigned)((bufoff) + _i * 8192)) : "memory"); } } while (0)
; #define PG8_WAIT_V(n) asm volatile("s_waitcnt vmcnt(" #n ")" ::: "memory")
; #define PG8_WAIT_L(n) asm volatile("s_waitcnt lgkmcnt(" #n ")" ::: "memory")
; #define PG8_BAR __builtin_amdgcn_s_barrier()
; #define PG8_SCHED __builtin_amdgcn_sched_barrier(0)
; template <class Epi, class Sched, bool ALIGN_EPI, bool FP8 = false>
; DI void gemm_phase(LAS unsigned char* lds, const Gemm g, const Sched& S, const Epi& E) {
;     ...
;             PG8_LDB(B0, 1, 0); PG8_LDB(B1, 1, 1); PG8_SCHED; PG8_LDA(At, 1, 0); PG8_STAGE(PG8_SA(0, 1), a2 + hstepA, voffA);
;             PG8_WAIT_V(8); PG8_WAIT_L(0); PG8_BAR; PG8_MMA(0, 0, At, B0); PG8_MMA(0, 1, At, B1); PG8_BAR; PG8_SCHED;
;             PG8_LDA(At, 1, 1); PG8_STAGE(PG8_SB(1, 0), b3, voffB); PG8_STAGE(PG8_SB(1, 1), b3 + hstepB, voffB); PG8_STAGE(PG8_SA(1, 0), a3, voffA);
;             PG8_WAIT_V(8); PG8_WAIT_L(0); PG8_BAR; PG8_MMA(1, 0, At, B0); PG8_MMA(1, 1, At, B1); PG8_BAR; PG8_SCHED;
;         }
	s_setprio 0
	s_nop 4
	ds_read_b128 v[0:3], v135 offset:32768
	ds_read_b128 v[4:7], v135 offset:32784
	ds_read_b128 v[16:19], v135 offset:34816
	ds_read_b128 v[20:23], v135 offset:34832
	ds_read_b128 v[144:147], v135 offset:49152
	ds_read_b128 v[148:151], v135 offset:49168
	ds_read_b128 v[152:155], v135 offset:51200
	ds_read_b128 v[156:159], v135 offset:51216
	ds_read_b128 v[8:11], v134 offset:32768
	ds_read_b128 v[12:15], v134 offset:32784
	ds_read_b128 v[24:27], v134 offset:34816
	ds_read_b128 v[28:31], v134 offset:34832
	ds_read_b128 v[32:35], v134 offset:36864
	ds_read_b128 v[36:39], v134 offset:36880
	ds_read_b128 v[40:43], v134 offset:38912
	ds_read_b128 v[44:47], v134 offset:38928
	s_add_u32 s48, s56, 0xb0000
	s_addc_u32 s49, s57, 0
	s_mov_b32 s56, m0
	s_mov_b32 m0, s64
	s_nop 0
	global_load_lds_dwordx4 v136, s[48:49]
	s_mov_b32 m0, s56
	s_nop 0
	s_mov_b32 s56, m0
	s_mov_b32 m0, s65
	s_nop 0
	global_load_lds_dwordx4 v138, s[48:49]
	s_mov_b32 m0, s56
	s_waitcnt vmcnt(8)
	s_waitcnt lgkmcnt(0)
	s_setprio 1
	s_barrier
	v_mfma_scale_f32_16x16x128_f8f6f4 v[124:127], v[0:7], v[8:15], v[124:127], v142, v142 op_sel_hi:[0,0,0]
	v_mfma_scale_f32_16x16x128_f8f6f4 v[120:123], v[16:23], v[8:15], v[120:123], v142, v142 op_sel_hi:[0,0,0]
	v_mfma_scale_f32_16x16x128_f8f6f4 v[108:111], v[0:7], v[24:31], v[108:111], v142, v142 op_sel_hi:[0,0,0]
	v_mfma_scale_f32_16x16x128_f8f6f4 v[104:107], v[16:23], v[24:31], v[104:107], v142, v142 op_sel_hi:[0,0,0]
	v_mfma_scale_f32_16x16x128_f8f6f4 v[92:95], v[0:7], v[32:39], v[208:211], v142, v142 op_sel_hi:[0,0,0]
	v_mfma_scale_f32_16x16x128_f8f6f4 v[88:91], v[16:23], v[32:39], v[212:215], v142, v142 op_sel_hi:[0,0,0]
	v_mfma_scale_f32_16x16x128_f8f6f4 v[76:79], v[0:7], v[40:47], v[216:219], v142, v142 op_sel_hi:[0,0,0]
	v_mfma_scale_f32_16x16x128_f8f6f4 v[72:75], v[16:23], v[40:47], v[220:223], v142, v142 op_sel_hi:[0,0,0]
	v_mfma_scale_f32_16x16x128_f8f6f4 v[116:119], v[144:151], v[8:15], v[116:119], v142, v142 op_sel_hi:[0,0,0]
	v_mfma_scale_f32_16x16x128_f8f6f4 v[112:115], v[152:159], v[8:15], v[112:115], v142, v142 op_sel_hi:[0,0,0]
	v_mfma_scale_f32_16x16x128_f8f6f4 v[100:103], v[144:151], v[24:31], v[100:103], v142, v142 op_sel_hi:[0,0,0]
	v_mfma_scale_f32_16x16x128_f8f6f4 v[96:99], v[152:159], v[24:31], v[96:99], v142, v142 op_sel_hi:[0,0,0]
	v_mfma_scale_f32_16x16x128_f8f6f4 v[84:87], v[144:151], v[32:39], v[176:179], v142, v142 op_sel_hi:[0,0,0]
	v_mfma_scale_f32_16x16x128_f8f6f4 v[80:83], v[152:159], v[32:39], v[180:183], v142, v142 op_sel_hi:[0,0,0]
	v_mfma_scale_f32_16x16x128_f8f6f4 v[68:71], v[144:151], v[40:47], v[184:187], v142, v142 op_sel_hi:[0,0,0]
	v_mfma_scale_f32_16x16x128_f8f6f4 v[64:67], v[152:159], v[40:47], v[188:191], v142, v142 op_sel_hi:[0,0,0]
	s_barrier
	s_setprio 0
	ds_read_b128 v[32:35], v134 offset:49152
	ds_read_b128 v[36:39], v134 offset:49168
	ds_read_b128 v[160:163], v134 offset:51200
	ds_read_b128 v[164:167], v134 offset:51216
	ds_read_b128 v[168:171], v134 offset:53248
	ds_read_b128 v[172:175], v134 offset:53264
	ds_read_b128 v[176:179], v134 offset:55296
	ds_read_b128 v[180:183], v134 offset:55312
	s_add_u32 s48, s54, 0x80
	s_addc_u32 s49, s55, 0
	s_mov_b32 s56, m0
	s_mov_b32 m0, s66
	s_nop 0
	global_load_lds_dwordx4 v137, s[48:49]
	s_mov_b32 m0, s56
	s_nop 0
	s_mov_b32 s56, m0
	s_mov_b32 m0, s67
	s_nop 0
	global_load_lds_dwordx4 v139, s[48:49]
	s_mov_b32 m0, s56
	s_add_u32 s48, s54, 0xb0080
	s_addc_u32 s49, s55, 0
	s_mov_b32 s54, m0
	s_mov_b32 m0, s70
	s_nop 0
	global_load_lds_dwordx4 v137, s[48:49]
	s_mov_b32 m0, s54
	s_nop 0
	s_mov_b32 s54, m0
	s_mov_b32 m0, s71
	s_nop 0
	global_load_lds_dwordx4 v139, s[48:49]
	s_mov_b32 m0, s54
	s_mov_b32 s48, m0
	s_mov_b32 m0, s68
	s_nop 0
	global_load_lds_dwordx4 v136, s[52:53]
	s_mov_b32 m0, s48
	s_nop 0
	s_mov_b32 s48, m0
	s_mov_b32 m0, s69
	s_nop 0
	global_load_lds_dwordx4 v138, s[52:53]
	s_mov_b32 m0, s48
	s_waitcnt vmcnt(8)
	s_waitcnt lgkmcnt(0)
	s_setprio 1
	s_barrier
	v_mfma_scale_f32_16x16x128_f8f6f4 v[60:63], v[0:7], v[32:39], v[60:63], v142, v142 op_sel_hi:[0,0,0]
	v_mfma_scale_f32_16x16x128_f8f6f4 v[56:59], v[16:23], v[32:39], v[56:59], v142, v142 op_sel_hi:[0,0,0]
	v_mfma_scale_f32_16x16x128_f8f6f4 v[44:47], v[0:7], v[160:167], v[192:195], v142, v142 op_sel_hi:[0,0,0]
	v_mfma_scale_f32_16x16x128_f8f6f4 v[40:43], v[16:23], v[160:167], v[196:199], v142, v142 op_sel_hi:[0,0,0]
	v_mfma_scale_f32_16x16x128_f8f6f4 v[28:31], v[0:7], v[168:175], v[200:203], v142, v142 op_sel_hi:[0,0,0]
	v_mfma_scale_f32_16x16x128_f8f6f4 v[24:27], v[16:23], v[168:175], v[204:207], v142, v142 op_sel_hi:[0,0,0]
	v_mfma_scale_f32_16x16x128_f8f6f4 v[12:15], v[0:7], v[176:183], v[224:227], v142, v142 op_sel_hi:[0,0,0]
	v_mfma_scale_f32_16x16x128_f8f6f4 v[8:11], v[16:23], v[176:183], v[228:231], v142, v142 op_sel_hi:[0,0,0]
	v_mfma_scale_f32_16x16x128_f8f6f4 v[52:55], v[144:151], v[32:39], v[52:55], v142, v142 op_sel_hi:[0,0,0]
	v_mfma_scale_f32_16x16x128_f8f6f4 v[48:51], v[152:159], v[32:39], v[48:51], v142, v142 op_sel_hi:[0,0,0]
	v_mfma_scale_f32_16x16x128_f8f6f4 v[36:39], v[144:151], v[160:167], v[232:235], v142, v142 op_sel_hi:[0,0,0]
	v_mfma_scale_f32_16x16x128_f8f6f4 v[32:35], v[152:159], v[160:167], v[236:239], v142, v142 op_sel_hi:[0,0,0]
	v_mfma_scale_f32_16x16x128_f8f6f4 v[20:23], v[144:151], v[168:175], v[240:243], v142, v142 op_sel_hi:[0,0,0]
	v_mfma_scale_f32_16x16x128_f8f6f4 v[16:19], v[152:159], v[168:175], v[244:247], v142, v142 op_sel_hi:[0,0,0]
	v_mfma_scale_f32_16x16x128_f8f6f4 v[4:7], v[144:151], v[176:183], v[248:251], v142, v142 op_sel_hi:[0,0,0]
	v_mfma_scale_f32_16x16x128_f8f6f4 v[0:3], v[152:159], v[176:183], v[128:131], v142, v142 op_sel_hi:[0,0,0]
	s_barrier
	s_setprio 0
	s_add_i32 s83, s83, 2
	s_add_u32 s81, s81, 0x100
	s_addc_u32 s82, s82, 0
	s_cmp_gt_u32 s83, 41
	s_mov_b64 s[48:49], s[50:51]
	s_cbranch_scc0 .LBB0_809
	s_and_b64 vcc, exec, s[20:21]
	s_cbranch_vccz .LBB0_812
	s_barrier

; #define PG8_STAGE(bufoff, gbase, voff) do { _Pragma("unroll") for (int _i = 0; _i < 2; ++_i) { unsigned keep_; \
;         asm volatile("s_mov_b32 %0, m0\n\ts_mov_b32 m0, %3\n\ts_nop 0\n\tglobal_load_lds_dwordx4 %1, %2\n\ts_mov_b32 m0, %0" : "=&s"(keep_) : "v"((voff)[_i]), "s"((const char*)(gbase)), "s"(ldsbase + (unsigned)((bufoff) + _i * 8192)) : "memory"); } } while (0)
; #define PG8_WAIT_V(n) asm volatile("s_waitcnt vmcnt(" #n ")" ::: "memory")
; #define PG8_WAIT_L(n) asm volatile("s_waitcnt lgkmcnt(" #n ")" ::: "memory")
; #define PG8_BAR __builtin_amdgcn_s_barrier()
; #define PG8_SCHED __builtin_amdgcn_sched_barrier(0)
;     DI int nt(const Unit& u) const { return (u.aux & 8) ? PLED / 64 : ((u.aux & 4) ? (D_ / 2) / 64 : D_ / 64); }
; template <class Epi, class Sched, bool ALIGN_EPI, bool FP8 = false>
; DI void gemm_phase(LAS unsigned char* lds, const Gemm g, const Sched& S, const Epi& E) {
;     ...
;         for (int t = 0; t < nt; t += 2) {
;             if constexpr (Epi::MID) { if (t == (nt >> 1)) E.mid(acc, cur, wr, wc, fr, fq); }
;             const bool last = (t == nt - 2);
;             const char* a1 = cA + (size_t)(t + 1) * kstep;
;             const char* a2 = last ? nA : cA + (size_t)(t + 2) * kstep; const char* b2 = last ? nB : cB + (size_t)(t + 2) * kstep;
;             const char* a3 = a2 + kstep; const char* b3 = b2 + kstep;
;             PG8_LDB(B0, 0, 0); PG8_LDB(B1, 0, 1); PG8_SCHED; PG8_LDA(At, 0, 0); PG8_STAGE(PG8_SA(1, 1), a1 + hstepA, voffA);
;             PG8_WAIT_V(8); PG8_WAIT_L(0); PG8_BAR; PG8_MMA(0, 0, At, B0); PG8_MMA(0, 1, At, B1); PG8_BAR; PG8_SCHED;
;             PG8_LDA(At, 0, 1); PG8_STAGE(PG8_SB(0, 0), b2, voffB); PG8_STAGE(PG8_SB(0, 1), b2 + hstepB, voffB); PG8_STAGE(PG8_SA(0, 0), a2, voffA);
;             PG8_WAIT_V(8); PG8_WAIT_L(0); PG8_BAR; PG8_MMA(1, 0, At, B0); PG8_MMA(1, 1, At, B1); PG8_BAR; PG8_SCHED;
.LBB0_991:
	s_add_i32 s53, s51, 2
	s_add_u32 s42, s18, s56
	s_addc_u32 s43, s19, s57
	s_add_u32 s58, s42, 0x100
	v_add_u32_e32 v130, 0x10000, v157
	s_addc_u32 s59, s43, 0
	ds_read_b128 v[146:149], v130
	ds_read_b128 v[150:153], v130 offset:1024
	ds_read_b128 v[160:163], v130 offset:2048
	ds_read_b128 v[164:167], v130 offset:3072
	v_add_u32_e32 v130, 0x14000, v157
	s_add_u32 s60, s22, s56
	ds_read_b128 v[168:171], v130
	ds_read_b128 v[172:175], v130 offset:1024
	ds_read_b128 v[176:179], v130 offset:2048
	ds_read_b128 v[180:183], v130 offset:3072
	s_addc_u32 s61, s23, s57
	s_add_u32 s60, s60, 0x100
	s_addc_u32 s61, s61, 0
	s_cmp_eq_u32 s20, s51
	s_cselect_b32 s62, s8, s58
	s_cselect_b32 s63, s9, s59
	s_cselect_b32 s60, s54, s60
	s_cselect_b32 s61, s55, s61
	s_add_u32 s58, s62, 0x80
	s_addc_u32 s59, s63, 0
	ds_read_b128 v[184:187], v158
	ds_read_b128 v[188:191], v158 offset:1024
	ds_read_b128 v[192:195], v158 offset:2048
	ds_read_b128 v[196:199], v158 offset:3072
	ds_read_b128 v[200:203], v158 offset:4096
	ds_read_b128 v[204:207], v158 offset:5120
	ds_read_b128 v[208:211], v158 offset:6144
	ds_read_b128 v[212:215], v158 offset:7168
	s_add_u32 s42, s42, 0x80080
	s_addc_u32 s43, s43, 0
	s_mov_b32 s51, m0
	s_mov_b32 m0, s89
	s_nop 0
	global_load_lds_dwordx4 v129, s[42:43]
	s_mov_b32 m0, s51
	s_nop 0
	s_mov_b32 s51, m0
	s_mov_b32 m0, s90
	s_nop 0
	global_load_lds_dwordx4 v154, s[42:43]
	s_mov_b32 m0, s51
	s_waitcnt vmcnt(8)
	s_waitcnt lgkmcnt(0)
	s_setprio 1
	s_barrier
	v_mfma_f32_16x16x32_bf16 v[124:127], v[146:149], v[184:187], v[124:127]
	v_mfma_f32_16x16x32_bf16 v[120:123], v[160:163], v[184:187], v[120:123]
	v_mfma_f32_16x16x32_bf16 v[116:119], v[146:149], v[192:195], v[116:119]
	v_mfma_f32_16x16x32_bf16 v[112:115], v[160:163], v[192:195], v[112:115]
	v_mfma_f32_16x16x32_bf16 v[108:111], v[146:149], v[200:203], v[108:111]
	v_mfma_f32_16x16x32_bf16 v[104:107], v[160:163], v[200:203], v[104:107]
	v_mfma_f32_16x16x32_bf16 v[100:103], v[146:149], v[208:211], v[100:103]
	v_mfma_f32_16x16x32_bf16 v[96:99], v[160:163], v[208:211], v[96:99]
	v_mfma_f32_16x16x32_bf16 v[124:127], v[150:153], v[188:191], v[124:127]
	v_mfma_f32_16x16x32_bf16 v[120:123], v[164:167], v[188:191], v[120:123]
	v_mfma_f32_16x16x32_bf16 v[116:119], v[150:153], v[196:199], v[116:119]
	v_mfma_f32_16x16x32_bf16 v[112:115], v[164:167], v[196:199], v[112:115]
	v_mfma_f32_16x16x32_bf16 v[108:111], v[150:153], v[204:207], v[108:111]
	v_mfma_f32_16x16x32_bf16 v[104:107], v[164:167], v[204:207], v[104:107]
	v_mfma_f32_16x16x32_bf16 v[100:103], v[150:153], v[212:215], v[100:103]
	v_mfma_f32_16x16x32_bf16 v[96:99], v[164:167], v[212:215], v[96:99]
	v_mfma_f32_16x16x32_bf16 v[92:95], v[168:171], v[184:187], v[92:95]
	v_mfma_f32_16x16x32_bf16 v[88:91], v[176:179], v[184:187], v[88:91]
	v_mfma_f32_16x16x32_bf16 v[84:87], v[168:171], v[192:195], v[84:87]
	v_mfma_f32_16x16x32_bf16 v[80:83], v[176:179], v[192:195], v[80:83]
	v_mfma_f32_16x16x32_bf16 v[76:79], v[168:171], v[200:203], v[76:79]
	v_mfma_f32_16x16x32_bf16 v[72:75], v[176:179], v[200:203], v[72:75]
	v_mfma_f32_16x16x32_bf16 v[68:71], v[168:171], v[208:211], v[68:71]
	v_mfma_f32_16x16x32_bf16 v[64:67], v[176:179], v[208:211], v[64:67]
	v_mfma_f32_16x16x32_bf16 v[92:95], v[172:175], v[188:191], v[92:95]
	v_mfma_f32_16x16x32_bf16 v[88:91], v[180:183], v[188:191], v[88:91]
	v_mfma_f32_16x16x32_bf16 v[84:87], v[172:175], v[196:199], v[84:87]
	v_mfma_f32_16x16x32_bf16 v[80:83], v[180:183], v[196:199], v[80:83]
	v_mfma_f32_16x16x32_bf16 v[76:79], v[172:175], v[204:207], v[76:79]
	v_mfma_f32_16x16x32_bf16 v[72:75], v[180:183], v[204:207], v[72:75]
	v_mfma_f32_16x16x32_bf16 v[68:71], v[172:175], v[212:215], v[68:71]
	v_mfma_f32_16x16x32_bf16 v[64:67], v[180:183], v[212:215], v[64:67]
	s_barrier
	s_setprio 0
	ds_read_b128 v[184:187], v158 offset:16384
	ds_read_b128 v[188:191], v158 offset:17408
	ds_read_b128 v[192:195], v158 offset:18432
	ds_read_b128 v[196:199], v158 offset:19456
	ds_read_b128 v[200:203], v158 offset:20480
	ds_read_b128 v[204:207], v158 offset:21504
	ds_read_b128 v[208:211], v158 offset:22528
	ds_read_b128 v[212:215], v158 offset:23552
	s_mov_b32 s42, m0
	s_mov_b32 m0, s17
	s_nop 0
	global_load_lds_dwordx4 v145, s[60:61]
	s_mov_b32 m0, s42
	s_nop 0
	s_mov_b32 s42, m0
	s_mov_b32 m0, s68
	s_nop 0
	global_load_lds_dwordx4 v155, s[60:61]
	s_mov_b32 m0, s42
	s_add_u32 s42, s60, 0x80000
	s_addc_u32 s43, s61, 0
	s_mov_b32 s51, m0
	s_mov_b32 m0, s69
	s_nop 0
	global_load_lds_dwordx4 v145, s[42:43]
	s_mov_b32 m0, s51
	s_nop 0
	s_mov_b32 s51, m0
	s_mov_b32 m0, s70
	s_nop 0
	global_load_lds_dwordx4 v155, s[42:43]
	s_mov_b32 m0, s51
	s_mov_b32 s42, m0
	s_mov_b32 m0, s15
	s_nop 0
	global_load_lds_dwordx4 v129, s[62:63]
	s_mov_b32 m0, s42
	s_nop 0
	s_mov_b32 s42, m0
	s_mov_b32 m0, s71
	s_nop 0
	global_load_lds_dwordx4 v154, s[62:63]
	s_mov_b32 m0, s42
	s_waitcnt vmcnt(8)
	s_waitcnt lgkmcnt(0)
	s_setprio 1
	s_barrier
; #define PG8_STAGE(bufoff, gbase, voff) do { _Pragma("unroll") for (int _i = 0; _i < 2; ++_i) { unsigned keep_; \
;         asm volatile("s_mov_b32 %0, m0\n\ts_mov_b32 m0, %3\n\ts_nop 0\n\tglobal_load_lds_dwordx4 %1, %2\n\ts_mov_b32 m0, %0" : "=&s"(keep_) : "v"((voff)[_i]), "s"((const char*)(gbase)), "s"(ldsbase + (unsigned)((bufoff) + _i * 8192)) : "memory"); } } while (0)
; #define PG8_WAIT_V(n) asm volatile("s_waitcnt vmcnt(" #n ")" ::: "memory")
; #define PG8_WAIT_L(n) asm volatile("s_waitcnt lgkmcnt(" #n ")" ::: "memory")
; #define PG8_BAR __builtin_amdgcn_s_barrier()
; #define PG8_SCHED __builtin_amdgcn_sched_barrier(0)
; template <class Epi, class Sched, bool ALIGN_EPI, bool FP8 = false>
; DI void gemm_phase(LAS unsigned char* lds, const Gemm g, const Sched& S, const Epi& E) {
;     ...
;             PG8_WAIT_V(8); PG8_WAIT_L(0); PG8_BAR; PG8_MMA(0, 0, At, B0); PG8_MMA(0, 1, At, B1); PG8_BAR; PG8_SCHED;
;             PG8_LDA(At, 0, 1); PG8_STAGE(PG8_SB(0, 0), b2, voffB); PG8_STAGE(PG8_SB(0, 1), b2 + hstepB, voffB); PG8_STAGE(PG8_SA(0, 0), a2, voffA);
;             PG8_WAIT_V(8); PG8_WAIT_L(0); PG8_BAR; PG8_MMA(1, 0, At, B0); PG8_MMA(1, 1, At, B1); PG8_BAR; PG8_SCHED;
;             PG8_LDB(B0, 1, 0); PG8_LDB(B1, 1, 1); PG8_SCHED; PG8_LDA(At, 1, 0); PG8_STAGE(PG8_SA(0, 1), a2 + hstepA, voffA);
;             PG8_WAIT_V(8); PG8_WAIT_L(0); PG8_BAR; PG8_MMA(0, 0, At, B0); PG8_MMA(0, 1, At, B1); PG8_BAR; PG8_SCHED;
	v_mfma_f32_16x16x32_bf16 v[60:63], v[146:149], v[184:187], v[60:63]
	v_mfma_f32_16x16x32_bf16 v[56:59], v[160:163], v[184:187], v[56:59]
	v_mfma_f32_16x16x32_bf16 v[52:55], v[146:149], v[192:195], v[52:55]
	v_mfma_f32_16x16x32_bf16 v[48:51], v[160:163], v[192:195], v[48:51]
	v_mfma_f32_16x16x32_bf16 v[44:47], v[146:149], v[200:203], v[44:47]
	v_mfma_f32_16x16x32_bf16 v[40:43], v[160:163], v[200:203], v[40:43]
	v_mfma_f32_16x16x32_bf16 v[36:39], v[146:149], v[208:211], v[36:39]
	v_mfma_f32_16x16x32_bf16 v[32:35], v[160:163], v[208:211], v[32:35]
	v_mfma_f32_16x16x32_bf16 v[60:63], v[150:153], v[188:191], v[60:63]
	v_mfma_f32_16x16x32_bf16 v[56:59], v[164:167], v[188:191], v[56:59]
	v_mfma_f32_16x16x32_bf16 v[52:55], v[150:153], v[196:199], v[52:55]
	v_mfma_f32_16x16x32_bf16 v[48:51], v[164:167], v[196:199], v[48:51]
	v_mfma_f32_16x16x32_bf16 v[44:47], v[150:153], v[204:207], v[44:47]
	v_mfma_f32_16x16x32_bf16 v[40:43], v[164:167], v[204:207], v[40:43]
	v_mfma_f32_16x16x32_bf16 v[36:39], v[150:153], v[212:215], v[36:39]
	v_mfma_f32_16x16x32_bf16 v[32:35], v[164:167], v[212:215], v[32:35]
	v_mfma_f32_16x16x32_bf16 v[28:31], v[168:171], v[184:187], v[28:31]
	v_mfma_f32_16x16x32_bf16 v[24:27], v[176:179], v[184:187], v[24:27]
	v_mfma_f32_16x16x32_bf16 v[20:23], v[168:171], v[192:195], v[20:23]
	v_mfma_f32_16x16x32_bf16 v[16:19], v[176:179], v[192:195], v[16:19]
	v_mfma_f32_16x16x32_bf16 v[12:15], v[168:171], v[200:203], v[12:15]
	v_mfma_f32_16x16x32_bf16 v[8:11], v[176:179], v[200:203], v[8:11]
	v_mfma_f32_16x16x32_bf16 v[4:7], v[168:171], v[208:211], v[4:7]
	v_mfma_f32_16x16x32_bf16 v[0:3], v[176:179], v[208:211], v[0:3]
	v_mfma_f32_16x16x32_bf16 v[28:31], v[172:175], v[188:191], v[28:31]
	v_mfma_f32_16x16x32_bf16 v[24:27], v[180:183], v[188:191], v[24:27]
	v_mfma_f32_16x16x32_bf16 v[20:23], v[172:175], v[196:199], v[20:23]
	v_mfma_f32_16x16x32_bf16 v[16:19], v[180:183], v[196:199], v[16:19]
	v_mfma_f32_16x16x32_bf16 v[12:15], v[172:175], v[204:207], v[12:15]
	v_mfma_f32_16x16x32_bf16 v[8:11], v[180:183], v[204:207], v[8:11]
	v_mfma_f32_16x16x32_bf16 v[4:7], v[172:175], v[212:215], v[4:7]
	v_mfma_f32_16x16x32_bf16 v[0:3], v[180:183], v[212:215], v[0:3]
	s_barrier
	s_setprio 0
	v_add_u32_e32 v130, 0x18000, v157
	ds_read_b128 v[146:149], v130
	ds_read_b128 v[150:153], v130 offset:1024
	ds_read_b128 v[160:163], v130 offset:2048
	ds_read_b128 v[164:167], v130 offset:3072
	v_add_u32_e32 v130, 0x1c000, v157
	ds_read_b128 v[168:171], v130
	ds_read_b128 v[172:175], v130 offset:1024
	ds_read_b128 v[176:179], v130 offset:2048
	ds_read_b128 v[180:183], v130 offset:3072
	ds_read_b128 v[184:187], v158 offset:32768
	ds_read_b128 v[188:191], v158 offset:33792
	ds_read_b128 v[192:195], v158 offset:34816
	ds_read_b128 v[196:199], v158 offset:35840
	ds_read_b128 v[200:203], v158 offset:36864
	ds_read_b128 v[204:207], v158 offset:37888
	ds_read_b128 v[208:211], v158 offset:38912
	ds_read_b128 v[212:215], v158 offset:39936
	s_add_u32 s42, s62, 0x80000
	s_addc_u32 s43, s63, 0
	s_mov_b32 s51, m0
	s_mov_b32 m0, s72
	s_nop 0
	global_load_lds_dwordx4 v129, s[42:43]
	s_mov_b32 m0, s51
	s_nop 0
	s_mov_b32 s51, m0
	s_mov_b32 m0, s73
	s_nop 0
	global_load_lds_dwordx4 v154, s[42:43]
	s_mov_b32 m0, s51
	s_waitcnt vmcnt(8)
	s_waitcnt lgkmcnt(0)
	s_setprio 1
	s_barrier
	v_mfma_f32_16x16x32_bf16 v[124:127], v[146:149], v[184:187], v[124:127]
	v_mfma_f32_16x16x32_bf16 v[120:123], v[160:163], v[184:187], v[120:123]
	v_mfma_f32_16x16x32_bf16 v[116:119], v[146:149], v[192:195], v[116:119]
	v_mfma_f32_16x16x32_bf16 v[112:115], v[160:163], v[192:195], v[112:115]
	v_mfma_f32_16x16x32_bf16 v[108:111], v[146:149], v[200:203], v[108:111]
	v_mfma_f32_16x16x32_bf16 v[104:107], v[160:163], v[200:203], v[104:107]
	v_mfma_f32_16x16x32_bf16 v[100:103], v[146:149], v[208:211], v[100:103]
	v_mfma_f32_16x16x32_bf16 v[96:99], v[160:163], v[208:211], v[96:99]
	v_mfma_f32_16x16x32_bf16 v[124:127], v[150:153], v[188:191], v[124:127]
	v_mfma_f32_16x16x32_bf16 v[120:123], v[164:167], v[188:191], v[120:123]
	v_mfma_f32_16x16x32_bf16 v[116:119], v[150:153], v[196:199], v[116:119]
	v_mfma_f32_16x16x32_bf16 v[112:115], v[164:167], v[196:199], v[112:115]
	v_mfma_f32_16x16x32_bf16 v[108:111], v[150:153], v[204:207], v[108:111]
	v_mfma_f32_16x16x32_bf16 v[104:107], v[164:167], v[204:207], v[104:107]
	v_mfma_f32_16x16x32_bf16 v[100:103], v[150:153], v[212:215], v[100:103]
	v_mfma_f32_16x16x32_bf16 v[96:99], v[164:167], v[212:215], v[96:99]
	v_mfma_f32_16x16x32_bf16 v[92:95], v[168:171], v[184:187], v[92:95]
	v_mfma_f32_16x16x32_bf16 v[88:91], v[176:179], v[184:187], v[88:91]
	v_mfma_f32_16x16x32_bf16 v[84:87], v[168:171], v[192:195], v[84:87]
	v_mfma_f32_16x16x32_bf16 v[80:83], v[176:179], v[192:195], v[80:83]
	v_mfma_f32_16x16x32_bf16 v[76:79], v[168:171], v[200:203], v[76:79]
	v_mfma_f32_16x16x32_bf16 v[72:75], v[176:179], v[200:203], v[72:75]
	v_mfma_f32_16x16x32_bf16 v[68:71], v[168:171], v[208:211], v[68:71]
	v_mfma_f32_16x16x32_bf16 v[64:67], v[176:179], v[208:211], v[64:67]
	v_mfma_f32_16x16x32_bf16 v[92:95], v[172:175], v[188:191], v[92:95]
	v_mfma_f32_16x16x32_bf16 v[88:91], v[180:183], v[188:191], v[88:91]
	v_mfma_f32_16x16x32_bf16 v[84:87], v[172:175], v[196:199], v[84:87]
	v_mfma_f32_16x16x32_bf16 v[80:83], v[180:183], v[196:199], v[80:83]
	v_mfma_f32_16x16x32_bf16 v[76:79], v[172:175], v[204:207], v[76:79]
	v_mfma_f32_16x16x32_bf16 v[72:75], v[180:183], v[204:207], v[72:75]
	v_mfma_f32_16x16x32_bf16 v[68:71], v[172:175], v[212:215], v[68:71]
	v_mfma_f32_16x16x32_bf16 v[64:67], v[180:183], v[212:215], v[64:67]
	s_barrier
; #define PG8_STAGE(bufoff, gbase, voff) do { _Pragma("unroll") for (int _i = 0; _i < 2; ++_i) { unsigned keep_; \
;         asm volatile("s_mov_b32 %0, m0\n\ts_mov_b32 m0, %3\n\ts_nop 0\n\tglobal_load_lds_dwordx4 %1, %2\n\ts_mov_b32 m0, %0" : "=&s"(keep_) : "v"((voff)[_i]), "s"((const char*)(gbase)), "s"(ldsbase + (unsigned)((bufoff) + _i * 8192)) : "memory"); } } while (0)
; #define PG8_WAIT_V(n) asm volatile("s_waitcnt vmcnt(" #n ")" ::: "memory")
; #define PG8_WAIT_L(n) asm volatile("s_waitcnt lgkmcnt(" #n ")" ::: "memory")
; #define PG8_BAR __builtin_amdgcn_s_barrier()
; #define PG8_SCHED __builtin_amdgcn_sched_barrier(0)
; template <class Epi, class Sched, bool ALIGN_EPI, bool FP8 = false>
; DI void gemm_phase(LAS unsigned char* lds, const Gemm g, const Sched& S, const Epi& E) {
;     ...
;             PG8_LDA(At, 1, 1); PG8_STAGE(PG8_SB(1, 0), b3, voffB); PG8_STAGE(PG8_SB(1, 1), b3 + hstepB, voffB); PG8_STAGE(PG8_SA(1, 0), a3, voffA);
;             PG8_WAIT_V(8); PG8_WAIT_L(0); PG8_BAR; PG8_MMA(1, 0, At, B0); PG8_MMA(1, 1, At, B1); PG8_BAR; PG8_SCHED;
;         }
;         if constexpr (ALIGN_EPI) { if (wr == 0) PG8_BAR; }
;         E(acc, cur, wr, wc, fr, fq);
	s_setprio 0
	ds_read_b128 v[184:187], v158 offset:49152
	ds_read_b128 v[188:191], v158 offset:50176
	ds_read_b128 v[192:195], v158 offset:51200
	ds_read_b128 v[196:199], v158 offset:52224
	ds_read_b128 v[200:203], v158 offset:53248
	ds_read_b128 v[204:207], v158 offset:54272
	ds_read_b128 v[208:211], v158 offset:55296
	ds_read_b128 v[212:215], v158 offset:56320
	s_add_u32 s42, s60, 0x80
	s_addc_u32 s43, s61, 0
	s_mov_b32 s51, m0
	s_mov_b32 m0, s83
	s_nop 0
	global_load_lds_dwordx4 v145, s[42:43]
	s_mov_b32 m0, s51
	s_nop 0
	s_mov_b32 s51, m0
	s_mov_b32 m0, s84
	s_nop 0
	global_load_lds_dwordx4 v155, s[42:43]
	s_mov_b32 m0, s51
	s_add_u32 s42, s60, 0x80080
	s_addc_u32 s43, s61, 0
	s_mov_b32 s51, m0
	s_mov_b32 m0, s87
	s_nop 0
	global_load_lds_dwordx4 v145, s[42:43]
	s_mov_b32 m0, s51
	s_nop 0
	s_mov_b32 s51, m0
	s_mov_b32 m0, s88
	s_nop 0
	global_load_lds_dwordx4 v155, s[42:43]
	s_mov_b32 m0, s51
	s_mov_b32 s42, m0
	s_mov_b32 m0, s85
	s_nop 0
	global_load_lds_dwordx4 v129, s[58:59]
	s_mov_b32 m0, s42
	s_nop 0
	s_mov_b32 s42, m0
	s_mov_b32 m0, s86
	s_nop 0
	global_load_lds_dwordx4 v154, s[58:59]
	s_mov_b32 m0, s42
	s_waitcnt vmcnt(8)
	s_waitcnt lgkmcnt(0)
	s_setprio 1
	s_barrier
	v_mfma_f32_16x16x32_bf16 v[60:63], v[146:149], v[184:187], v[60:63]
	v_mfma_f32_16x16x32_bf16 v[56:59], v[160:163], v[184:187], v[56:59]
	v_mfma_f32_16x16x32_bf16 v[52:55], v[146:149], v[192:195], v[52:55]
	v_mfma_f32_16x16x32_bf16 v[48:51], v[160:163], v[192:195], v[48:51]
	v_mfma_f32_16x16x32_bf16 v[44:47], v[146:149], v[200:203], v[44:47]
	v_mfma_f32_16x16x32_bf16 v[40:43], v[160:163], v[200:203], v[40:43]
	v_mfma_f32_16x16x32_bf16 v[36:39], v[146:149], v[208:211], v[36:39]
	v_mfma_f32_16x16x32_bf16 v[32:35], v[160:163], v[208:211], v[32:35]
	v_mfma_f32_16x16x32_bf16 v[60:63], v[150:153], v[188:191], v[60:63]
	v_mfma_f32_16x16x32_bf16 v[56:59], v[164:167], v[188:191], v[56:59]
	v_mfma_f32_16x16x32_bf16 v[52:55], v[150:153], v[196:199], v[52:55]
	v_mfma_f32_16x16x32_bf16 v[48:51], v[164:167], v[196:199], v[48:51]
	v_mfma_f32_16x16x32_bf16 v[44:47], v[150:153], v[204:207], v[44:47]
	v_mfma_f32_16x16x32_bf16 v[40:43], v[164:167], v[204:207], v[40:43]
	v_mfma_f32_16x16x32_bf16 v[36:39], v[150:153], v[212:215], v[36:39]
	v_mfma_f32_16x16x32_bf16 v[32:35], v[164:167], v[212:215], v[32:35]
	v_mfma_f32_16x16x32_bf16 v[28:31], v[168:171], v[184:187], v[28:31]
	v_mfma_f32_16x16x32_bf16 v[24:27], v[176:179], v[184:187], v[24:27]
	v_mfma_f32_16x16x32_bf16 v[20:23], v[168:171], v[192:195], v[20:23]
	v_mfma_f32_16x16x32_bf16 v[16:19], v[176:179], v[192:195], v[16:19]
	v_mfma_f32_16x16x32_bf16 v[12:15], v[168:171], v[200:203], v[12:15]
	v_mfma_f32_16x16x32_bf16 v[8:11], v[176:179], v[200:203], v[8:11]
	v_mfma_f32_16x16x32_bf16 v[4:7], v[168:171], v[208:211], v[4:7]
	v_mfma_f32_16x16x32_bf16 v[0:3], v[176:179], v[208:211], v[0:3]
	v_mfma_f32_16x16x32_bf16 v[28:31], v[172:175], v[188:191], v[28:31]
	v_mfma_f32_16x16x32_bf16 v[24:27], v[180:183], v[188:191], v[24:27]
	v_mfma_f32_16x16x32_bf16 v[20:23], v[172:175], v[196:199], v[20:23]
	v_mfma_f32_16x16x32_bf16 v[16:19], v[180:183], v[196:199], v[16:19]
	v_mfma_f32_16x16x32_bf16 v[12:15], v[172:175], v[204:207], v[12:15]
	v_mfma_f32_16x16x32_bf16 v[8:11], v[180:183], v[204:207], v[8:11]
	v_mfma_f32_16x16x32_bf16 v[4:7], v[172:175], v[212:215], v[4:7]
	v_mfma_f32_16x16x32_bf16 v[0:3], v[180:183], v[212:215], v[0:3]
	s_barrier
	s_setprio 0
	s_add_u32 s56, s56, 0x100
	s_addc_u32 s57, s57, 0
	s_cmp_ge_u32 s53, s81
	s_mov_b32 s51, s53
	s_cbranch_scc0 .LBB0_991
	s_and_b64 vcc, exec, s[26:27]
	s_cbranch_vccnz .LBB0_1001
	s_bitcmp0_b32 s67, 1
	s_mov_b64 s[56:57], -1
	v_lshl_add_u32 v142, s14, 8, v156
	s_cbranch_scc0 .LBB0_1002

; #define PG8_STAGE(bufoff, gbase, voff) do { _Pragma("unroll") for (int _i = 0; _i < 2; ++_i) { unsigned keep_; \
;         asm volatile("s_mov_b32 %0, m0\n\ts_mov_b32 m0, %3\n\ts_nop 0\n\tglobal_load_lds_dwordx4 %1, %2\n\ts_mov_b32 m0, %0" : "=&s"(keep_) : "v"((voff)[_i]), "s"((const char*)(gbase)), "s"(ldsbase + (unsigned)((bufoff) + _i * 8192)) : "memory"); } } while (0)
; #define PG8_WAIT_V(n) asm volatile("s_waitcnt vmcnt(" #n ")" ::: "memory")
; #define PG8_WAIT_L(n) asm volatile("s_waitcnt lgkmcnt(" #n ")" ::: "memory")
; #define PG8_BAR __builtin_amdgcn_s_barrier()
; #define PG8_SCHED __builtin_amdgcn_sched_barrier(0)
;     DI int nt(const Unit& u) const { return (u.aux & 8) ? PLED / 64 : ((u.aux & 4) ? (D_ / 2) / 64 : D_ / 64); }
; template <class Epi, class Sched, bool ALIGN_EPI, bool FP8 = false>
; DI void gemm_phase(LAS unsigned char* lds, const Gemm g, const Sched& S, const Epi& E) {
;     ...
;         for (int t = 0; t < nt; t += 2) {
;             if constexpr (Epi::MID) { if (t == (nt >> 1)) E.mid(acc, cur, wr, wc, fr, fq); }
;             const bool last = (t == nt - 2);
;             const char* a1 = cA + (size_t)(t + 1) * kstep;
;             const char* a2 = last ? nA : cA + (size_t)(t + 2) * kstep; const char* b2 = last ? nB : cB + (size_t)(t + 2) * kstep;
;             const char* a3 = a2 + kstep; const char* b3 = b2 + kstep;
;             PG8_LDB(B0, 0, 0); PG8_LDB(B1, 0, 1); PG8_SCHED; PG8_LDA(At, 0, 0); PG8_STAGE(PG8_SA(1, 1), a1 + hstepA, voffA);
;             PG8_WAIT_V(8); PG8_WAIT_L(0); PG8_BAR; PG8_MMA(0, 0, At, B0); PG8_MMA(0, 1, At, B1); PG8_BAR; PG8_SCHED;
;             PG8_LDA(At, 0, 1); PG8_STAGE(PG8_SB(0, 0), b2, voffB); PG8_STAGE(PG8_SB(0, 1), b2 + hstepB, voffB); PG8_STAGE(PG8_SA(0, 0), a2, voffA);
;             PG8_WAIT_V(8); PG8_WAIT_L(0); PG8_BAR; PG8_MMA(1, 0, At, B0); PG8_MMA(1, 1, At, B1); PG8_BAR; PG8_SCHED;
;             PG8_LDB(B0, 1, 0); PG8_LDB(B1, 1, 1); PG8_SCHED; PG8_LDA(At, 1, 0); PG8_STAGE(PG8_SA(0, 1), a2 + hstepA, voffA);
;             PG8_WAIT_V(8); PG8_WAIT_L(0); PG8_BAR; PG8_MMA(0, 0, At, B0); PG8_MMA(0, 1, At, B1); PG8_BAR; PG8_SCHED;
.LBB0_1608:
	ds_read_b128 v[144:147], v133
	ds_read_b128 v[148:151], v133 offset:16
	ds_read_b128 v[152:155], v133 offset:2048
	ds_read_b128 v[156:159], v133 offset:2064
	ds_read_b128 v[160:163], v133 offset:16384
	ds_read_b128 v[164:167], v133 offset:16400
	ds_read_b128 v[168:171], v133 offset:18432
	ds_read_b128 v[172:175], v133 offset:18448
	s_add_u32 s6, s26, 0x100
	s_addc_u32 s7, s27, 0
	s_cmp_eq_u32 s70, 12
	s_cselect_b32 s42, s17, s6
	s_cselect_b32 s43, s15, s7
	s_cselect_b32 s40, s18, s68
	s_cselect_b32 s41, s19, s69
	s_add_u32 s28, s42, 0x80
	s_addc_u32 s29, s43, 0
	ds_read_b128 v[176:179], v132
	ds_read_b128 v[180:183], v132 offset:16
	ds_read_b128 v[184:187], v132 offset:2048
	ds_read_b128 v[188:191], v132 offset:2064
	ds_read_b128 v[192:195], v132 offset:4096
	ds_read_b128 v[196:199], v132 offset:4112
	ds_read_b128 v[200:203], v132 offset:6144
	ds_read_b128 v[204:207], v132 offset:6160
	s_add_u32 s26, s26, 0x40080
	s_addc_u32 s27, s27, 0
	s_mov_b32 s71, m0
	s_mov_b32 m0, s62
	s_nop 0
	global_load_lds_dwordx4 v134, s[26:27]
	s_mov_b32 m0, s71
	s_nop 0
	s_mov_b32 s71, m0
	s_mov_b32 m0, s63
	s_nop 0
	global_load_lds_dwordx4 v136, s[26:27]
	s_mov_b32 m0, s71
	s_waitcnt vmcnt(8)
	s_waitcnt lgkmcnt(0)
	s_setprio 1
	s_barrier
	v_mfma_scale_f32_16x16x128_f8f6f4 v[124:127], v[144:151], v[176:183], v[124:127], v140, v140 op_sel_hi:[0,0,0]
	v_mfma_scale_f32_16x16x128_f8f6f4 v[120:123], v[152:159], v[176:183], v[120:123], v140, v140 op_sel_hi:[0,0,0]
	v_mfma_scale_f32_16x16x128_f8f6f4 v[108:111], v[144:151], v[184:191], v[108:111], v140, v140 op_sel_hi:[0,0,0]
	v_mfma_scale_f32_16x16x128_f8f6f4 v[104:107], v[152:159], v[184:191], v[104:107], v140, v140 op_sel_hi:[0,0,0]
	v_mfma_scale_f32_16x16x128_f8f6f4 v[208:211], v[144:151], v[192:199], v[92:95], v140, v140 op_sel_hi:[0,0,0]
	v_mfma_scale_f32_16x16x128_f8f6f4 v[212:215], v[152:159], v[192:199], v[88:91], v140, v140 op_sel_hi:[0,0,0]
	v_mfma_scale_f32_16x16x128_f8f6f4 v[216:219], v[144:151], v[200:207], v[76:79], v140, v140 op_sel_hi:[0,0,0]
	v_mfma_scale_f32_16x16x128_f8f6f4 v[220:223], v[152:159], v[200:207], v[72:75], v140, v140 op_sel_hi:[0,0,0]
	v_mfma_scale_f32_16x16x128_f8f6f4 v[116:119], v[160:167], v[176:183], v[116:119], v141, v140 op_sel_hi:[0,0,0]
	v_mfma_scale_f32_16x16x128_f8f6f4 v[112:115], v[168:175], v[176:183], v[112:115], v141, v140 op_sel_hi:[0,0,0]
	v_mfma_scale_f32_16x16x128_f8f6f4 v[100:103], v[160:167], v[184:191], v[100:103], v141, v140 op_sel_hi:[0,0,0]
	v_mfma_scale_f32_16x16x128_f8f6f4 v[96:99], v[168:175], v[184:191], v[96:99], v141, v140 op_sel_hi:[0,0,0]
	v_mfma_scale_f32_16x16x128_f8f6f4 v[176:179], v[160:167], v[192:199], v[84:87], v141, v140 op_sel_hi:[0,0,0]
	v_mfma_scale_f32_16x16x128_f8f6f4 v[180:183], v[168:175], v[192:199], v[80:83], v141, v140 op_sel_hi:[0,0,0]
	v_mfma_scale_f32_16x16x128_f8f6f4 v[184:187], v[160:167], v[200:207], v[68:71], v141, v140 op_sel_hi:[0,0,0]
	v_mfma_scale_f32_16x16x128_f8f6f4 v[188:191], v[168:175], v[200:207], v[64:67], v141, v140 op_sel_hi:[0,0,0]
	s_barrier
	s_setprio 0
	s_nop 4
	ds_read_b128 v[64:67], v132 offset:16384
	ds_read_b128 v[68:71], v132 offset:16400
	ds_read_b128 v[72:75], v132 offset:18432
	ds_read_b128 v[76:79], v132 offset:18448
	ds_read_b128 v[80:83], v132 offset:20480
	ds_read_b128 v[84:87], v132 offset:20496
	ds_read_b128 v[88:91], v132 offset:22528
	ds_read_b128 v[92:95], v132 offset:22544
	s_mov_b32 s26, m0
	s_mov_b32 m0, s23
	s_nop 0
	global_load_lds_dwordx4 v135, s[40:41]
	s_mov_b32 m0, s26
	s_nop 0
	s_mov_b32 s26, m0
	s_mov_b32 m0, s25
	s_nop 0
	global_load_lds_dwordx4 v137, s[40:41]
	s_mov_b32 m0, s26
	s_add_u32 s26, s40, 0x40000
	s_addc_u32 s27, s41, 0
	s_mov_b32 s71, m0
	s_mov_b32 m0, s48
	s_nop 0
	global_load_lds_dwordx4 v135, s[26:27]
	s_mov_b32 m0, s71
	s_nop 0
	s_mov_b32 s71, m0
	s_mov_b32 m0, s49
	s_nop 0
	global_load_lds_dwordx4 v137, s[26:27]
	s_mov_b32 m0, s71
	s_mov_b32 s26, m0
	s_mov_b32 m0, s44
	s_nop 0
	global_load_lds_dwordx4 v134, s[42:43]
	s_mov_b32 m0, s26
	s_nop 0
	s_mov_b32 s26, m0
	s_mov_b32 m0, s50
	s_nop 0
	global_load_lds_dwordx4 v136, s[42:43]
	s_mov_b32 m0, s26
	s_waitcnt vmcnt(8)
	s_waitcnt lgkmcnt(0)
	s_setprio 1
	s_barrier
	v_mfma_scale_f32_16x16x128_f8f6f4 v[60:63], v[144:151], v[64:71], v[60:63], v140, v140 op_sel_hi:[0,0,0]
	v_mfma_scale_f32_16x16x128_f8f6f4 v[56:59], v[152:159], v[64:71], v[56:59], v140, v140 op_sel_hi:[0,0,0]
	v_mfma_scale_f32_16x16x128_f8f6f4 v[192:195], v[144:151], v[72:79], v[44:47], v140, v140 op_sel_hi:[0,0,0]
	v_mfma_scale_f32_16x16x128_f8f6f4 v[196:199], v[152:159], v[72:79], v[40:43], v140, v140 op_sel_hi:[0,0,0]
	v_mfma_scale_f32_16x16x128_f8f6f4 v[200:203], v[144:151], v[80:87], v[28:31], v140, v140 op_sel_hi:[0,0,0]
	v_mfma_scale_f32_16x16x128_f8f6f4 v[204:207], v[152:159], v[80:87], v[24:27], v140, v140 op_sel_hi:[0,0,0]
	v_mfma_scale_f32_16x16x128_f8f6f4 v[224:227], v[144:151], v[88:95], v[12:15], v140, v140 op_sel_hi:[0,0,0]
	v_mfma_scale_f32_16x16x128_f8f6f4 v[228:231], v[152:159], v[88:95], v[8:11], v140, v140 op_sel_hi:[0,0,0]
	v_mfma_scale_f32_16x16x128_f8f6f4 v[52:55], v[160:167], v[64:71], v[52:55], v141, v140 op_sel_hi:[0,0,0]
	v_mfma_scale_f32_16x16x128_f8f6f4 v[48:51], v[168:175], v[64:71], v[48:51], v141, v140 op_sel_hi:[0,0,0]
	v_mfma_scale_f32_16x16x128_f8f6f4 v[232:235], v[160:167], v[72:79], v[36:39], v141, v140 op_sel_hi:[0,0,0]
	v_mfma_scale_f32_16x16x128_f8f6f4 v[236:239], v[168:175], v[72:79], v[32:35], v141, v140 op_sel_hi:[0,0,0]
	v_mfma_scale_f32_16x16x128_f8f6f4 v[240:243], v[160:167], v[80:87], v[20:23], v141, v140 op_sel_hi:[0,0,0]
	v_mfma_scale_f32_16x16x128_f8f6f4 v[244:247], v[168:175], v[80:87], v[16:19], v141, v140 op_sel_hi:[0,0,0]
	v_mfma_scale_f32_16x16x128_f8f6f4 v[248:251], v[160:167], v[88:95], v[4:7], v141, v140 op_sel_hi:[0,0,0]
	v_mfma_scale_f32_16x16x128_f8f6f4 v[128:131], v[168:175], v[88:95], v[0:3], v141, v140 op_sel_hi:[0,0,0]
	s_barrier
; #define PG8_STAGE(bufoff, gbase, voff) do { _Pragma("unroll") for (int _i = 0; _i < 2; ++_i) { unsigned keep_; \
;         asm volatile("s_mov_b32 %0, m0\n\ts_mov_b32 m0, %3\n\ts_nop 0\n\tglobal_load_lds_dwordx4 %1, %2\n\ts_mov_b32 m0, %0" : "=&s"(keep_) : "v"((voff)[_i]), "s"((const char*)(gbase)), "s"(ldsbase + (unsigned)((bufoff) + _i * 8192)) : "memory"); } } while (0)
; #define PG8_WAIT_V(n) asm volatile("s_waitcnt vmcnt(" #n ")" ::: "memory")
; #define PG8_WAIT_L(n) asm volatile("s_waitcnt lgkmcnt(" #n ")" ::: "memory")
; #define PG8_BAR __builtin_amdgcn_s_barrier()
; #define PG8_SCHED __builtin_amdgcn_sched_barrier(0)
; template <class Epi, class Sched, bool ALIGN_EPI, bool FP8 = false>
; DI void gemm_phase(LAS unsigned char* lds, const Gemm g, const Sched& S, const Epi& E) {
;     ...
;             PG8_LDB(B0, 1, 0); PG8_LDB(B1, 1, 1); PG8_SCHED; PG8_LDA(At, 1, 0); PG8_STAGE(PG8_SA(0, 1), a2 + hstepA, voffA);
;             PG8_WAIT_V(8); PG8_WAIT_L(0); PG8_BAR; PG8_MMA(0, 0, At, B0); PG8_MMA(0, 1, At, B1); PG8_BAR; PG8_SCHED;
;             PG8_LDA(At, 1, 1); PG8_STAGE(PG8_SB(1, 0), b3, voffB); PG8_STAGE(PG8_SB(1, 1), b3 + hstepB, voffB); PG8_STAGE(PG8_SA(1, 0), a3, voffA);
;             PG8_WAIT_V(8); PG8_WAIT_L(0); PG8_BAR; PG8_MMA(1, 0, At, B0); PG8_MMA(1, 1, At, B1); PG8_BAR; PG8_SCHED;
;         }
;         if constexpr (ALIGN_EPI) { if (wr == 0) PG8_BAR; }
;         E(acc, cur, wr, wc, fr, fq);
	s_setprio 0
	s_nop 4
	ds_read_b128 v[0:3], v133 offset:32768
	ds_read_b128 v[4:7], v133 offset:32784
	ds_read_b128 v[16:19], v133 offset:34816
	ds_read_b128 v[20:23], v133 offset:34832
	ds_read_b128 v[144:147], v133 offset:49152
	ds_read_b128 v[148:151], v133 offset:49168
	ds_read_b128 v[152:155], v133 offset:51200
	ds_read_b128 v[156:159], v133 offset:51216
	ds_read_b128 v[8:11], v132 offset:32768
	ds_read_b128 v[12:15], v132 offset:32784
	ds_read_b128 v[24:27], v132 offset:34816
	ds_read_b128 v[28:31], v132 offset:34832
	ds_read_b128 v[32:35], v132 offset:36864
	ds_read_b128 v[36:39], v132 offset:36880
	ds_read_b128 v[40:43], v132 offset:38912
	ds_read_b128 v[44:47], v132 offset:38928
	s_add_u32 s26, s42, 0x40000
	s_addc_u32 s27, s43, 0
	s_mov_b32 s42, m0
	s_mov_b32 m0, s51
	s_nop 0
	global_load_lds_dwordx4 v134, s[26:27]
	s_mov_b32 m0, s42
	s_nop 0
	s_mov_b32 s42, m0
	s_mov_b32 m0, s52
	s_nop 0
	global_load_lds_dwordx4 v136, s[26:27]
	s_mov_b32 m0, s42
	s_waitcnt vmcnt(8)
	s_waitcnt lgkmcnt(0)
	s_setprio 1
	s_barrier
	v_mfma_scale_f32_16x16x128_f8f6f4 v[124:127], v[0:7], v[8:15], v[124:127], v140, v140 op_sel_hi:[0,0,0]
	v_mfma_scale_f32_16x16x128_f8f6f4 v[120:123], v[16:23], v[8:15], v[120:123], v140, v140 op_sel_hi:[0,0,0]
	v_mfma_scale_f32_16x16x128_f8f6f4 v[108:111], v[0:7], v[24:31], v[108:111], v140, v140 op_sel_hi:[0,0,0]
	v_mfma_scale_f32_16x16x128_f8f6f4 v[104:107], v[16:23], v[24:31], v[104:107], v140, v140 op_sel_hi:[0,0,0]
	v_mfma_scale_f32_16x16x128_f8f6f4 v[92:95], v[0:7], v[32:39], v[208:211], v140, v140 op_sel_hi:[0,0,0]
	v_mfma_scale_f32_16x16x128_f8f6f4 v[88:91], v[16:23], v[32:39], v[212:215], v140, v140 op_sel_hi:[0,0,0]
	v_mfma_scale_f32_16x16x128_f8f6f4 v[76:79], v[0:7], v[40:47], v[216:219], v140, v140 op_sel_hi:[0,0,0]
	v_mfma_scale_f32_16x16x128_f8f6f4 v[72:75], v[16:23], v[40:47], v[220:223], v140, v140 op_sel_hi:[0,0,0]
	v_mfma_scale_f32_16x16x128_f8f6f4 v[116:119], v[144:151], v[8:15], v[116:119], v141, v140 op_sel_hi:[0,0,0]
	v_mfma_scale_f32_16x16x128_f8f6f4 v[112:115], v[152:159], v[8:15], v[112:115], v141, v140 op_sel_hi:[0,0,0]
	v_mfma_scale_f32_16x16x128_f8f6f4 v[100:103], v[144:151], v[24:31], v[100:103], v141, v140 op_sel_hi:[0,0,0]
	v_mfma_scale_f32_16x16x128_f8f6f4 v[96:99], v[152:159], v[24:31], v[96:99], v141, v140 op_sel_hi:[0,0,0]
	v_mfma_scale_f32_16x16x128_f8f6f4 v[84:87], v[144:151], v[32:39], v[176:179], v141, v140 op_sel_hi:[0,0,0]
	v_mfma_scale_f32_16x16x128_f8f6f4 v[80:83], v[152:159], v[32:39], v[180:183], v141, v140 op_sel_hi:[0,0,0]
	v_mfma_scale_f32_16x16x128_f8f6f4 v[68:71], v[144:151], v[40:47], v[184:187], v141, v140 op_sel_hi:[0,0,0]
	v_mfma_scale_f32_16x16x128_f8f6f4 v[64:67], v[152:159], v[40:47], v[188:191], v141, v140 op_sel_hi:[0,0,0]
	s_barrier
	s_setprio 0
	ds_read_b128 v[32:35], v132 offset:49152
	ds_read_b128 v[36:39], v132 offset:49168
	ds_read_b128 v[160:163], v132 offset:51200
	ds_read_b128 v[164:167], v132 offset:51216
	ds_read_b128 v[168:171], v132 offset:53248
	ds_read_b128 v[172:175], v132 offset:53264
	ds_read_b128 v[176:179], v132 offset:55296
	ds_read_b128 v[180:183], v132 offset:55312
	s_add_u32 s26, s40, 0x80
	s_addc_u32 s27, s41, 0
	s_mov_b32 s42, m0
	s_mov_b32 m0, s56
	s_nop 0
	global_load_lds_dwordx4 v135, s[26:27]
	s_mov_b32 m0, s42
	s_nop 0
	s_mov_b32 s42, m0
	s_mov_b32 m0, s57
	s_nop 0
	global_load_lds_dwordx4 v137, s[26:27]
	s_mov_b32 m0, s42
	s_add_u32 s26, s40, 0x40080
	s_addc_u32 s27, s41, 0
	s_mov_b32 s40, m0
	s_mov_b32 m0, s60
	s_nop 0
	global_load_lds_dwordx4 v135, s[26:27]
	s_mov_b32 m0, s40
	s_nop 0
	s_mov_b32 s40, m0
	s_mov_b32 m0, s61
	s_nop 0
	global_load_lds_dwordx4 v137, s[26:27]
	s_mov_b32 m0, s40
	s_mov_b32 s26, m0
	s_mov_b32 m0, s58
	s_nop 0
	global_load_lds_dwordx4 v134, s[28:29]
	s_mov_b32 m0, s26
	s_nop 0
	s_mov_b32 s26, m0
	s_mov_b32 m0, s59
	s_nop 0
	global_load_lds_dwordx4 v136, s[28:29]
	s_mov_b32 m0, s26
	s_waitcnt vmcnt(8)
	s_waitcnt lgkmcnt(0)
	s_setprio 1
	s_barrier
	v_mfma_scale_f32_16x16x128_f8f6f4 v[60:63], v[0:7], v[32:39], v[60:63], v140, v140 op_sel_hi:[0,0,0]
	v_mfma_scale_f32_16x16x128_f8f6f4 v[56:59], v[16:23], v[32:39], v[56:59], v140, v140 op_sel_hi:[0,0,0]
	v_mfma_scale_f32_16x16x128_f8f6f4 v[44:47], v[0:7], v[160:167], v[192:195], v140, v140 op_sel_hi:[0,0,0]
	v_mfma_scale_f32_16x16x128_f8f6f4 v[40:43], v[16:23], v[160:167], v[196:199], v140, v140 op_sel_hi:[0,0,0]
	v_mfma_scale_f32_16x16x128_f8f6f4 v[28:31], v[0:7], v[168:175], v[200:203], v140, v140 op_sel_hi:[0,0,0]
	v_mfma_scale_f32_16x16x128_f8f6f4 v[24:27], v[16:23], v[168:175], v[204:207], v140, v140 op_sel_hi:[0,0,0]
	v_mfma_scale_f32_16x16x128_f8f6f4 v[12:15], v[0:7], v[176:183], v[224:227], v140, v140 op_sel_hi:[0,0,0]
	v_mfma_scale_f32_16x16x128_f8f6f4 v[8:11], v[16:23], v[176:183], v[228:231], v140, v140 op_sel_hi:[0,0,0]
	v_mfma_scale_f32_16x16x128_f8f6f4 v[52:55], v[144:151], v[32:39], v[52:55], v141, v140 op_sel_hi:[0,0,0]
	v_mfma_scale_f32_16x16x128_f8f6f4 v[48:51], v[152:159], v[32:39], v[48:51], v141, v140 op_sel_hi:[0,0,0]
	v_mfma_scale_f32_16x16x128_f8f6f4 v[36:39], v[144:151], v[160:167], v[232:235], v141, v140 op_sel_hi:[0,0,0]
	v_mfma_scale_f32_16x16x128_f8f6f4 v[32:35], v[152:159], v[160:167], v[236:239], v141, v140 op_sel_hi:[0,0,0]
	v_mfma_scale_f32_16x16x128_f8f6f4 v[20:23], v[144:151], v[168:175], v[240:243], v141, v140 op_sel_hi:[0,0,0]
	v_mfma_scale_f32_16x16x128_f8f6f4 v[16:19], v[152:159], v[168:175], v[244:247], v141, v140 op_sel_hi:[0,0,0]
	v_mfma_scale_f32_16x16x128_f8f6f4 v[4:7], v[144:151], v[176:183], v[248:251], v141, v140 op_sel_hi:[0,0,0]
	v_mfma_scale_f32_16x16x128_f8f6f4 v[0:3], v[152:159], v[176:183], v[128:131], v141, v140 op_sel_hi:[0,0,0]
	s_barrier
	s_setprio 0
	s_add_i32 s70, s70, 2
	s_add_u32 s68, s68, 0x100
	s_addc_u32 s69, s69, 0
	s_cmp_gt_u32 s70, 13
	s_mov_b64 s[26:27], s[6:7]
	s_cbranch_scc0 .LBB0_1608
	s_and_b64 vcc, exec, s[12:13]
	s_cbranch_vccz .LBB0_1611
	s_barrier

; #define PG8_STAGE(bufoff, gbase, voff) do { _Pragma("unroll") for (int _i = 0; _i < 2; ++_i) { unsigned keep_; \
;         asm volatile("s_mov_b32 %0, m0\n\ts_mov_b32 m0, %3\n\ts_nop 0\n\tglobal_load_lds_dwordx4 %1, %2\n\ts_mov_b32 m0, %0" : "=&s"(keep_) : "v"((voff)[_i]), "s"((const char*)(gbase)), "s"(ldsbase + (unsigned)((bufoff) + _i * 8192)) : "memory"); } } while (0)
; #define PG8_WAIT_V(n) asm volatile("s_waitcnt vmcnt(" #n ")" ::: "memory")
; #define PG8_WAIT_L(n) asm volatile("s_waitcnt lgkmcnt(" #n ")" ::: "memory")
; #define PG8_BAR __builtin_amdgcn_s_barrier()
; #define PG8_SCHED __builtin_amdgcn_sched_barrier(0)
;     DI int nt(const Unit& u) const { return (u.aux & 8) ? PLED / 64 : ((u.aux & 4) ? (D_ / 2) / 64 : D_ / 64); }
; template <class Epi, class Sched, bool ALIGN_EPI, bool FP8 = false>
; DI void gemm_phase(LAS unsigned char* lds, const Gemm g, const Sched& S, const Epi& E) {
;     ...
;         for (int t = 0; t < nt; t += 2) {
;             if constexpr (Epi::MID) { if (t == (nt >> 1)) E.mid(acc, cur, wr, wc, fr, fq); }
;             const bool last = (t == nt - 2);
;             const char* a1 = cA + (size_t)(t + 1) * kstep;
;             const char* a2 = last ? nA : cA + (size_t)(t + 2) * kstep; const char* b2 = last ? nB : cB + (size_t)(t + 2) * kstep;
;             const char* a3 = a2 + kstep; const char* b3 = b2 + kstep;
;             PG8_LDB(B0, 0, 0); PG8_LDB(B1, 0, 1); PG8_SCHED; PG8_LDA(At, 0, 0); PG8_STAGE(PG8_SA(1, 1), a1 + hstepA, voffA);
;             PG8_WAIT_V(8); PG8_WAIT_L(0); PG8_BAR; PG8_MMA(0, 0, At, B0); PG8_MMA(0, 1, At, B1); PG8_BAR; PG8_SCHED;
;             PG8_LDA(At, 0, 1); PG8_STAGE(PG8_SB(0, 0), b2, voffB); PG8_STAGE(PG8_SB(0, 1), b2 + hstepB, voffB); PG8_STAGE(PG8_SA(0, 0), a2, voffA);
;             PG8_WAIT_V(8); PG8_WAIT_L(0); PG8_BAR; PG8_MMA(1, 0, At, B0); PG8_MMA(1, 1, At, B1); PG8_BAR; PG8_SCHED;
;             PG8_LDB(B0, 1, 0); PG8_LDB(B1, 1, 1); PG8_SCHED; PG8_LDA(At, 1, 0); PG8_STAGE(PG8_SA(0, 1), a2 + hstepA, voffA);
;             PG8_WAIT_V(8); PG8_WAIT_L(0); PG8_BAR; PG8_MMA(0, 0, At, B0); PG8_MMA(0, 1, At, B1); PG8_BAR; PG8_SCHED;
.LBB0_1685:
	ds_read_b128 v[140:143], v131
	ds_read_b128 v[144:147], v131 offset:16
	ds_read_b128 v[148:151], v131 offset:2048
	ds_read_b128 v[152:155], v131 offset:2064
	ds_read_b128 v[156:159], v131 offset:16384
	ds_read_b128 v[160:163], v131 offset:16400
	ds_read_b128 v[164:167], v131 offset:18432
	ds_read_b128 v[168:171], v131 offset:18448
	s_add_u32 s46, s44, 0x100
	s_addc_u32 s47, s45, 0
	s_cmp_eq_u32 s92, 52
	s_cselect_b32 s52, s6, s46
	s_cselect_b32 s53, s7, s47
	s_cselect_b32 s50, s42, s90
	s_cselect_b32 s51, s43, s91
	s_add_u32 s48, s52, 0x80
	s_addc_u32 s49, s53, 0
	ds_read_b128 v[172:175], v130
	ds_read_b128 v[176:179], v130 offset:16
	ds_read_b128 v[180:183], v130 offset:2048
	ds_read_b128 v[184:187], v130 offset:2064
	ds_read_b128 v[188:191], v130 offset:4096
	ds_read_b128 v[192:195], v130 offset:4112
	ds_read_b128 v[196:199], v130 offset:6144
	ds_read_b128 v[200:203], v130 offset:6160
	s_add_u32 s44, s44, 0xe0080
	s_addc_u32 s45, s45, 0
	s_mov_b32 s93, m0
	s_mov_b32 m0, s73
	s_nop 0
	global_load_lds_dwordx4 v132, s[44:45]
	s_mov_b32 m0, s93
	s_nop 0
	s_mov_b32 s93, m0
	s_mov_b32 m0, s74
	s_nop 0
	global_load_lds_dwordx4 v134, s[44:45]
	s_mov_b32 m0, s93
	s_waitcnt vmcnt(8)
	s_waitcnt lgkmcnt(0)
	s_setprio 1
	s_barrier
	v_mfma_scale_f32_16x16x128_f8f6f4 v[124:127], v[140:147], v[172:179], v[124:127], v138, v138 op_sel_hi:[0,0,0]
	v_mfma_scale_f32_16x16x128_f8f6f4 v[120:123], v[148:155], v[172:179], v[120:123], v138, v138 op_sel_hi:[0,0,0]
	v_mfma_scale_f32_16x16x128_f8f6f4 v[116:119], v[140:147], v[180:187], v[116:119], v138, v138 op_sel_hi:[0,0,0]
	v_mfma_scale_f32_16x16x128_f8f6f4 v[112:115], v[148:155], v[180:187], v[112:115], v138, v138 op_sel_hi:[0,0,0]
	v_mfma_scale_f32_16x16x128_f8f6f4 v[100:103], v[140:147], v[188:195], v[100:103], v138, v138 op_sel_hi:[0,0,0]
	v_mfma_scale_f32_16x16x128_f8f6f4 v[96:99], v[148:155], v[188:195], v[96:99], v138, v138 op_sel_hi:[0,0,0]
	v_mfma_scale_f32_16x16x128_f8f6f4 v[204:207], v[140:147], v[196:203], v[84:87], v138, v138 op_sel_hi:[0,0,0]
	v_mfma_scale_f32_16x16x128_f8f6f4 v[208:211], v[148:155], v[196:203], v[80:83], v138, v138 op_sel_hi:[0,0,0]
	v_mfma_scale_f32_16x16x128_f8f6f4 v[108:111], v[156:163], v[172:179], v[108:111], v138, v138 op_sel_hi:[0,0,0]
	v_mfma_scale_f32_16x16x128_f8f6f4 v[104:107], v[164:171], v[172:179], v[104:107], v138, v138 op_sel_hi:[0,0,0]
	v_mfma_scale_f32_16x16x128_f8f6f4 v[172:175], v[156:163], v[180:187], v[92:95], v138, v138 op_sel_hi:[0,0,0]
	v_mfma_scale_f32_16x16x128_f8f6f4 v[176:179], v[164:171], v[180:187], v[88:91], v138, v138 op_sel_hi:[0,0,0]
	v_mfma_scale_f32_16x16x128_f8f6f4 v[180:183], v[156:163], v[188:195], v[76:79], v138, v138 op_sel_hi:[0,0,0]
	v_mfma_scale_f32_16x16x128_f8f6f4 v[184:187], v[164:171], v[188:195], v[72:75], v138, v138 op_sel_hi:[0,0,0]
	v_mfma_scale_f32_16x16x128_f8f6f4 v[188:191], v[156:163], v[196:203], v[68:71], v138, v138 op_sel_hi:[0,0,0]
	v_mfma_scale_f32_16x16x128_f8f6f4 v[192:195], v[164:171], v[196:203], v[64:67], v138, v138 op_sel_hi:[0,0,0]
	s_barrier
	s_setprio 0
	s_nop 4
	ds_read_b128 v[64:67], v130 offset:16384
	ds_read_b128 v[68:71], v130 offset:16400
	ds_read_b128 v[72:75], v130 offset:18432
	ds_read_b128 v[76:79], v130 offset:18448
	ds_read_b128 v[80:83], v130 offset:20480
	ds_read_b128 v[84:87], v130 offset:20496
	ds_read_b128 v[88:91], v130 offset:22528
	ds_read_b128 v[92:95], v130 offset:22544
	s_mov_b32 s44, m0
	s_mov_b32 m0, s57
	s_nop 0
	global_load_lds_dwordx4 v133, s[50:51]
	s_mov_b32 m0, s44
	s_nop 0
	s_mov_b32 s44, m0
	s_mov_b32 m0, s58
	s_nop 0
	global_load_lds_dwordx4 v135, s[50:51]
	s_mov_b32 m0, s44
	s_add_u32 s44, s50, 0xe0000
	s_addc_u32 s45, s51, 0
	s_mov_b32 s93, m0
	s_mov_b32 m0, s59
	s_nop 0
	global_load_lds_dwordx4 v133, s[44:45]
	s_mov_b32 m0, s93
	s_nop 0
	s_mov_b32 s93, m0
	s_mov_b32 m0, s60
	s_nop 0
	global_load_lds_dwordx4 v135, s[44:45]
	s_mov_b32 m0, s93
	s_mov_b32 s44, m0
	s_mov_b32 m0, s54
	s_nop 0
	global_load_lds_dwordx4 v132, s[52:53]
	s_mov_b32 m0, s44
	s_nop 0
	s_mov_b32 s44, m0
	s_mov_b32 m0, s61
	s_nop 0
	global_load_lds_dwordx4 v134, s[52:53]
	s_mov_b32 m0, s44
	s_waitcnt vmcnt(8)
	s_waitcnt lgkmcnt(0)
	s_setprio 1
	s_barrier
	v_mfma_scale_f32_16x16x128_f8f6f4 v[60:63], v[140:147], v[64:71], v[60:63], v138, v138 op_sel_hi:[0,0,0]
	v_mfma_scale_f32_16x16x128_f8f6f4 v[56:59], v[148:155], v[64:71], v[56:59], v138, v138 op_sel_hi:[0,0,0]
	v_mfma_scale_f32_16x16x128_f8f6f4 v[52:55], v[140:147], v[72:79], v[52:55], v138, v138 op_sel_hi:[0,0,0]
	v_mfma_scale_f32_16x16x128_f8f6f4 v[48:51], v[148:155], v[72:79], v[48:51], v138, v138 op_sel_hi:[0,0,0]
	v_mfma_scale_f32_16x16x128_f8f6f4 v[196:199], v[140:147], v[80:87], v[36:39], v138, v138 op_sel_hi:[0,0,0]
	v_mfma_scale_f32_16x16x128_f8f6f4 v[200:203], v[148:155], v[80:87], v[32:35], v138, v138 op_sel_hi:[0,0,0]
	v_mfma_scale_f32_16x16x128_f8f6f4 v[212:215], v[140:147], v[88:95], v[20:23], v138, v138 op_sel_hi:[0,0,0]
	v_mfma_scale_f32_16x16x128_f8f6f4 v[216:219], v[148:155], v[88:95], v[16:19], v138, v138 op_sel_hi:[0,0,0]
	v_mfma_scale_f32_16x16x128_f8f6f4 v[220:223], v[156:163], v[64:71], v[44:47], v138, v138 op_sel_hi:[0,0,0]
	v_mfma_scale_f32_16x16x128_f8f6f4 v[224:227], v[164:171], v[64:71], v[40:43], v138, v138 op_sel_hi:[0,0,0]
	v_mfma_scale_f32_16x16x128_f8f6f4 v[228:231], v[156:163], v[72:79], v[28:31], v138, v138 op_sel_hi:[0,0,0]
	v_mfma_scale_f32_16x16x128_f8f6f4 v[232:235], v[164:171], v[72:79], v[24:27], v138, v138 op_sel_hi:[0,0,0]
	v_mfma_scale_f32_16x16x128_f8f6f4 v[236:239], v[156:163], v[80:87], v[12:15], v138, v138 op_sel_hi:[0,0,0]
	v_mfma_scale_f32_16x16x128_f8f6f4 v[240:243], v[164:171], v[80:87], v[8:11], v138, v138 op_sel_hi:[0,0,0]
	v_mfma_scale_f32_16x16x128_f8f6f4 v[244:247], v[156:163], v[88:95], v[4:7], v138, v138 op_sel_hi:[0,0,0]
	v_mfma_scale_f32_16x16x128_f8f6f4 v[248:251], v[164:171], v[88:95], v[0:3], v138, v138 op_sel_hi:[0,0,0]
	s_barrier
; #define PG8_STAGE(bufoff, gbase, voff) do { _Pragma("unroll") for (int _i = 0; _i < 2; ++_i) { unsigned keep_; \
;         asm volatile("s_mov_b32 %0, m0\n\ts_mov_b32 m0, %3\n\ts_nop 0\n\tglobal_load_lds_dwordx4 %1, %2\n\ts_mov_b32 m0, %0" : "=&s"(keep_) : "v"((voff)[_i]), "s"((const char*)(gbase)), "s"(ldsbase + (unsigned)((bufoff) + _i * 8192)) : "memory"); } } while (0)
; #define PG8_WAIT_V(n) asm volatile("s_waitcnt vmcnt(" #n ")" ::: "memory")
; #define PG8_WAIT_L(n) asm volatile("s_waitcnt lgkmcnt(" #n ")" ::: "memory")
; #define PG8_BAR __builtin_amdgcn_s_barrier()
; #define PG8_SCHED __builtin_amdgcn_sched_barrier(0)
; template <class Epi, class Sched, bool ALIGN_EPI, bool FP8 = false>
; DI void gemm_phase(LAS unsigned char* lds, const Gemm g, const Sched& S, const Epi& E) {
;     ...
;             PG8_LDB(B0, 1, 0); PG8_LDB(B1, 1, 1); PG8_SCHED; PG8_LDA(At, 1, 0); PG8_STAGE(PG8_SA(0, 1), a2 + hstepA, voffA);
;             PG8_WAIT_V(8); PG8_WAIT_L(0); PG8_BAR; PG8_MMA(0, 0, At, B0); PG8_MMA(0, 1, At, B1); PG8_BAR; PG8_SCHED;
;             PG8_LDA(At, 1, 1); PG8_STAGE(PG8_SB(1, 0), b3, voffB); PG8_STAGE(PG8_SB(1, 1), b3 + hstepB, voffB); PG8_STAGE(PG8_SA(1, 0), a3, voffA);
;             PG8_WAIT_V(8); PG8_WAIT_L(0); PG8_BAR; PG8_MMA(1, 0, At, B0); PG8_MMA(1, 1, At, B1); PG8_BAR; PG8_SCHED;
;         }
;         if constexpr (ALIGN_EPI) { if (wr == 0) PG8_BAR; }
;         E(acc, cur, wr, wc, fr, fq);
	s_setprio 0
	s_nop 4
	ds_read_b128 v[0:3], v131 offset:32768
	ds_read_b128 v[4:7], v131 offset:32784
	ds_read_b128 v[8:11], v131 offset:34816
	ds_read_b128 v[12:15], v131 offset:34832
	ds_read_b128 v[140:143], v131 offset:49152
	ds_read_b128 v[144:147], v131 offset:49168
	ds_read_b128 v[148:151], v131 offset:51200
	ds_read_b128 v[152:155], v131 offset:51216
	ds_read_b128 v[16:19], v130 offset:32768
	ds_read_b128 v[20:23], v130 offset:32784
	ds_read_b128 v[24:27], v130 offset:34816
	ds_read_b128 v[28:31], v130 offset:34832
	ds_read_b128 v[32:35], v130 offset:36864
	ds_read_b128 v[36:39], v130 offset:36880
	ds_read_b128 v[40:43], v130 offset:38912
	ds_read_b128 v[44:47], v130 offset:38928
	s_add_u32 s44, s52, 0xe0000
	s_addc_u32 s45, s53, 0
	s_mov_b32 s52, m0
	s_mov_b32 m0, s62
	s_nop 0
	global_load_lds_dwordx4 v132, s[44:45]
	s_mov_b32 m0, s52
	s_nop 0
	s_mov_b32 s52, m0
	s_mov_b32 m0, s63
	s_nop 0
	global_load_lds_dwordx4 v134, s[44:45]
	s_mov_b32 m0, s52
	s_waitcnt vmcnt(8)
	s_waitcnt lgkmcnt(0)
	s_setprio 1
	s_barrier
	v_mfma_scale_f32_16x16x128_f8f6f4 v[124:127], v[0:7], v[16:23], v[124:127], v138, v138 op_sel_hi:[0,0,0]
	v_mfma_scale_f32_16x16x128_f8f6f4 v[120:123], v[8:15], v[16:23], v[120:123], v138, v138 op_sel_hi:[0,0,0]
	v_mfma_scale_f32_16x16x128_f8f6f4 v[116:119], v[0:7], v[24:31], v[116:119], v138, v138 op_sel_hi:[0,0,0]
	v_mfma_scale_f32_16x16x128_f8f6f4 v[112:115], v[8:15], v[24:31], v[112:115], v138, v138 op_sel_hi:[0,0,0]
	v_mfma_scale_f32_16x16x128_f8f6f4 v[100:103], v[0:7], v[32:39], v[100:103], v138, v138 op_sel_hi:[0,0,0]
	v_mfma_scale_f32_16x16x128_f8f6f4 v[96:99], v[8:15], v[32:39], v[96:99], v138, v138 op_sel_hi:[0,0,0]
	v_mfma_scale_f32_16x16x128_f8f6f4 v[84:87], v[0:7], v[40:47], v[204:207], v138, v138 op_sel_hi:[0,0,0]
	v_mfma_scale_f32_16x16x128_f8f6f4 v[80:83], v[8:15], v[40:47], v[208:211], v138, v138 op_sel_hi:[0,0,0]
	v_mfma_scale_f32_16x16x128_f8f6f4 v[108:111], v[140:147], v[16:23], v[108:111], v138, v138 op_sel_hi:[0,0,0]
	v_mfma_scale_f32_16x16x128_f8f6f4 v[104:107], v[148:155], v[16:23], v[104:107], v138, v138 op_sel_hi:[0,0,0]
	v_mfma_scale_f32_16x16x128_f8f6f4 v[92:95], v[140:147], v[24:31], v[172:175], v138, v138 op_sel_hi:[0,0,0]
	v_mfma_scale_f32_16x16x128_f8f6f4 v[88:91], v[148:155], v[24:31], v[176:179], v138, v138 op_sel_hi:[0,0,0]
	v_mfma_scale_f32_16x16x128_f8f6f4 v[76:79], v[140:147], v[32:39], v[180:183], v138, v138 op_sel_hi:[0,0,0]
	v_mfma_scale_f32_16x16x128_f8f6f4 v[72:75], v[148:155], v[32:39], v[184:187], v138, v138 op_sel_hi:[0,0,0]
	v_mfma_scale_f32_16x16x128_f8f6f4 v[68:71], v[140:147], v[40:47], v[188:191], v138, v138 op_sel_hi:[0,0,0]
	v_mfma_scale_f32_16x16x128_f8f6f4 v[64:67], v[148:155], v[40:47], v[192:195], v138, v138 op_sel_hi:[0,0,0]
	s_barrier
	s_setprio 0
	ds_read_b128 v[24:27], v130 offset:49152
	ds_read_b128 v[28:31], v130 offset:49168
	ds_read_b128 v[156:159], v130 offset:51200
	ds_read_b128 v[160:163], v130 offset:51216
	ds_read_b128 v[164:167], v130 offset:53248
	ds_read_b128 v[168:171], v130 offset:53264
	ds_read_b128 v[172:175], v130 offset:55296
	ds_read_b128 v[176:179], v130 offset:55312
	s_add_u32 s44, s50, 0x80
	s_addc_u32 s45, s51, 0
	s_mov_b32 s52, m0
	s_mov_b32 m0, s67
	s_nop 0
	global_load_lds_dwordx4 v133, s[44:45]
	s_mov_b32 m0, s52
	s_nop 0
	s_mov_b32 s52, m0
	s_mov_b32 m0, s68
	s_nop 0
	global_load_lds_dwordx4 v135, s[44:45]
	s_mov_b32 m0, s52
	s_add_u32 s44, s50, 0xe0080
	s_addc_u32 s45, s51, 0
	s_mov_b32 s50, m0
	s_mov_b32 m0, s71
	s_nop 0
	global_load_lds_dwordx4 v133, s[44:45]
	s_mov_b32 m0, s50
	s_nop 0
	s_mov_b32 s50, m0
	s_mov_b32 m0, s72
	s_nop 0
	global_load_lds_dwordx4 v135, s[44:45]
	s_mov_b32 m0, s50
	s_mov_b32 s44, m0
	s_mov_b32 m0, s69
	s_nop 0
	global_load_lds_dwordx4 v132, s[48:49]
	s_mov_b32 m0, s44
	s_nop 0
	s_mov_b32 s44, m0
	s_mov_b32 m0, s70
	s_nop 0
	global_load_lds_dwordx4 v134, s[48:49]
	s_mov_b32 m0, s44
	s_waitcnt vmcnt(8)
	s_waitcnt lgkmcnt(0)
	s_setprio 1
	s_barrier
	v_mfma_scale_f32_16x16x128_f8f6f4 v[60:63], v[0:7], v[24:31], v[60:63], v138, v138 op_sel_hi:[0,0,0]
	v_mfma_scale_f32_16x16x128_f8f6f4 v[56:59], v[8:15], v[24:31], v[56:59], v138, v138 op_sel_hi:[0,0,0]
	v_mfma_scale_f32_16x16x128_f8f6f4 v[52:55], v[0:7], v[156:163], v[52:55], v138, v138 op_sel_hi:[0,0,0]
	v_mfma_scale_f32_16x16x128_f8f6f4 v[48:51], v[8:15], v[156:163], v[48:51], v138, v138 op_sel_hi:[0,0,0]
	v_mfma_scale_f32_16x16x128_f8f6f4 v[36:39], v[0:7], v[164:171], v[196:199], v138, v138 op_sel_hi:[0,0,0]
	v_mfma_scale_f32_16x16x128_f8f6f4 v[32:35], v[8:15], v[164:171], v[200:203], v138, v138 op_sel_hi:[0,0,0]
	v_mfma_scale_f32_16x16x128_f8f6f4 v[20:23], v[0:7], v[172:179], v[212:215], v138, v138 op_sel_hi:[0,0,0]
	v_mfma_scale_f32_16x16x128_f8f6f4 v[16:19], v[8:15], v[172:179], v[216:219], v138, v138 op_sel_hi:[0,0,0]
	v_mfma_scale_f32_16x16x128_f8f6f4 v[44:47], v[140:147], v[24:31], v[220:223], v138, v138 op_sel_hi:[0,0,0]
	v_mfma_scale_f32_16x16x128_f8f6f4 v[40:43], v[148:155], v[24:31], v[224:227], v138, v138 op_sel_hi:[0,0,0]
	v_mfma_scale_f32_16x16x128_f8f6f4 v[28:31], v[140:147], v[156:163], v[228:231], v138, v138 op_sel_hi:[0,0,0]
	v_mfma_scale_f32_16x16x128_f8f6f4 v[24:27], v[148:155], v[156:163], v[232:235], v138, v138 op_sel_hi:[0,0,0]
	v_mfma_scale_f32_16x16x128_f8f6f4 v[12:15], v[140:147], v[164:171], v[236:239], v138, v138 op_sel_hi:[0,0,0]
	v_mfma_scale_f32_16x16x128_f8f6f4 v[8:11], v[148:155], v[164:171], v[240:243], v138, v138 op_sel_hi:[0,0,0]
	v_mfma_scale_f32_16x16x128_f8f6f4 v[4:7], v[140:147], v[172:179], v[244:247], v138, v138 op_sel_hi:[0,0,0]
	v_mfma_scale_f32_16x16x128_f8f6f4 v[0:3], v[148:155], v[172:179], v[248:251], v138, v138 op_sel_hi:[0,0,0]
	s_barrier
	s_setprio 0
	s_add_i32 s92, s92, 2
	s_add_u32 s90, s90, 0x100
	s_addc_u32 s91, s91, 0
	s_cmp_gt_u32 s92, 53
	s_mov_b64 s[44:45], s[46:47]
	s_cbranch_scc0 .LBB0_1685
	s_and_b64 vcc, exec, s[16:17]
	s_cbranch_vccz .LBB0_1688
	s_barrier

; #define PG8_STAGE(bufoff, gbase, voff) do { _Pragma("unroll") for (int _i = 0; _i < 2; ++_i) { unsigned keep_; \
;         asm volatile("s_mov_b32 %0, m0\n\ts_mov_b32 m0, %3\n\ts_nop 0\n\tglobal_load_lds_dwordx4 %1, %2\n\ts_mov_b32 m0, %0" : "=&s"(keep_) : "v"((voff)[_i]), "s"((const char*)(gbase)), "s"(ldsbase + (unsigned)((bufoff) + _i * 8192)) : "memory"); } } while (0)
; #define PG8_WAIT_V(n) asm volatile("s_waitcnt vmcnt(" #n ")" ::: "memory")
; #define PG8_WAIT_L(n) asm volatile("s_waitcnt lgkmcnt(" #n ")" ::: "memory")
; #define PG8_BAR __builtin_amdgcn_s_barrier()
; #define PG8_SCHED __builtin_amdgcn_sched_barrier(0)
;     DI int nt(const Unit& u) const { return (u.aux & 8) ? PLED / 64 : ((u.aux & 4) ? (D_ / 2) / 64 : D_ / 64); }
; template <class Epi, class Sched, bool ALIGN_EPI, bool FP8 = false>
; DI void gemm_phase(LAS unsigned char* lds, const Gemm g, const Sched& S, const Epi& E) {
;     ...
;         for (int t = 0; t < nt; t += 2) {
;             if constexpr (Epi::MID) { if (t == (nt >> 1)) E.mid(acc, cur, wr, wc, fr, fq); }
;             const bool last = (t == nt - 2);
;             const char* a1 = cA + (size_t)(t + 1) * kstep;
;             const char* a2 = last ? nA : cA + (size_t)(t + 2) * kstep; const char* b2 = last ? nB : cB + (size_t)(t + 2) * kstep;
;             const char* a3 = a2 + kstep; const char* b3 = b2 + kstep;
;             PG8_LDB(B0, 0, 0); PG8_LDB(B1, 0, 1); PG8_SCHED; PG8_LDA(At, 0, 0); PG8_STAGE(PG8_SA(1, 1), a1 + hstepA, voffA);
;             PG8_WAIT_V(8); PG8_WAIT_L(0); PG8_BAR; PG8_MMA(0, 0, At, B0); PG8_MMA(0, 1, At, B1); PG8_BAR; PG8_SCHED;
;             PG8_LDA(At, 0, 1); PG8_STAGE(PG8_SB(0, 0), b2, voffB); PG8_STAGE(PG8_SB(0, 1), b2 + hstepB, voffB); PG8_STAGE(PG8_SA(0, 0), a2, voffA);
;             PG8_WAIT_V(8); PG8_WAIT_L(0); PG8_BAR; PG8_MMA(1, 0, At, B0); PG8_MMA(1, 1, At, B1); PG8_BAR; PG8_SCHED;
;             PG8_LDB(B0, 1, 0); PG8_LDB(B1, 1, 1); PG8_SCHED; PG8_LDA(At, 1, 0); PG8_STAGE(PG8_SA(0, 1), a2 + hstepA, voffA);
;             PG8_WAIT_V(8); PG8_WAIT_L(0); PG8_BAR; PG8_MMA(0, 0, At, B0); PG8_MMA(0, 1, At, B1); PG8_BAR; PG8_SCHED;
.LBB0_1710:
	ds_read_b128 v[146:149], v140
	ds_read_b128 v[150:153], v140 offset:1024
	ds_read_b128 v[154:157], v140 offset:2048
	ds_read_b128 v[158:161], v140 offset:3072
	ds_read_b128 v[162:165], v141
	ds_read_b128 v[166:169], v141 offset:1024
	ds_read_b128 v[170:173], v141 offset:2048
	ds_read_b128 v[174:177], v141 offset:3072
	s_add_u32 s64, s62, 0x100
	s_addc_u32 s65, s63, 0
	s_cmp_eq_u32 vcc_lo, 28
	s_cselect_b32 s70, s94, s64
	s_cselect_b32 s71, s55, s65
	s_cselect_b32 s68, s95, s96
	s_cselect_b32 s69, s53, s97
	s_add_u32 s66, s70, 0x80
	s_addc_u32 s67, s71, 0
	ds_read_b128 v[178:181], v142
	ds_read_b128 v[182:185], v142 offset:1024
	ds_read_b128 v[186:189], v142 offset:2048
	ds_read_b128 v[190:193], v142 offset:3072
	ds_read_b128 v[194:197], v142 offset:4096
	ds_read_b128 v[198:201], v142 offset:5120
	ds_read_b128 v[202:205], v142 offset:6144
	ds_read_b128 v[206:209], v142 offset:7168
	s_add_u32 s62, s62, 0x80080
	s_addc_u32 s63, s63, 0
	s_mov_b32 vcc_hi, m0
	s_mov_b32 m0, s89
	s_nop 0
	global_load_lds_dwordx4 v134, s[62:63]
	s_mov_b32 m0, vcc_hi
	s_nop 0
	s_mov_b32 vcc_hi, m0
	s_mov_b32 m0, s90
	s_nop 0
	global_load_lds_dwordx4 v136, s[62:63]
	s_mov_b32 m0, vcc_hi
	s_waitcnt vmcnt(8)
	s_waitcnt lgkmcnt(0)
	s_setprio 1
	s_barrier
	v_mfma_f32_16x16x32_bf16 v[124:127], v[146:149], v[178:181], v[124:127]
	v_mfma_f32_16x16x32_bf16 v[120:123], v[154:157], v[178:181], v[120:123]
	v_mfma_f32_16x16x32_bf16 v[108:111], v[146:149], v[186:189], v[108:111]
	v_mfma_f32_16x16x32_bf16 v[104:107], v[154:157], v[186:189], v[104:107]
	v_mfma_f32_16x16x32_bf16 v[92:95], v[146:149], v[194:197], v[92:95]
	v_mfma_f32_16x16x32_bf16 v[88:91], v[154:157], v[194:197], v[88:91]
	v_mfma_f32_16x16x32_bf16 v[76:79], v[146:149], v[202:205], v[76:79]
	v_mfma_f32_16x16x32_bf16 v[72:75], v[154:157], v[202:205], v[72:75]
	v_mfma_f32_16x16x32_bf16 v[124:127], v[150:153], v[182:185], v[124:127]
	v_mfma_f32_16x16x32_bf16 v[120:123], v[158:161], v[182:185], v[120:123]
	v_mfma_f32_16x16x32_bf16 v[108:111], v[150:153], v[190:193], v[108:111]
	v_mfma_f32_16x16x32_bf16 v[104:107], v[158:161], v[190:193], v[104:107]
	v_mfma_f32_16x16x32_bf16 v[92:95], v[150:153], v[198:201], v[92:95]
	v_mfma_f32_16x16x32_bf16 v[88:91], v[158:161], v[198:201], v[88:91]
	v_mfma_f32_16x16x32_bf16 v[76:79], v[150:153], v[206:209], v[76:79]
	v_mfma_f32_16x16x32_bf16 v[72:75], v[158:161], v[206:209], v[72:75]
	v_mfma_f32_16x16x32_bf16 v[116:119], v[162:165], v[178:181], v[116:119]
	v_mfma_f32_16x16x32_bf16 v[112:115], v[170:173], v[178:181], v[112:115]
	v_mfma_f32_16x16x32_bf16 v[100:103], v[162:165], v[186:189], v[100:103]
	v_mfma_f32_16x16x32_bf16 v[96:99], v[170:173], v[186:189], v[96:99]
	v_mfma_f32_16x16x32_bf16 v[84:87], v[162:165], v[194:197], v[84:87]
	v_mfma_f32_16x16x32_bf16 v[80:83], v[170:173], v[194:197], v[80:83]
	v_mfma_f32_16x16x32_bf16 v[68:71], v[162:165], v[202:205], v[68:71]
	v_mfma_f32_16x16x32_bf16 v[64:67], v[170:173], v[202:205], v[64:67]
	v_mfma_f32_16x16x32_bf16 v[116:119], v[166:169], v[182:185], v[116:119]
	v_mfma_f32_16x16x32_bf16 v[112:115], v[174:177], v[182:185], v[112:115]
	v_mfma_f32_16x16x32_bf16 v[100:103], v[166:169], v[190:193], v[100:103]
	v_mfma_f32_16x16x32_bf16 v[96:99], v[174:177], v[190:193], v[96:99]
	v_mfma_f32_16x16x32_bf16 v[84:87], v[166:169], v[198:201], v[84:87]
	v_mfma_f32_16x16x32_bf16 v[80:83], v[174:177], v[198:201], v[80:83]
	v_mfma_f32_16x16x32_bf16 v[68:71], v[166:169], v[206:209], v[68:71]
	v_mfma_f32_16x16x32_bf16 v[64:67], v[174:177], v[206:209], v[64:67]
	s_barrier
	s_setprio 0
	ds_read_b128 v[178:181], v142 offset:16384
	ds_read_b128 v[182:185], v142 offset:17408
	ds_read_b128 v[186:189], v142 offset:18432
	ds_read_b128 v[190:193], v142 offset:19456
	ds_read_b128 v[194:197], v142 offset:20480
	ds_read_b128 v[198:201], v142 offset:21504
	ds_read_b128 v[202:205], v142 offset:22528
	ds_read_b128 v[206:209], v142 offset:23552
	s_mov_b32 s62, m0
	s_mov_b32 m0, s61
	s_nop 0
	global_load_lds_dwordx4 v135, s[68:69]
	s_mov_b32 m0, s62
	s_nop 0
	s_mov_b32 s62, m0
	s_mov_b32 m0, s75
	s_nop 0
	global_load_lds_dwordx4 v137, s[68:69]
	s_mov_b32 m0, s62
	s_add_u32 s62, s68, 0x80000
	s_addc_u32 s63, s69, 0
	s_mov_b32 vcc_hi, m0
	s_mov_b32 m0, s77
	s_nop 0
	global_load_lds_dwordx4 v135, s[62:63]
	s_mov_b32 m0, vcc_hi
	s_nop 0
	s_mov_b32 vcc_hi, m0
	s_mov_b32 m0, s79
	s_nop 0
	global_load_lds_dwordx4 v137, s[62:63]
	s_mov_b32 m0, vcc_hi
	s_mov_b32 s62, m0
	s_mov_b32 m0, s74
	s_nop 0
	global_load_lds_dwordx4 v134, s[70:71]
	s_mov_b32 m0, s62
	s_nop 0
	s_mov_b32 s62, m0
	s_mov_b32 m0, s80
	s_nop 0
	global_load_lds_dwordx4 v136, s[70:71]
	s_mov_b32 m0, s62
	s_waitcnt vmcnt(8)
	s_waitcnt lgkmcnt(0)
	s_setprio 1
	s_barrier
; #define PG8_STAGE(bufoff, gbase, voff) do { _Pragma("unroll") for (int _i = 0; _i < 2; ++_i) { unsigned keep_; \
;         asm volatile("s_mov_b32 %0, m0\n\ts_mov_b32 m0, %3\n\ts_nop 0\n\tglobal_load_lds_dwordx4 %1, %2\n\ts_mov_b32 m0, %0" : "=&s"(keep_) : "v"((voff)[_i]), "s"((const char*)(gbase)), "s"(ldsbase + (unsigned)((bufoff) + _i * 8192)) : "memory"); } } while (0)
; #define PG8_WAIT_V(n) asm volatile("s_waitcnt vmcnt(" #n ")" ::: "memory")
; #define PG8_WAIT_L(n) asm volatile("s_waitcnt lgkmcnt(" #n ")" ::: "memory")
; #define PG8_BAR __builtin_amdgcn_s_barrier()
; #define PG8_SCHED __builtin_amdgcn_sched_barrier(0)
; template <class Epi, class Sched, bool ALIGN_EPI, bool FP8 = false>
; DI void gemm_phase(LAS unsigned char* lds, const Gemm g, const Sched& S, const Epi& E) {
;     ...
;             PG8_WAIT_V(8); PG8_WAIT_L(0); PG8_BAR; PG8_MMA(0, 0, At, B0); PG8_MMA(0, 1, At, B1); PG8_BAR; PG8_SCHED;
;             PG8_LDA(At, 0, 1); PG8_STAGE(PG8_SB(0, 0), b2, voffB); PG8_STAGE(PG8_SB(0, 1), b2 + hstepB, voffB); PG8_STAGE(PG8_SA(0, 0), a2, voffA);
;             PG8_WAIT_V(8); PG8_WAIT_L(0); PG8_BAR; PG8_MMA(1, 0, At, B0); PG8_MMA(1, 1, At, B1); PG8_BAR; PG8_SCHED;
;             PG8_LDB(B0, 1, 0); PG8_LDB(B1, 1, 1); PG8_SCHED; PG8_LDA(At, 1, 0); PG8_STAGE(PG8_SA(0, 1), a2 + hstepA, voffA);
;             PG8_WAIT_V(8); PG8_WAIT_L(0); PG8_BAR; PG8_MMA(0, 0, At, B0); PG8_MMA(0, 1, At, B1); PG8_BAR; PG8_SCHED;
	v_mfma_f32_16x16x32_bf16 v[60:63], v[146:149], v[178:181], v[60:63]
	v_mfma_f32_16x16x32_bf16 v[56:59], v[154:157], v[178:181], v[56:59]
	v_mfma_f32_16x16x32_bf16 v[44:47], v[146:149], v[186:189], v[44:47]
	v_mfma_f32_16x16x32_bf16 v[40:43], v[154:157], v[186:189], v[40:43]
	v_mfma_f32_16x16x32_bf16 v[28:31], v[146:149], v[194:197], v[28:31]
	v_mfma_f32_16x16x32_bf16 v[24:27], v[154:157], v[194:197], v[24:27]
	v_mfma_f32_16x16x32_bf16 v[12:15], v[146:149], v[202:205], v[12:15]
	v_mfma_f32_16x16x32_bf16 v[8:11], v[154:157], v[202:205], v[8:11]
	v_mfma_f32_16x16x32_bf16 v[60:63], v[150:153], v[182:185], v[60:63]
	v_mfma_f32_16x16x32_bf16 v[56:59], v[158:161], v[182:185], v[56:59]
	v_mfma_f32_16x16x32_bf16 v[44:47], v[150:153], v[190:193], v[44:47]
	v_mfma_f32_16x16x32_bf16 v[40:43], v[158:161], v[190:193], v[40:43]
	v_mfma_f32_16x16x32_bf16 v[28:31], v[150:153], v[198:201], v[28:31]
	v_mfma_f32_16x16x32_bf16 v[24:27], v[158:161], v[198:201], v[24:27]
	v_mfma_f32_16x16x32_bf16 v[12:15], v[150:153], v[206:209], v[12:15]
	v_mfma_f32_16x16x32_bf16 v[8:11], v[158:161], v[206:209], v[8:11]
	v_mfma_f32_16x16x32_bf16 v[52:55], v[162:165], v[178:181], v[52:55]
	v_mfma_f32_16x16x32_bf16 v[48:51], v[170:173], v[178:181], v[48:51]
	v_mfma_f32_16x16x32_bf16 v[36:39], v[162:165], v[186:189], v[36:39]
	v_mfma_f32_16x16x32_bf16 v[32:35], v[170:173], v[186:189], v[32:35]
	v_mfma_f32_16x16x32_bf16 v[20:23], v[162:165], v[194:197], v[20:23]
	v_mfma_f32_16x16x32_bf16 v[16:19], v[170:173], v[194:197], v[16:19]
	v_mfma_f32_16x16x32_bf16 v[4:7], v[162:165], v[202:205], v[4:7]
	v_mfma_f32_16x16x32_bf16 v[0:3], v[170:173], v[202:205], v[0:3]
	v_mfma_f32_16x16x32_bf16 v[52:55], v[166:169], v[182:185], v[52:55]
	v_mfma_f32_16x16x32_bf16 v[48:51], v[174:177], v[182:185], v[48:51]
	v_mfma_f32_16x16x32_bf16 v[36:39], v[166:169], v[190:193], v[36:39]
	v_mfma_f32_16x16x32_bf16 v[32:35], v[174:177], v[190:193], v[32:35]
	v_mfma_f32_16x16x32_bf16 v[20:23], v[166:169], v[198:201], v[20:23]
	v_mfma_f32_16x16x32_bf16 v[16:19], v[174:177], v[198:201], v[16:19]
	v_mfma_f32_16x16x32_bf16 v[4:7], v[166:169], v[206:209], v[4:7]
	v_mfma_f32_16x16x32_bf16 v[0:3], v[174:177], v[206:209], v[0:3]
	s_barrier
	s_setprio 0
	ds_read_b128 v[146:149], v143
	ds_read_b128 v[150:153], v143 offset:1024
	ds_read_b128 v[154:157], v143 offset:2048
	ds_read_b128 v[158:161], v143 offset:3072
	ds_read_b128 v[162:165], v144
	ds_read_b128 v[166:169], v144 offset:1024
	ds_read_b128 v[170:173], v144 offset:2048
	ds_read_b128 v[174:177], v144 offset:3072
	ds_read_b128 v[178:181], v142 offset:32768
	ds_read_b128 v[182:185], v142 offset:33792
	ds_read_b128 v[186:189], v142 offset:34816
	ds_read_b128 v[190:193], v142 offset:35840
	ds_read_b128 v[194:197], v142 offset:36864
	ds_read_b128 v[198:201], v142 offset:37888
	ds_read_b128 v[202:205], v142 offset:38912
	ds_read_b128 v[206:209], v142 offset:39936
	s_add_u32 s62, s70, 0x80000
	s_addc_u32 s63, s71, 0
	s_mov_b32 s70, m0
	s_mov_b32 m0, s81
	s_nop 0
	global_load_lds_dwordx4 v134, s[62:63]
	s_mov_b32 m0, s70
	s_nop 0
	s_mov_b32 s70, m0
	s_mov_b32 m0, s82
	s_nop 0
	global_load_lds_dwordx4 v136, s[62:63]
	s_mov_b32 m0, s70
	s_waitcnt vmcnt(8)
	s_waitcnt lgkmcnt(0)
	s_setprio 1
	s_barrier
	v_mfma_f32_16x16x32_bf16 v[124:127], v[146:149], v[178:181], v[124:127]
	v_mfma_f32_16x16x32_bf16 v[120:123], v[154:157], v[178:181], v[120:123]
	v_mfma_f32_16x16x32_bf16 v[108:111], v[146:149], v[186:189], v[108:111]
	v_mfma_f32_16x16x32_bf16 v[104:107], v[154:157], v[186:189], v[104:107]
	v_mfma_f32_16x16x32_bf16 v[92:95], v[146:149], v[194:197], v[92:95]
	v_mfma_f32_16x16x32_bf16 v[88:91], v[154:157], v[194:197], v[88:91]
	v_mfma_f32_16x16x32_bf16 v[76:79], v[146:149], v[202:205], v[76:79]
	v_mfma_f32_16x16x32_bf16 v[72:75], v[154:157], v[202:205], v[72:75]
	v_mfma_f32_16x16x32_bf16 v[124:127], v[150:153], v[182:185], v[124:127]
	v_mfma_f32_16x16x32_bf16 v[120:123], v[158:161], v[182:185], v[120:123]
	v_mfma_f32_16x16x32_bf16 v[108:111], v[150:153], v[190:193], v[108:111]
	v_mfma_f32_16x16x32_bf16 v[104:107], v[158:161], v[190:193], v[104:107]
	v_mfma_f32_16x16x32_bf16 v[92:95], v[150:153], v[198:201], v[92:95]
	v_mfma_f32_16x16x32_bf16 v[88:91], v[158:161], v[198:201], v[88:91]
	v_mfma_f32_16x16x32_bf16 v[76:79], v[150:153], v[206:209], v[76:79]
	v_mfma_f32_16x16x32_bf16 v[72:75], v[158:161], v[206:209], v[72:75]
	v_mfma_f32_16x16x32_bf16 v[116:119], v[162:165], v[178:181], v[116:119]
	v_mfma_f32_16x16x32_bf16 v[112:115], v[170:173], v[178:181], v[112:115]
	v_mfma_f32_16x16x32_bf16 v[100:103], v[162:165], v[186:189], v[100:103]
	v_mfma_f32_16x16x32_bf16 v[96:99], v[170:173], v[186:189], v[96:99]
	v_mfma_f32_16x16x32_bf16 v[84:87], v[162:165], v[194:197], v[84:87]
	v_mfma_f32_16x16x32_bf16 v[80:83], v[170:173], v[194:197], v[80:83]
	v_mfma_f32_16x16x32_bf16 v[68:71], v[162:165], v[202:205], v[68:71]
	v_mfma_f32_16x16x32_bf16 v[64:67], v[170:173], v[202:205], v[64:67]
	v_mfma_f32_16x16x32_bf16 v[116:119], v[166:169], v[182:185], v[116:119]
	v_mfma_f32_16x16x32_bf16 v[112:115], v[174:177], v[182:185], v[112:115]
	v_mfma_f32_16x16x32_bf16 v[100:103], v[166:169], v[190:193], v[100:103]
	v_mfma_f32_16x16x32_bf16 v[96:99], v[174:177], v[190:193], v[96:99]
	v_mfma_f32_16x16x32_bf16 v[84:87], v[166:169], v[198:201], v[84:87]
	v_mfma_f32_16x16x32_bf16 v[80:83], v[174:177], v[198:201], v[80:83]
	v_mfma_f32_16x16x32_bf16 v[68:71], v[166:169], v[206:209], v[68:71]
	v_mfma_f32_16x16x32_bf16 v[64:67], v[174:177], v[206:209], v[64:67]
	s_barrier
; #define PG8_STAGE(bufoff, gbase, voff) do { _Pragma("unroll") for (int _i = 0; _i < 2; ++_i) { unsigned keep_; \
;         asm volatile("s_mov_b32 %0, m0\n\ts_mov_b32 m0, %3\n\ts_nop 0\n\tglobal_load_lds_dwordx4 %1, %2\n\ts_mov_b32 m0, %0" : "=&s"(keep_) : "v"((voff)[_i]), "s"((const char*)(gbase)), "s"(ldsbase + (unsigned)((bufoff) + _i * 8192)) : "memory"); } } while (0)
; #define PG8_WAIT_V(n) asm volatile("s_waitcnt vmcnt(" #n ")" ::: "memory")
; #define PG8_WAIT_L(n) asm volatile("s_waitcnt lgkmcnt(" #n ")" ::: "memory")
; #define PG8_BAR __builtin_amdgcn_s_barrier()
; #define PG8_SCHED __builtin_amdgcn_sched_barrier(0)
; template <class Epi, class Sched, bool ALIGN_EPI, bool FP8 = false>
; DI void gemm_phase(LAS unsigned char* lds, const Gemm g, const Sched& S, const Epi& E) {
;     ...
;             PG8_LDA(At, 1, 1); PG8_STAGE(PG8_SB(1, 0), b3, voffB); PG8_STAGE(PG8_SB(1, 1), b3 + hstepB, voffB); PG8_STAGE(PG8_SA(1, 0), a3, voffA);
;             PG8_WAIT_V(8); PG8_WAIT_L(0); PG8_BAR; PG8_MMA(1, 0, At, B0); PG8_MMA(1, 1, At, B1); PG8_BAR; PG8_SCHED;
;         }
;         if constexpr (ALIGN_EPI) { if (wr == 0) PG8_BAR; }
;         E(acc, cur, wr, wc, fr, fq);
	s_setprio 0
	ds_read_b128 v[178:181], v142 offset:49152
	ds_read_b128 v[182:185], v142 offset:50176
	ds_read_b128 v[186:189], v142 offset:51200
	ds_read_b128 v[190:193], v142 offset:52224
	ds_read_b128 v[194:197], v142 offset:53248
	ds_read_b128 v[198:201], v142 offset:54272
	ds_read_b128 v[202:205], v142 offset:55296
	ds_read_b128 v[206:209], v142 offset:56320
	s_add_u32 s62, s68, 0x80
	s_addc_u32 s63, s69, 0
	s_mov_b32 s70, m0
	s_mov_b32 m0, s83
	s_nop 0
	global_load_lds_dwordx4 v135, s[62:63]
	s_mov_b32 m0, s70
	s_nop 0
	s_mov_b32 s70, m0
	s_mov_b32 m0, s84
	s_nop 0
	global_load_lds_dwordx4 v137, s[62:63]
	s_mov_b32 m0, s70
	s_add_u32 s62, s68, 0x80080
	s_addc_u32 s63, s69, 0
	s_mov_b32 s68, m0
	s_mov_b32 m0, s87
	s_nop 0
	global_load_lds_dwordx4 v135, s[62:63]
	s_mov_b32 m0, s68
	s_nop 0
	s_mov_b32 s68, m0
	s_mov_b32 m0, s88
	s_nop 0
	global_load_lds_dwordx4 v137, s[62:63]
	s_mov_b32 m0, s68
	s_mov_b32 s62, m0
	s_mov_b32 m0, s85
	s_nop 0
	global_load_lds_dwordx4 v134, s[66:67]
	s_mov_b32 m0, s62
	s_nop 0
	s_mov_b32 s62, m0
	s_mov_b32 m0, s86
	s_nop 0
	global_load_lds_dwordx4 v136, s[66:67]
	s_mov_b32 m0, s62
	s_waitcnt vmcnt(8)
	s_waitcnt lgkmcnt(0)
	s_setprio 1
	s_barrier
	v_mfma_f32_16x16x32_bf16 v[60:63], v[146:149], v[178:181], v[60:63]
	v_mfma_f32_16x16x32_bf16 v[56:59], v[154:157], v[178:181], v[56:59]
	v_mfma_f32_16x16x32_bf16 v[44:47], v[146:149], v[186:189], v[44:47]
	v_mfma_f32_16x16x32_bf16 v[40:43], v[154:157], v[186:189], v[40:43]
	v_mfma_f32_16x16x32_bf16 v[28:31], v[146:149], v[194:197], v[28:31]
	v_mfma_f32_16x16x32_bf16 v[24:27], v[154:157], v[194:197], v[24:27]
	v_mfma_f32_16x16x32_bf16 v[12:15], v[146:149], v[202:205], v[12:15]
	v_mfma_f32_16x16x32_bf16 v[8:11], v[154:157], v[202:205], v[8:11]
	v_mfma_f32_16x16x32_bf16 v[60:63], v[150:153], v[182:185], v[60:63]
	v_mfma_f32_16x16x32_bf16 v[56:59], v[158:161], v[182:185], v[56:59]
	v_mfma_f32_16x16x32_bf16 v[44:47], v[150:153], v[190:193], v[44:47]
	v_mfma_f32_16x16x32_bf16 v[40:43], v[158:161], v[190:193], v[40:43]
	v_mfma_f32_16x16x32_bf16 v[28:31], v[150:153], v[198:201], v[28:31]
	v_mfma_f32_16x16x32_bf16 v[24:27], v[158:161], v[198:201], v[24:27]
	v_mfma_f32_16x16x32_bf16 v[12:15], v[150:153], v[206:209], v[12:15]
	v_mfma_f32_16x16x32_bf16 v[8:11], v[158:161], v[206:209], v[8:11]
	v_mfma_f32_16x16x32_bf16 v[52:55], v[162:165], v[178:181], v[52:55]
	v_mfma_f32_16x16x32_bf16 v[48:51], v[170:173], v[178:181], v[48:51]
	v_mfma_f32_16x16x32_bf16 v[36:39], v[162:165], v[186:189], v[36:39]
	v_mfma_f32_16x16x32_bf16 v[32:35], v[170:173], v[186:189], v[32:35]
	v_mfma_f32_16x16x32_bf16 v[20:23], v[162:165], v[194:197], v[20:23]
	v_mfma_f32_16x16x32_bf16 v[16:19], v[170:173], v[194:197], v[16:19]
	v_mfma_f32_16x16x32_bf16 v[4:7], v[162:165], v[202:205], v[4:7]
	v_mfma_f32_16x16x32_bf16 v[0:3], v[170:173], v[202:205], v[0:3]
	v_mfma_f32_16x16x32_bf16 v[52:55], v[166:169], v[182:185], v[52:55]
	v_mfma_f32_16x16x32_bf16 v[48:51], v[174:177], v[182:185], v[48:51]
	v_mfma_f32_16x16x32_bf16 v[36:39], v[166:169], v[190:193], v[36:39]
	v_mfma_f32_16x16x32_bf16 v[32:35], v[174:177], v[190:193], v[32:35]
	v_mfma_f32_16x16x32_bf16 v[20:23], v[166:169], v[198:201], v[20:23]
	v_mfma_f32_16x16x32_bf16 v[16:19], v[174:177], v[198:201], v[16:19]
	v_mfma_f32_16x16x32_bf16 v[4:7], v[166:169], v[206:209], v[4:7]
	v_mfma_f32_16x16x32_bf16 v[0:3], v[174:177], v[206:209], v[0:3]
	s_barrier
	s_setprio 0
	s_add_i32 vcc_lo, vcc_lo, 2
	s_add_u32 s96, s96, 0x100
	s_addc_u32 s97, s97, 0
	s_cmp_gt_u32 vcc_lo, 29
	s_mov_b64 s[62:63], s[64:65]
	s_cbranch_scc0 .LBB0_1710
	s_and_b64 vcc, exec, s[14:15]
	s_cbranch_vccz .LBB0_1713
	s_barrier
